# skip L2 writeback at group-local seams when all members share an XCC; K-loop end-of-compute barrier issued 2 MFMAs early with priority boost
# speedup vs baseline: 1.1757x; 1.1757x over previous
.LBB0_166:
	v_add_u32_e32 v142, s15, v144
	ds_read_b128 v[148:151], v142
	ds_read_b128 v[152:155], v142 offset:1024
	ds_read_b128 v[156:159], v142 offset:2048
	ds_read_b128 v[160:163], v142 offset:3072
	v_add_u32_e32 v142, s30, v144
	ds_read_b128 v[164:167], v142
	ds_read_b128 v[168:171], v142 offset:1024
	ds_read_b128 v[172:175], v142 offset:2048
	ds_read_b128 v[176:179], v142 offset:3072
	s_add_u32 s22, s18, 0xfff80080
	s_addc_u32 s23, s19, -1
	s_cmp_eq_u32 s53, 28
	s_cselect_b32 s25, s9, s23
	s_cselect_b32 s24, s49, s22
	s_cselect_b32 s23, s7, s52
	s_cselect_b32 s22, s50, s51
	v_lshl_add_u64 v[142:143], s[18:19], 0, v[140:141]
	s_add_i32 m0, s35, 0xc000
	ds_read_b128 v[180:183], v147
	ds_read_b128 v[184:187], v147 offset:1024
	ds_read_b128 v[188:191], v147 offset:2048
	ds_read_b128 v[192:195], v147 offset:3072
	ds_read_b128 v[196:199], v147 offset:4096
	ds_read_b128 v[206:209], v147 offset:5120
	ds_read_b128 v[210:213], v147 offset:6144
	ds_read_b128 v[214:217], v147 offset:7168
	global_load_lds_dwordx4 v[142:143], off
	v_lshl_add_u64 v[142:143], s[18:19], 0, v[138:139]
	s_add_i32 m0, s35, 0xe000
	s_nop 0
	global_load_lds_dwordx4 v[142:143], off
	s_waitcnt vmcnt(8)
	s_waitcnt lgkmcnt(0)
	s_barrier
	s_setprio 1
	s_waitcnt lgkmcnt(0)
	v_mfma_f32_16x16x32_bf16 v[130:133], v[148:151], v[180:183], v[130:133]
	v_mfma_f32_16x16x32_bf16 v[122:125], v[156:159], v[180:183], v[122:125]
	v_mfma_f32_16x16x32_bf16 v[114:117], v[148:151], v[188:191], v[114:117]
	v_mfma_f32_16x16x32_bf16 v[106:109], v[156:159], v[188:191], v[106:109]
	v_mfma_f32_16x16x32_bf16 v[98:101], v[148:151], v[196:199], v[98:101]
	v_mfma_f32_16x16x32_bf16 v[90:93], v[156:159], v[196:199], v[90:93]
	v_mfma_f32_16x16x32_bf16 v[82:85], v[148:151], v[210:213], v[82:85]
	v_mfma_f32_16x16x32_bf16 v[74:77], v[156:159], v[210:213], v[74:77]
	v_mfma_f32_16x16x32_bf16 v[130:133], v[152:155], v[184:187], v[130:133]
	v_mfma_f32_16x16x32_bf16 v[122:125], v[160:163], v[184:187], v[122:125]
	v_mfma_f32_16x16x32_bf16 v[114:117], v[152:155], v[192:195], v[114:117]
	v_mfma_f32_16x16x32_bf16 v[106:109], v[160:163], v[192:195], v[106:109]
	v_mfma_f32_16x16x32_bf16 v[98:101], v[152:155], v[206:209], v[98:101]
	v_mfma_f32_16x16x32_bf16 v[90:93], v[160:163], v[206:209], v[90:93]
	v_mfma_f32_16x16x32_bf16 v[82:85], v[152:155], v[214:217], v[82:85]
	v_mfma_f32_16x16x32_bf16 v[74:77], v[160:163], v[214:217], v[74:77]
	s_setprio 0
	s_setprio 1
	v_mfma_f32_16x16x32_bf16 v[126:129], v[164:167], v[180:183], v[126:129]
	v_mfma_f32_16x16x32_bf16 v[118:121], v[172:175], v[180:183], v[118:121]
	v_mfma_f32_16x16x32_bf16 v[110:113], v[164:167], v[188:191], v[110:113]
	v_mfma_f32_16x16x32_bf16 v[102:105], v[172:175], v[188:191], v[102:105]
	v_mfma_f32_16x16x32_bf16 v[94:97], v[164:167], v[196:199], v[94:97]
	v_mfma_f32_16x16x32_bf16 v[86:89], v[172:175], v[196:199], v[86:89]
	v_mfma_f32_16x16x32_bf16 v[78:81], v[164:167], v[210:213], v[78:81]
	v_mfma_f32_16x16x32_bf16 v[70:73], v[172:175], v[210:213], v[70:73]
	v_mfma_f32_16x16x32_bf16 v[126:129], v[168:171], v[184:187], v[126:129]
	v_mfma_f32_16x16x32_bf16 v[118:121], v[176:179], v[184:187], v[118:121]
	v_mfma_f32_16x16x32_bf16 v[110:113], v[168:171], v[192:195], v[110:113]
	v_mfma_f32_16x16x32_bf16 v[102:105], v[176:179], v[192:195], v[102:105]
	v_mfma_f32_16x16x32_bf16 v[94:97], v[168:171], v[206:209], v[94:97]
	v_mfma_f32_16x16x32_bf16 v[86:89], v[176:179], v[206:209], v[86:89]
	s_setprio 2
	s_barrier
	v_mfma_f32_16x16x32_bf16 v[78:81], v[168:171], v[214:217], v[78:81]
	v_mfma_f32_16x16x32_bf16 v[70:73], v[176:179], v[214:217], v[70:73]
	s_setprio 0
	s_mov_b32 m0, s20
	v_lshl_add_u64 v[142:143], s[22:23], 0, v[0:1]
	s_add_u32 s54, s22, 0x80000
	ds_read_b128 v[180:183], v147 offset:16384
	ds_read_b128 v[184:187], v147 offset:17408
	ds_read_b128 v[188:191], v147 offset:18432
	ds_read_b128 v[192:195], v147 offset:19456
	ds_read_b128 v[196:199], v147 offset:20480
	ds_read_b128 v[206:209], v147 offset:21504
	ds_read_b128 v[210:213], v147 offset:22528
	ds_read_b128 v[214:217], v147 offset:23552
	global_load_lds_dwordx4 v[142:143], off
	v_lshl_add_u64 v[200:201], s[22:23], 0, v[2:3]
	s_mov_b32 m0, s26
	s_addc_u32 s55, s23, 0
	global_load_lds_dwordx4 v[200:201], off
	v_lshl_add_u64 v[218:219], s[54:55], 0, v[0:1]
	s_mov_b32 m0, s31
	v_lshl_add_u64 v[220:221], s[24:25], 0, v[134:135]
	global_load_lds_dwordx4 v[218:219], off
	v_lshl_add_u64 v[218:219], s[54:55], 0, v[2:3]
	s_mov_b32 m0, s34
	s_nop 0
	global_load_lds_dwordx4 v[218:219], off
	v_lshl_add_u64 v[218:219], s[24:25], 0, v[136:137]
	s_mov_b32 m0, s35
	s_nop 0
	global_load_lds_dwordx4 v[218:219], off
	s_mov_b32 m0, s36
	s_nop 0
	global_load_lds_dwordx4 v[220:221], off
	s_waitcnt vmcnt(8)
	s_waitcnt lgkmcnt(0)
	s_barrier
	s_setprio 1
	s_waitcnt lgkmcnt(0)
	v_mfma_f32_16x16x32_bf16 v[66:69], v[148:151], v[180:183], v[66:69]
	v_mfma_f32_16x16x32_bf16 v[58:61], v[156:159], v[180:183], v[58:61]
	v_mfma_f32_16x16x32_bf16 v[50:53], v[148:151], v[188:191], v[50:53]
	v_mfma_f32_16x16x32_bf16 v[42:45], v[156:159], v[188:191], v[42:45]
	v_mfma_f32_16x16x32_bf16 v[34:37], v[148:151], v[196:199], v[34:37]
	v_mfma_f32_16x16x32_bf16 v[26:29], v[156:159], v[196:199], v[26:29]
	v_mfma_f32_16x16x32_bf16 v[18:21], v[148:151], v[210:213], v[18:21]
	v_mfma_f32_16x16x32_bf16 v[10:13], v[156:159], v[210:213], v[10:13]
	v_mfma_f32_16x16x32_bf16 v[66:69], v[152:155], v[184:187], v[66:69]
	v_mfma_f32_16x16x32_bf16 v[58:61], v[160:163], v[184:187], v[58:61]
	v_mfma_f32_16x16x32_bf16 v[50:53], v[152:155], v[192:195], v[50:53]
	v_mfma_f32_16x16x32_bf16 v[42:45], v[160:163], v[192:195], v[42:45]
	v_mfma_f32_16x16x32_bf16 v[34:37], v[152:155], v[206:209], v[34:37]
	v_mfma_f32_16x16x32_bf16 v[26:29], v[160:163], v[206:209], v[26:29]
	v_mfma_f32_16x16x32_bf16 v[18:21], v[152:155], v[214:217], v[18:21]
	v_mfma_f32_16x16x32_bf16 v[10:13], v[160:163], v[214:217], v[10:13]
	s_setprio 0
	s_setprio 1
	v_mfma_f32_16x16x32_bf16 v[62:65], v[164:167], v[180:183], v[62:65]
	v_mfma_f32_16x16x32_bf16 v[54:57], v[172:175], v[180:183], v[54:57]
	v_mfma_f32_16x16x32_bf16 v[46:49], v[164:167], v[188:191], v[46:49]
	v_mfma_f32_16x16x32_bf16 v[38:41], v[172:175], v[188:191], v[38:41]
	v_mfma_f32_16x16x32_bf16 v[30:33], v[164:167], v[196:199], v[30:33]
	v_mfma_f32_16x16x32_bf16 v[22:25], v[172:175], v[196:199], v[22:25]
	v_mfma_f32_16x16x32_bf16 v[14:17], v[164:167], v[210:213], v[14:17]
	v_mfma_f32_16x16x32_bf16 v[6:9], v[172:175], v[210:213], v[6:9]
	v_mfma_f32_16x16x32_bf16 v[62:65], v[168:171], v[184:187], v[62:65]
	v_mfma_f32_16x16x32_bf16 v[54:57], v[176:179], v[184:187], v[54:57]
	v_mfma_f32_16x16x32_bf16 v[46:49], v[168:171], v[192:195], v[46:49]
	v_mfma_f32_16x16x32_bf16 v[38:41], v[176:179], v[192:195], v[38:41]
	v_mfma_f32_16x16x32_bf16 v[30:33], v[168:171], v[206:209], v[30:33]
	v_mfma_f32_16x16x32_bf16 v[22:25], v[176:179], v[206:209], v[22:25]
	s_setprio 2
	s_barrier
	v_mfma_f32_16x16x32_bf16 v[14:17], v[168:171], v[214:217], v[14:17]
	v_mfma_f32_16x16x32_bf16 v[6:9], v[176:179], v[214:217], v[6:9]
	s_setprio 0
	v_add_u32_e32 v160, s39, v144
	v_add_u32_e32 v176, s44, v144
	ds_read_b128 v[148:151], v160
	ds_read_b128 v[152:155], v160 offset:1024
	ds_read_b128 v[156:159], v160 offset:2048
	ds_read_b128 v[160:163], v160 offset:3072
	ds_read_b128 v[164:167], v176
	ds_read_b128 v[168:171], v176 offset:1024
	ds_read_b128 v[172:175], v176 offset:2048
	ds_read_b128 v[176:179], v176 offset:3072
	s_add_u32 s24, s24, 0x80000
	s_addc_u32 s25, s25, 0
	s_mov_b32 m0, s37
	v_lshl_add_u64 v[222:223], s[24:25], 0, v[136:137]
	ds_read_b128 v[180:183], v147 offset:32768
	ds_read_b128 v[184:187], v147 offset:33792
	ds_read_b128 v[188:191], v147 offset:34816
	ds_read_b128 v[192:195], v147 offset:35840
	ds_read_b128 v[196:199], v147 offset:36864
	ds_read_b128 v[206:209], v147 offset:37888
	ds_read_b128 v[210:213], v147 offset:38912
	ds_read_b128 v[214:217], v147 offset:39936
	global_load_lds_dwordx4 v[222:223], off
	v_lshl_add_u64 v[222:223], s[24:25], 0, v[134:135]
	s_mov_b32 m0, s38
	s_nop 0
	global_load_lds_dwordx4 v[222:223], off
	s_waitcnt vmcnt(8)
	s_waitcnt lgkmcnt(0)
	s_barrier
	s_setprio 1
	s_waitcnt lgkmcnt(0)
	v_mfma_f32_16x16x32_bf16 v[130:133], v[148:151], v[180:183], v[130:133]
	v_mfma_f32_16x16x32_bf16 v[122:125], v[156:159], v[180:183], v[122:125]
	v_mfma_f32_16x16x32_bf16 v[114:117], v[148:151], v[188:191], v[114:117]
	v_mfma_f32_16x16x32_bf16 v[106:109], v[156:159], v[188:191], v[106:109]
	v_mfma_f32_16x16x32_bf16 v[98:101], v[148:151], v[196:199], v[98:101]
	v_mfma_f32_16x16x32_bf16 v[90:93], v[156:159], v[196:199], v[90:93]
	v_mfma_f32_16x16x32_bf16 v[82:85], v[148:151], v[210:213], v[82:85]
	v_mfma_f32_16x16x32_bf16 v[74:77], v[156:159], v[210:213], v[74:77]
	v_mfma_f32_16x16x32_bf16 v[130:133], v[152:155], v[184:187], v[130:133]
	v_mfma_f32_16x16x32_bf16 v[122:125], v[160:163], v[184:187], v[122:125]
	v_mfma_f32_16x16x32_bf16 v[114:117], v[152:155], v[192:195], v[114:117]
	v_mfma_f32_16x16x32_bf16 v[106:109], v[160:163], v[192:195], v[106:109]
	v_mfma_f32_16x16x32_bf16 v[98:101], v[152:155], v[206:209], v[98:101]
	v_mfma_f32_16x16x32_bf16 v[90:93], v[160:163], v[206:209], v[90:93]
	v_mfma_f32_16x16x32_bf16 v[82:85], v[152:155], v[214:217], v[82:85]
	v_mfma_f32_16x16x32_bf16 v[74:77], v[160:163], v[214:217], v[74:77]
	s_setprio 0
	s_setprio 1
	v_mfma_f32_16x16x32_bf16 v[126:129], v[164:167], v[180:183], v[126:129]
	v_mfma_f32_16x16x32_bf16 v[118:121], v[172:175], v[180:183], v[118:121]
	v_mfma_f32_16x16x32_bf16 v[110:113], v[164:167], v[188:191], v[110:113]
	v_mfma_f32_16x16x32_bf16 v[102:105], v[172:175], v[188:191], v[102:105]
	v_mfma_f32_16x16x32_bf16 v[94:97], v[164:167], v[196:199], v[94:97]
	v_mfma_f32_16x16x32_bf16 v[86:89], v[172:175], v[196:199], v[86:89]
	v_mfma_f32_16x16x32_bf16 v[78:81], v[164:167], v[210:213], v[78:81]
	v_mfma_f32_16x16x32_bf16 v[70:73], v[172:175], v[210:213], v[70:73]
	v_mfma_f32_16x16x32_bf16 v[126:129], v[168:171], v[184:187], v[126:129]
	v_mfma_f32_16x16x32_bf16 v[118:121], v[176:179], v[184:187], v[118:121]
	v_mfma_f32_16x16x32_bf16 v[110:113], v[168:171], v[192:195], v[110:113]
	v_mfma_f32_16x16x32_bf16 v[102:105], v[176:179], v[192:195], v[102:105]
	v_mfma_f32_16x16x32_bf16 v[94:97], v[168:171], v[206:209], v[94:97]
	v_mfma_f32_16x16x32_bf16 v[86:89], v[176:179], v[206:209], v[86:89]
	s_setprio 2
	s_barrier
	v_mfma_f32_16x16x32_bf16 v[78:81], v[168:171], v[214:217], v[78:81]
	v_mfma_f32_16x16x32_bf16 v[70:73], v[176:179], v[214:217], v[70:73]
	s_setprio 0
	s_mov_b32 m0, s40
	v_lshl_add_u64 v[142:143], v[142:143], 0, s[28:29]
	s_add_u32 s22, s22, 0x80080
	ds_read_b128 v[180:183], v147 offset:49152
	ds_read_b128 v[184:187], v147 offset:50176
	ds_read_b128 v[188:191], v147 offset:51200
	ds_read_b128 v[192:195], v147 offset:52224
	ds_read_b128 v[196:199], v147 offset:53248
	ds_read_b128 v[206:209], v147 offset:54272
	ds_read_b128 v[210:213], v147 offset:55296
	ds_read_b128 v[214:217], v147 offset:56320
	global_load_lds_dwordx4 v[142:143], off
	v_lshl_add_u64 v[142:143], v[200:201], 0, s[28:29]
	s_mov_b32 m0, s41
	s_addc_u32 s23, s23, 0
	global_load_lds_dwordx4 v[142:143], off
	v_lshl_add_u64 v[142:143], s[22:23], 0, v[0:1]
	s_mov_b32 m0, s45
	s_nop 0
	global_load_lds_dwordx4 v[142:143], off
	v_lshl_add_u64 v[142:143], s[22:23], 0, v[2:3]
	s_mov_b32 m0, s46
	s_nop 0
	global_load_lds_dwordx4 v[142:143], off
	v_lshl_add_u64 v[142:143], v[218:219], 0, s[28:29]
	s_mov_b32 m0, s42
	s_nop 0
	global_load_lds_dwordx4 v[142:143], off
	v_lshl_add_u64 v[142:143], v[220:221], 0, s[28:29]
	s_mov_b32 m0, s43
	s_nop 0
	global_load_lds_dwordx4 v[142:143], off
	s_waitcnt vmcnt(8)
	s_waitcnt lgkmcnt(0)
	s_barrier
	s_setprio 1
	s_waitcnt lgkmcnt(0)
	v_mfma_f32_16x16x32_bf16 v[66:69], v[148:151], v[180:183], v[66:69]
	v_mfma_f32_16x16x32_bf16 v[58:61], v[156:159], v[180:183], v[58:61]
	v_mfma_f32_16x16x32_bf16 v[50:53], v[148:151], v[188:191], v[50:53]
	v_mfma_f32_16x16x32_bf16 v[42:45], v[156:159], v[188:191], v[42:45]
	v_mfma_f32_16x16x32_bf16 v[34:37], v[148:151], v[196:199], v[34:37]
	v_mfma_f32_16x16x32_bf16 v[26:29], v[156:159], v[196:199], v[26:29]
	v_mfma_f32_16x16x32_bf16 v[18:21], v[148:151], v[210:213], v[18:21]
	v_mfma_f32_16x16x32_bf16 v[10:13], v[156:159], v[210:213], v[10:13]
	v_mfma_f32_16x16x32_bf16 v[66:69], v[152:155], v[184:187], v[66:69]
	v_mfma_f32_16x16x32_bf16 v[58:61], v[160:163], v[184:187], v[58:61]
	v_mfma_f32_16x16x32_bf16 v[50:53], v[152:155], v[192:195], v[50:53]
	v_mfma_f32_16x16x32_bf16 v[42:45], v[160:163], v[192:195], v[42:45]
	v_mfma_f32_16x16x32_bf16 v[34:37], v[152:155], v[206:209], v[34:37]
	v_mfma_f32_16x16x32_bf16 v[26:29], v[160:163], v[206:209], v[26:29]
	v_mfma_f32_16x16x32_bf16 v[18:21], v[152:155], v[214:217], v[18:21]
	v_mfma_f32_16x16x32_bf16 v[10:13], v[160:163], v[214:217], v[10:13]
	s_setprio 0
	s_setprio 1
	v_mfma_f32_16x16x32_bf16 v[62:65], v[164:167], v[180:183], v[62:65]
	v_mfma_f32_16x16x32_bf16 v[54:57], v[172:175], v[180:183], v[54:57]
	v_mfma_f32_16x16x32_bf16 v[46:49], v[164:167], v[188:191], v[46:49]
	v_mfma_f32_16x16x32_bf16 v[38:41], v[172:175], v[188:191], v[38:41]
	v_mfma_f32_16x16x32_bf16 v[30:33], v[164:167], v[196:199], v[30:33]
	v_mfma_f32_16x16x32_bf16 v[22:25], v[172:175], v[196:199], v[22:25]
	v_mfma_f32_16x16x32_bf16 v[14:17], v[164:167], v[210:213], v[14:17]
	v_mfma_f32_16x16x32_bf16 v[6:9], v[172:175], v[210:213], v[6:9]
	v_mfma_f32_16x16x32_bf16 v[62:65], v[168:171], v[184:187], v[62:65]
	v_mfma_f32_16x16x32_bf16 v[54:57], v[176:179], v[184:187], v[54:57]
	v_mfma_f32_16x16x32_bf16 v[46:49], v[168:171], v[192:195], v[46:49]
	v_mfma_f32_16x16x32_bf16 v[38:41], v[176:179], v[192:195], v[38:41]
	v_mfma_f32_16x16x32_bf16 v[30:33], v[168:171], v[206:209], v[30:33]
	v_mfma_f32_16x16x32_bf16 v[22:25], v[176:179], v[206:209], v[22:25]
	s_setprio 2
	s_barrier
	v_mfma_f32_16x16x32_bf16 v[14:17], v[168:171], v[214:217], v[14:17]
	v_mfma_f32_16x16x32_bf16 v[6:9], v[176:179], v[214:217], v[6:9]
	s_setprio 0
	s_add_i32 s53, s53, 2
	s_add_u32 s51, s51, 0x100
	s_addc_u32 s52, s52, 0
	s_add_u32 s18, s18, 0x100
	s_addc_u32 s19, s19, 0
	s_cmp_gt_u32 s53, 29
	s_cbranch_scc0 .LBB0_166
	s_and_b64 vcc, exec, s[4:5]
	s_cbranch_vccz .LBB0_169
	s_barrier

.LBB0_202:
	s_andn2_saveexec_b64 s[4:5], s[4:5]
	s_cbranch_execz .LBB0_219
	v_cmp_lt_u32_e32 vcc, 1, v0
	s_and_saveexec_b64 s[4:5], vcc
	s_cbranch_execz .LBB0_218
	buffer_wbl2 sc1
	s_waitcnt vmcnt(0)
	v_mov_b32_e32 v2, s2
	v_add_co_u32_e32 v2, vcc, 0x3000, v2
	v_mov_b32_e32 v3, s3
	s_nop 0
	v_addc_co_u32_e32 v3, vcc, 0, v3, vcc
	v_mov_b32_e32 v5, 1
	flat_atomic_add v2, v[2:3], v5 offset:1024 sc0
	v_cvt_f32_u32_e32 v3, v0
	v_sub_u32_e32 v5, 0, v0
	s_mov_b64 s[10:11], -1
	v_rcp_iflag_f32_e32 v3, v3
	s_nop 0
	v_mul_f32_e32 v3, 0x4f7ffffe, v3
	v_cvt_u32_f32_e32 v3, v3
	v_mul_lo_u32 v5, v5, v3
	v_mul_hi_u32 v5, v3, v5
	v_add_u32_e32 v3, v3, v5
	s_waitcnt vmcnt(0) lgkmcnt(0)
	v_mul_hi_u32 v3, v2, v3
	v_mul_lo_u32 v5, v3, v0
	v_sub_u32_e32 v5, v2, v5
	v_cmp_ge_u32_e32 vcc, v5, v0
	v_add_u32_e32 v6, 1, v3
	s_nop 0
	v_cndmask_b32_e32 v3, v3, v6, vcc
	v_sub_u32_e32 v6, v5, v0
	v_cndmask_b32_e32 v5, v5, v6, vcc
	v_cmp_ge_u32_e32 vcc, v5, v0
	v_add_u32_e32 v5, 1, v3
	v_add_u32_e32 v6, 1, v2
	v_cndmask_b32_e32 v5, v3, v5, vcc
	v_mad_u64_u32 v[2:3], s[6:7], v0, v5, v[0:1]
	s_add_u32 s6, s2, 0x3500
	s_addc_u32 s7, s3, 0
	v_cmp_ne_u32_e32 vcc, v6, v2
	v_mov_b64_e32 v[2:3], s[6:7]
	s_and_saveexec_b64 s[8:9], vcc
	s_cbranch_execz .LBB0_216
	v_mov_b64_e32 v[2:3], s[6:7]
	flat_load_dword v0, v[2:3] sc1
	s_mov_b64 s[14:15], 0
	s_waitcnt vmcnt(0) lgkmcnt(0)
	v_cmp_eq_u32_e32 vcc, v0, v5
	s_and_saveexec_b64 s[12:13], vcc
	s_cbranch_execz .LBB0_215
	s_add_u32 s10, s2, 0x200
	s_addc_u32 s11, s3, 0
	s_mov_b32 s31, 1
	s_mov_b64 s[2:3], 0
	s_branch .LBB0_208

.LBB0_246:
	v_add_u32_e32 v146, s19, v182
	v_add_u32_e32 v170, s23, v182
	ds_read_b128 v[134:137], v146
	ds_read_b128 v[138:141], v146 offset:1024
	ds_read_b128 v[142:145], v146 offset:2048
	ds_read_b128 v[146:149], v146 offset:3072
	ds_read_b128 v[150:153], v170
	ds_read_b128 v[154:157], v170 offset:1024
	ds_read_b128 v[158:161], v170 offset:2048
	ds_read_b128 v[170:173], v170 offset:3072
	s_add_u32 s10, s8, 0x100
	s_addc_u32 s11, s9, 0
	s_cmpk_eq_i32 s56, 0x52
	s_cselect_b32 s15, s3, s11
	s_cselect_b32 s14, s2, s10
	s_cselect_b32 s13, s7, s55
	s_cselect_b32 s12, s6, s54
	v_lshl_add_u64 v[214:215], s[8:9], 0, v[168:169]
	s_add_i32 m0, s30, 0xc000
	ds_read_b128 v[174:177], v184
	ds_read_b128 v[178:181], v184 offset:1024
	ds_read_b128 v[186:189], v184 offset:2048
	ds_read_b128 v[190:193], v184 offset:3072
	ds_read_b128 v[194:197], v184 offset:4096
	ds_read_b128 v[198:201], v184 offset:5120
	ds_read_b128 v[206:209], v184 offset:6144
	ds_read_b128 v[210:213], v184 offset:7168
	global_load_lds_dwordx4 v[214:215], off
	v_lshl_add_u64 v[214:215], s[8:9], 0, v[166:167]
	s_add_i32 m0, s30, 0xe000
	s_nop 0
	global_load_lds_dwordx4 v[214:215], off
	s_waitcnt vmcnt(8)
	s_waitcnt lgkmcnt(0)
	s_barrier
	s_setprio 1
	s_waitcnt lgkmcnt(0)
	v_mfma_f32_16x16x32_bf16 v[130:133], v[134:137], v[174:177], v[130:133]
	v_mfma_f32_16x16x32_bf16 v[126:129], v[142:145], v[174:177], v[126:129]
	v_mfma_f32_16x16x32_bf16 v[114:117], v[134:137], v[186:189], v[114:117]
	v_mfma_f32_16x16x32_bf16 v[110:113], v[142:145], v[186:189], v[110:113]
	v_mfma_f32_16x16x32_bf16 v[98:101], v[134:137], v[194:197], v[98:101]
	v_mfma_f32_16x16x32_bf16 v[94:97], v[142:145], v[194:197], v[94:97]
	v_mfma_f32_16x16x32_bf16 v[82:85], v[134:137], v[206:209], v[82:85]
	v_mfma_f32_16x16x32_bf16 v[78:81], v[142:145], v[206:209], v[78:81]
	v_mfma_f32_16x16x32_bf16 v[130:133], v[138:141], v[178:181], v[130:133]
	v_mfma_f32_16x16x32_bf16 v[126:129], v[146:149], v[178:181], v[126:129]
	v_mfma_f32_16x16x32_bf16 v[114:117], v[138:141], v[190:193], v[114:117]
	v_mfma_f32_16x16x32_bf16 v[110:113], v[146:149], v[190:193], v[110:113]
	v_mfma_f32_16x16x32_bf16 v[98:101], v[138:141], v[198:201], v[98:101]
	v_mfma_f32_16x16x32_bf16 v[94:97], v[146:149], v[198:201], v[94:97]
	v_mfma_f32_16x16x32_bf16 v[82:85], v[138:141], v[210:213], v[82:85]
	v_mfma_f32_16x16x32_bf16 v[78:81], v[146:149], v[210:213], v[78:81]
	s_setprio 0
	s_setprio 1
	v_mfma_f32_16x16x32_bf16 v[122:125], v[150:153], v[174:177], v[122:125]
	v_mfma_f32_16x16x32_bf16 v[118:121], v[158:161], v[174:177], v[118:121]
	v_mfma_f32_16x16x32_bf16 v[106:109], v[150:153], v[186:189], v[106:109]
	v_mfma_f32_16x16x32_bf16 v[102:105], v[158:161], v[186:189], v[102:105]
	v_mfma_f32_16x16x32_bf16 v[90:93], v[150:153], v[194:197], v[90:93]
	v_mfma_f32_16x16x32_bf16 v[86:89], v[158:161], v[194:197], v[86:89]
	v_mfma_f32_16x16x32_bf16 v[74:77], v[150:153], v[206:209], v[74:77]
	v_mfma_f32_16x16x32_bf16 v[70:73], v[158:161], v[206:209], v[70:73]
	v_mfma_f32_16x16x32_bf16 v[122:125], v[154:157], v[178:181], v[122:125]
	v_mfma_f32_16x16x32_bf16 v[118:121], v[170:173], v[178:181], v[118:121]
	v_mfma_f32_16x16x32_bf16 v[106:109], v[154:157], v[190:193], v[106:109]
	v_mfma_f32_16x16x32_bf16 v[102:105], v[170:173], v[190:193], v[102:105]
	v_mfma_f32_16x16x32_bf16 v[90:93], v[154:157], v[198:201], v[90:93]
	v_mfma_f32_16x16x32_bf16 v[86:89], v[170:173], v[198:201], v[86:89]
	s_setprio 2
	s_barrier
	v_mfma_f32_16x16x32_bf16 v[74:77], v[154:157], v[210:213], v[74:77]
	v_mfma_f32_16x16x32_bf16 v[70:73], v[170:173], v[210:213], v[70:73]
	s_setprio 0
	s_mov_b32 m0, s20
	v_lshl_add_u64 v[214:215], s[12:13], 0, v[0:1]
	s_add_u32 s8, s12, 0x158000
	ds_read_b128 v[174:177], v184 offset:16384
	ds_read_b128 v[178:181], v184 offset:17408
	ds_read_b128 v[186:189], v184 offset:18432
	ds_read_b128 v[190:193], v184 offset:19456
	ds_read_b128 v[194:197], v184 offset:20480
	ds_read_b128 v[198:201], v184 offset:21504
	ds_read_b128 v[206:209], v184 offset:22528
	ds_read_b128 v[210:213], v184 offset:23552
	global_load_lds_dwordx4 v[214:215], off
	v_lshl_add_u64 v[216:217], s[12:13], 0, v[164:165]
	s_mov_b32 m0, s22
	s_addc_u32 s9, s13, 0
	global_load_lds_dwordx4 v[216:217], off
	v_lshl_add_u64 v[218:219], s[8:9], 0, v[0:1]
	s_mov_b32 m0, s24
	v_lshl_add_u64 v[220:221], s[14:15], 0, v[162:163]
	global_load_lds_dwordx4 v[218:219], off
	v_lshl_add_u64 v[218:219], s[8:9], 0, v[164:165]
	s_mov_b32 m0, s25
	s_nop 0
	global_load_lds_dwordx4 v[218:219], off
	v_lshl_add_u64 v[218:219], s[14:15], 0, v[2:3]
	s_mov_b32 m0, s30
	s_nop 0
	global_load_lds_dwordx4 v[218:219], off
	s_mov_b32 m0, s31
	s_nop 0
	global_load_lds_dwordx4 v[220:221], off
	s_waitcnt vmcnt(8)
	s_waitcnt lgkmcnt(0)
	s_barrier
	s_setprio 1
	s_waitcnt lgkmcnt(0)
	v_mfma_f32_16x16x32_bf16 v[66:69], v[134:137], v[174:177], v[66:69]
	v_mfma_f32_16x16x32_bf16 v[62:65], v[142:145], v[174:177], v[62:65]
	v_mfma_f32_16x16x32_bf16 v[50:53], v[134:137], v[186:189], v[50:53]
	v_mfma_f32_16x16x32_bf16 v[46:49], v[142:145], v[186:189], v[46:49]
	v_mfma_f32_16x16x32_bf16 v[34:37], v[134:137], v[194:197], v[34:37]
	v_mfma_f32_16x16x32_bf16 v[30:33], v[142:145], v[194:197], v[30:33]
	v_mfma_f32_16x16x32_bf16 v[18:21], v[134:137], v[206:209], v[18:21]
	v_mfma_f32_16x16x32_bf16 v[14:17], v[142:145], v[206:209], v[14:17]
	v_mfma_f32_16x16x32_bf16 v[66:69], v[138:141], v[178:181], v[66:69]
	v_mfma_f32_16x16x32_bf16 v[62:65], v[146:149], v[178:181], v[62:65]
	v_mfma_f32_16x16x32_bf16 v[50:53], v[138:141], v[190:193], v[50:53]
	v_mfma_f32_16x16x32_bf16 v[46:49], v[146:149], v[190:193], v[46:49]
	v_mfma_f32_16x16x32_bf16 v[34:37], v[138:141], v[198:201], v[34:37]
	v_mfma_f32_16x16x32_bf16 v[30:33], v[146:149], v[198:201], v[30:33]
	v_mfma_f32_16x16x32_bf16 v[18:21], v[138:141], v[210:213], v[18:21]
	v_mfma_f32_16x16x32_bf16 v[14:17], v[146:149], v[210:213], v[14:17]
	s_setprio 0
	s_setprio 1
	v_mfma_f32_16x16x32_bf16 v[58:61], v[150:153], v[174:177], v[58:61]
	v_mfma_f32_16x16x32_bf16 v[54:57], v[158:161], v[174:177], v[54:57]
	v_mfma_f32_16x16x32_bf16 v[42:45], v[150:153], v[186:189], v[42:45]
	v_mfma_f32_16x16x32_bf16 v[38:41], v[158:161], v[186:189], v[38:41]
	v_mfma_f32_16x16x32_bf16 v[26:29], v[150:153], v[194:197], v[26:29]
	v_mfma_f32_16x16x32_bf16 v[22:25], v[158:161], v[194:197], v[22:25]
	v_mfma_f32_16x16x32_bf16 v[10:13], v[150:153], v[206:209], v[10:13]
	v_mfma_f32_16x16x32_bf16 v[6:9], v[158:161], v[206:209], v[6:9]
	v_mfma_f32_16x16x32_bf16 v[58:61], v[154:157], v[178:181], v[58:61]
	v_mfma_f32_16x16x32_bf16 v[54:57], v[170:173], v[178:181], v[54:57]
	v_mfma_f32_16x16x32_bf16 v[42:45], v[154:157], v[190:193], v[42:45]
	v_mfma_f32_16x16x32_bf16 v[38:41], v[170:173], v[190:193], v[38:41]
	v_mfma_f32_16x16x32_bf16 v[26:29], v[154:157], v[198:201], v[26:29]
	v_mfma_f32_16x16x32_bf16 v[22:25], v[170:173], v[198:201], v[22:25]
	s_setprio 2
	s_barrier
	v_mfma_f32_16x16x32_bf16 v[10:13], v[154:157], v[210:213], v[10:13]
	v_mfma_f32_16x16x32_bf16 v[6:9], v[170:173], v[210:213], v[6:9]
	s_setprio 0
	v_add_u32_e32 v146, s41, v182
	v_add_u32_e32 v170, s46, v182
	ds_read_b128 v[134:137], v146
	ds_read_b128 v[138:141], v146 offset:1024
	ds_read_b128 v[142:145], v146 offset:2048
	ds_read_b128 v[146:149], v146 offset:3072
	ds_read_b128 v[150:153], v170
	ds_read_b128 v[154:157], v170 offset:1024
	ds_read_b128 v[158:161], v170 offset:2048
	ds_read_b128 v[170:173], v170 offset:3072
	s_add_u32 s8, s14, 0x280000
	s_addc_u32 s9, s15, 0
	s_mov_b32 m0, s34
	v_lshl_add_u64 v[222:223], s[8:9], 0, v[2:3]
	ds_read_b128 v[174:177], v184 offset:32768
	ds_read_b128 v[178:181], v184 offset:33792
	ds_read_b128 v[186:189], v184 offset:34816
	ds_read_b128 v[190:193], v184 offset:35840
	ds_read_b128 v[194:197], v184 offset:36864
	ds_read_b128 v[198:201], v184 offset:37888
	ds_read_b128 v[206:209], v184 offset:38912
	ds_read_b128 v[210:213], v184 offset:39936
	global_load_lds_dwordx4 v[222:223], off
	v_lshl_add_u64 v[222:223], s[8:9], 0, v[162:163]
	s_mov_b32 m0, s35
	s_nop 0
	global_load_lds_dwordx4 v[222:223], off
	s_waitcnt vmcnt(8)
	s_waitcnt lgkmcnt(0)
	s_barrier
	s_setprio 1
	s_waitcnt lgkmcnt(0)
	v_mfma_f32_16x16x32_bf16 v[130:133], v[134:137], v[174:177], v[130:133]
	v_mfma_f32_16x16x32_bf16 v[126:129], v[142:145], v[174:177], v[126:129]
	v_mfma_f32_16x16x32_bf16 v[114:117], v[134:137], v[186:189], v[114:117]
	v_mfma_f32_16x16x32_bf16 v[110:113], v[142:145], v[186:189], v[110:113]
	v_mfma_f32_16x16x32_bf16 v[98:101], v[134:137], v[194:197], v[98:101]
	v_mfma_f32_16x16x32_bf16 v[94:97], v[142:145], v[194:197], v[94:97]
	v_mfma_f32_16x16x32_bf16 v[82:85], v[134:137], v[206:209], v[82:85]
	v_mfma_f32_16x16x32_bf16 v[78:81], v[142:145], v[206:209], v[78:81]
	v_mfma_f32_16x16x32_bf16 v[130:133], v[138:141], v[178:181], v[130:133]
	v_mfma_f32_16x16x32_bf16 v[126:129], v[146:149], v[178:181], v[126:129]
	v_mfma_f32_16x16x32_bf16 v[114:117], v[138:141], v[190:193], v[114:117]
	v_mfma_f32_16x16x32_bf16 v[110:113], v[146:149], v[190:193], v[110:113]
	v_mfma_f32_16x16x32_bf16 v[98:101], v[138:141], v[198:201], v[98:101]
	v_mfma_f32_16x16x32_bf16 v[94:97], v[146:149], v[198:201], v[94:97]
	v_mfma_f32_16x16x32_bf16 v[82:85], v[138:141], v[210:213], v[82:85]
	v_mfma_f32_16x16x32_bf16 v[78:81], v[146:149], v[210:213], v[78:81]
	s_setprio 0
	s_setprio 1
	v_mfma_f32_16x16x32_bf16 v[122:125], v[150:153], v[174:177], v[122:125]
	v_mfma_f32_16x16x32_bf16 v[118:121], v[158:161], v[174:177], v[118:121]
	v_mfma_f32_16x16x32_bf16 v[106:109], v[150:153], v[186:189], v[106:109]
	v_mfma_f32_16x16x32_bf16 v[102:105], v[158:161], v[186:189], v[102:105]
	v_mfma_f32_16x16x32_bf16 v[90:93], v[150:153], v[194:197], v[90:93]
	v_mfma_f32_16x16x32_bf16 v[86:89], v[158:161], v[194:197], v[86:89]
	v_mfma_f32_16x16x32_bf16 v[74:77], v[150:153], v[206:209], v[74:77]
	v_mfma_f32_16x16x32_bf16 v[70:73], v[158:161], v[206:209], v[70:73]
	v_mfma_f32_16x16x32_bf16 v[122:125], v[154:157], v[178:181], v[122:125]
	v_mfma_f32_16x16x32_bf16 v[118:121], v[170:173], v[178:181], v[118:121]
	v_mfma_f32_16x16x32_bf16 v[106:109], v[154:157], v[190:193], v[106:109]
	v_mfma_f32_16x16x32_bf16 v[102:105], v[170:173], v[190:193], v[102:105]
	v_mfma_f32_16x16x32_bf16 v[90:93], v[154:157], v[198:201], v[90:93]
	v_mfma_f32_16x16x32_bf16 v[86:89], v[170:173], v[198:201], v[86:89]
	s_setprio 2
	s_barrier
	v_mfma_f32_16x16x32_bf16 v[74:77], v[154:157], v[210:213], v[74:77]
	v_mfma_f32_16x16x32_bf16 v[70:73], v[170:173], v[210:213], v[70:73]
	s_setprio 0
	s_mov_b32 m0, s42
	v_lshl_add_u64 v[214:215], v[214:215], 0, s[28:29]
	s_add_u32 s8, s12, 0x158080
	ds_read_b128 v[174:177], v184 offset:49152
	ds_read_b128 v[178:181], v184 offset:50176
	ds_read_b128 v[186:189], v184 offset:51200
	ds_read_b128 v[190:193], v184 offset:52224
	ds_read_b128 v[194:197], v184 offset:53248
	ds_read_b128 v[198:201], v184 offset:54272
	ds_read_b128 v[206:209], v184 offset:55296
	ds_read_b128 v[210:213], v184 offset:56320
	global_load_lds_dwordx4 v[214:215], off
	v_lshl_add_u64 v[214:215], v[216:217], 0, s[28:29]
	s_mov_b32 m0, s43
	s_addc_u32 s9, s13, 0
	global_load_lds_dwordx4 v[214:215], off
	v_lshl_add_u64 v[214:215], s[8:9], 0, v[0:1]
	s_mov_b32 m0, s47
	s_nop 0
	global_load_lds_dwordx4 v[214:215], off
	v_lshl_add_u64 v[214:215], s[8:9], 0, v[164:165]
	s_mov_b32 m0, s48
	s_nop 0
	global_load_lds_dwordx4 v[214:215], off
	v_lshl_add_u64 v[214:215], v[218:219], 0, s[28:29]
	s_mov_b32 m0, s44
	s_nop 0
	global_load_lds_dwordx4 v[214:215], off
	v_lshl_add_u64 v[214:215], v[220:221], 0, s[28:29]
	s_mov_b32 m0, s45
	s_nop 0
	global_load_lds_dwordx4 v[214:215], off
	s_waitcnt vmcnt(8)
	s_waitcnt lgkmcnt(0)
	s_barrier
	s_setprio 1
	s_waitcnt lgkmcnt(0)
	v_mfma_f32_16x16x32_bf16 v[66:69], v[134:137], v[174:177], v[66:69]
	v_mfma_f32_16x16x32_bf16 v[62:65], v[142:145], v[174:177], v[62:65]
	v_mfma_f32_16x16x32_bf16 v[50:53], v[134:137], v[186:189], v[50:53]
	v_mfma_f32_16x16x32_bf16 v[46:49], v[142:145], v[186:189], v[46:49]
	v_mfma_f32_16x16x32_bf16 v[34:37], v[134:137], v[194:197], v[34:37]
	v_mfma_f32_16x16x32_bf16 v[30:33], v[142:145], v[194:197], v[30:33]
	v_mfma_f32_16x16x32_bf16 v[18:21], v[134:137], v[206:209], v[18:21]
	v_mfma_f32_16x16x32_bf16 v[14:17], v[142:145], v[206:209], v[14:17]
	v_mfma_f32_16x16x32_bf16 v[66:69], v[138:141], v[178:181], v[66:69]
	v_mfma_f32_16x16x32_bf16 v[62:65], v[146:149], v[178:181], v[62:65]
	v_mfma_f32_16x16x32_bf16 v[50:53], v[138:141], v[190:193], v[50:53]
	v_mfma_f32_16x16x32_bf16 v[46:49], v[146:149], v[190:193], v[46:49]
	v_mfma_f32_16x16x32_bf16 v[34:37], v[138:141], v[198:201], v[34:37]
	v_mfma_f32_16x16x32_bf16 v[30:33], v[146:149], v[198:201], v[30:33]
	v_mfma_f32_16x16x32_bf16 v[18:21], v[138:141], v[210:213], v[18:21]
	v_mfma_f32_16x16x32_bf16 v[14:17], v[146:149], v[210:213], v[14:17]
	s_setprio 0
	s_setprio 1
	v_mfma_f32_16x16x32_bf16 v[58:61], v[150:153], v[174:177], v[58:61]
	v_mfma_f32_16x16x32_bf16 v[54:57], v[158:161], v[174:177], v[54:57]
	v_mfma_f32_16x16x32_bf16 v[42:45], v[150:153], v[186:189], v[42:45]
	v_mfma_f32_16x16x32_bf16 v[38:41], v[158:161], v[186:189], v[38:41]
	v_mfma_f32_16x16x32_bf16 v[26:29], v[150:153], v[194:197], v[26:29]
	v_mfma_f32_16x16x32_bf16 v[22:25], v[158:161], v[194:197], v[22:25]
	v_mfma_f32_16x16x32_bf16 v[10:13], v[150:153], v[206:209], v[10:13]
	v_mfma_f32_16x16x32_bf16 v[6:9], v[158:161], v[206:209], v[6:9]
	v_mfma_f32_16x16x32_bf16 v[58:61], v[154:157], v[178:181], v[58:61]
	v_mfma_f32_16x16x32_bf16 v[54:57], v[170:173], v[178:181], v[54:57]
	v_mfma_f32_16x16x32_bf16 v[42:45], v[154:157], v[190:193], v[42:45]
	v_mfma_f32_16x16x32_bf16 v[38:41], v[170:173], v[190:193], v[38:41]
	v_mfma_f32_16x16x32_bf16 v[26:29], v[154:157], v[198:201], v[26:29]
	v_mfma_f32_16x16x32_bf16 v[22:25], v[170:173], v[198:201], v[22:25]
	s_setprio 2
	s_barrier
	v_mfma_f32_16x16x32_bf16 v[10:13], v[154:157], v[210:213], v[10:13]
	v_mfma_f32_16x16x32_bf16 v[6:9], v[170:173], v[210:213], v[6:9]
	s_setprio 0
	s_add_i32 s56, s56, 2
	s_add_u32 s54, s54, 0x100
	s_addc_u32 s55, s55, 0
	s_cmpk_gt_u32 s56, 0x53
	s_mov_b64 s[8:9], s[10:11]
	s_cbranch_scc0 .LBB0_246
	s_and_b64 vcc, exec, s[4:5]
	s_cbranch_vccz .LBB0_249
	s_barrier

.LBB0_332:
	v_add_u32_e32 v146, s19, v168
	v_add_u32_e32 v166, s48, v168
	ds_read_b128 v[134:137], v146
	ds_read_b128 v[138:141], v146 offset:1024
	ds_read_b128 v[142:145], v146 offset:2048
	ds_read_b128 v[146:149], v146 offset:3072
	ds_read_b128 v[150:153], v166
	ds_read_b128 v[162:165], v166 offset:1024
	ds_read_b128 v[190:193], v166 offset:2048
	ds_read_b128 v[194:197], v166 offset:3072
	s_add_u32 s30, s40, 0xfff80080
	s_addc_u32 s31, s41, -1
	s_cmp_eq_u32 s42, 28
	s_cselect_b32 s31, s3, s31
	s_cselect_b32 s30, s15, s30
	s_cselect_b32 s35, s13, s67
	s_cselect_b32 s34, s16, s17
	v_lshl_add_u64 v[166:167], s[40:41], 0, v[160:161]
	s_add_i32 m0, s51, 0xc000
	ds_read_b128 v[198:201], v187
	ds_read_b128 v[206:209], v187 offset:1024
	ds_read_b128 v[210:213], v187 offset:2048
	ds_read_b128 v[214:217], v187 offset:3072
	ds_read_b128 v[218:221], v187 offset:4096
	ds_read_b128 v[222:225], v187 offset:5120
	ds_read_b128 v[226:229], v187 offset:6144
	ds_read_b128 v[242:245], v187 offset:7168
	global_load_lds_dwordx4 v[166:167], off
	v_lshl_add_u64 v[166:167], s[40:41], 0, v[158:159]
	s_add_i32 m0, s51, 0xe000
	s_nop 0
	global_load_lds_dwordx4 v[166:167], off
	s_waitcnt vmcnt(8)
	s_waitcnt lgkmcnt(0)
	s_barrier
	s_setprio 1
	s_waitcnt lgkmcnt(0)
	v_mfma_f32_16x16x32_bf16 v[130:133], v[134:137], v[198:201], v[130:133]
	v_mfma_f32_16x16x32_bf16 v[126:129], v[142:145], v[198:201], v[126:129]
	v_mfma_f32_16x16x32_bf16 v[114:117], v[134:137], v[210:213], v[114:117]
	v_mfma_f32_16x16x32_bf16 v[110:113], v[142:145], v[210:213], v[110:113]
	v_mfma_f32_16x16x32_bf16 v[98:101], v[134:137], v[218:221], v[98:101]
	v_mfma_f32_16x16x32_bf16 v[94:97], v[142:145], v[218:221], v[94:97]
	v_mfma_f32_16x16x32_bf16 v[82:85], v[134:137], v[226:229], v[82:85]
	v_mfma_f32_16x16x32_bf16 v[78:81], v[142:145], v[226:229], v[78:81]
	v_mfma_f32_16x16x32_bf16 v[130:133], v[138:141], v[206:209], v[130:133]
	v_mfma_f32_16x16x32_bf16 v[126:129], v[146:149], v[206:209], v[126:129]
	v_mfma_f32_16x16x32_bf16 v[114:117], v[138:141], v[214:217], v[114:117]
	v_mfma_f32_16x16x32_bf16 v[110:113], v[146:149], v[214:217], v[110:113]
	v_mfma_f32_16x16x32_bf16 v[98:101], v[138:141], v[222:225], v[98:101]
	v_mfma_f32_16x16x32_bf16 v[94:97], v[146:149], v[222:225], v[94:97]
	v_mfma_f32_16x16x32_bf16 v[82:85], v[138:141], v[242:245], v[82:85]
	v_mfma_f32_16x16x32_bf16 v[78:81], v[146:149], v[242:245], v[78:81]
	s_setprio 0
	s_setprio 1
	v_mfma_f32_16x16x32_bf16 v[122:125], v[150:153], v[198:201], v[122:125]
	v_mfma_f32_16x16x32_bf16 v[118:121], v[190:193], v[198:201], v[118:121]
	v_mfma_f32_16x16x32_bf16 v[106:109], v[150:153], v[210:213], v[106:109]
	v_mfma_f32_16x16x32_bf16 v[102:105], v[190:193], v[210:213], v[102:105]
	v_mfma_f32_16x16x32_bf16 v[90:93], v[150:153], v[218:221], v[90:93]
	v_mfma_f32_16x16x32_bf16 v[86:89], v[190:193], v[218:221], v[86:89]
	v_mfma_f32_16x16x32_bf16 v[74:77], v[150:153], v[226:229], v[74:77]
	v_mfma_f32_16x16x32_bf16 v[70:73], v[190:193], v[226:229], v[70:73]
	v_mfma_f32_16x16x32_bf16 v[122:125], v[162:165], v[206:209], v[122:125]
	v_mfma_f32_16x16x32_bf16 v[118:121], v[194:197], v[206:209], v[118:121]
	v_mfma_f32_16x16x32_bf16 v[106:109], v[162:165], v[214:217], v[106:109]
	v_mfma_f32_16x16x32_bf16 v[102:105], v[194:197], v[214:217], v[102:105]
	v_mfma_f32_16x16x32_bf16 v[90:93], v[162:165], v[222:225], v[90:93]
	v_mfma_f32_16x16x32_bf16 v[86:89], v[194:197], v[222:225], v[86:89]
	s_setprio 2
	s_barrier
	v_mfma_f32_16x16x32_bf16 v[74:77], v[162:165], v[242:245], v[74:77]
	v_mfma_f32_16x16x32_bf16 v[70:73], v[194:197], v[242:245], v[70:73]
	s_setprio 0
	s_mov_b32 m0, s46
	v_lshl_add_u64 v[166:167], s[34:35], 0, v[0:1]
	s_add_u32 s68, s34, 0x80000
	ds_read_b128 v[198:201], v187 offset:16384
	ds_read_b128 v[206:209], v187 offset:17408
	ds_read_b128 v[210:213], v187 offset:18432
	ds_read_b128 v[214:217], v187 offset:19456
	ds_read_b128 v[218:221], v187 offset:20480
	ds_read_b128 v[222:225], v187 offset:21504
	ds_read_b128 v[226:229], v187 offset:22528
	ds_read_b128 v[242:245], v187 offset:23552
	global_load_lds_dwordx4 v[166:167], off
	v_lshl_add_u64 v[232:233], s[34:35], 0, v[156:157]
	s_mov_b32 m0, s47
	s_addc_u32 s69, s35, 0
	global_load_lds_dwordx4 v[232:233], off
	v_lshl_add_u64 v[236:237], s[68:69], 0, v[0:1]
	s_mov_b32 m0, s49
	v_lshl_add_u64 v[246:247], s[30:31], 0, v[154:155]
	global_load_lds_dwordx4 v[236:237], off
	v_lshl_add_u64 v[236:237], s[68:69], 0, v[156:157]
	s_mov_b32 m0, s50
	s_nop 0
	global_load_lds_dwordx4 v[236:237], off
	v_lshl_add_u64 v[236:237], s[30:31], 0, v[2:3]
	s_mov_b32 m0, s51
	s_nop 0
	global_load_lds_dwordx4 v[236:237], off
	s_mov_b32 m0, s52
	s_nop 0
	global_load_lds_dwordx4 v[246:247], off
	s_waitcnt vmcnt(8)
	s_waitcnt lgkmcnt(0)
	s_barrier
	s_setprio 1
	s_waitcnt lgkmcnt(0)
	v_mfma_f32_16x16x32_bf16 v[66:69], v[134:137], v[198:201], v[66:69]
	v_mfma_f32_16x16x32_bf16 v[62:65], v[142:145], v[198:201], v[62:65]
	v_mfma_f32_16x16x32_bf16 v[50:53], v[134:137], v[210:213], v[50:53]
	v_mfma_f32_16x16x32_bf16 v[46:49], v[142:145], v[210:213], v[46:49]
	v_mfma_f32_16x16x32_bf16 v[34:37], v[134:137], v[218:221], v[34:37]
	v_mfma_f32_16x16x32_bf16 v[30:33], v[142:145], v[218:221], v[30:33]
	v_mfma_f32_16x16x32_bf16 v[18:21], v[134:137], v[226:229], v[18:21]
	v_mfma_f32_16x16x32_bf16 v[14:17], v[142:145], v[226:229], v[14:17]
	v_mfma_f32_16x16x32_bf16 v[66:69], v[138:141], v[206:209], v[66:69]
	v_mfma_f32_16x16x32_bf16 v[62:65], v[146:149], v[206:209], v[62:65]
	v_mfma_f32_16x16x32_bf16 v[50:53], v[138:141], v[214:217], v[50:53]
	v_mfma_f32_16x16x32_bf16 v[46:49], v[146:149], v[214:217], v[46:49]
	v_mfma_f32_16x16x32_bf16 v[34:37], v[138:141], v[222:225], v[34:37]
	v_mfma_f32_16x16x32_bf16 v[30:33], v[146:149], v[222:225], v[30:33]
	v_mfma_f32_16x16x32_bf16 v[18:21], v[138:141], v[242:245], v[18:21]
	v_mfma_f32_16x16x32_bf16 v[14:17], v[146:149], v[242:245], v[14:17]
	s_setprio 0
	s_setprio 1
	v_mfma_f32_16x16x32_bf16 v[58:61], v[150:153], v[198:201], v[58:61]
	v_mfma_f32_16x16x32_bf16 v[54:57], v[190:193], v[198:201], v[54:57]
	v_mfma_f32_16x16x32_bf16 v[42:45], v[150:153], v[210:213], v[42:45]
	v_mfma_f32_16x16x32_bf16 v[38:41], v[190:193], v[210:213], v[38:41]
	v_mfma_f32_16x16x32_bf16 v[26:29], v[150:153], v[218:221], v[26:29]
	v_mfma_f32_16x16x32_bf16 v[22:25], v[190:193], v[218:221], v[22:25]
	v_mfma_f32_16x16x32_bf16 v[10:13], v[150:153], v[226:229], v[10:13]
	v_mfma_f32_16x16x32_bf16 v[6:9], v[190:193], v[226:229], v[6:9]
	v_mfma_f32_16x16x32_bf16 v[58:61], v[162:165], v[206:209], v[58:61]
	v_mfma_f32_16x16x32_bf16 v[54:57], v[194:197], v[206:209], v[54:57]
	v_mfma_f32_16x16x32_bf16 v[42:45], v[162:165], v[214:217], v[42:45]
	v_mfma_f32_16x16x32_bf16 v[38:41], v[194:197], v[214:217], v[38:41]
	v_mfma_f32_16x16x32_bf16 v[26:29], v[162:165], v[222:225], v[26:29]
	v_mfma_f32_16x16x32_bf16 v[22:25], v[194:197], v[222:225], v[22:25]
	s_setprio 2
	s_barrier
	v_mfma_f32_16x16x32_bf16 v[10:13], v[162:165], v[242:245], v[10:13]
	v_mfma_f32_16x16x32_bf16 v[6:9], v[194:197], v[242:245], v[6:9]
	s_setprio 0
	v_add_u32_e32 v146, s56, v168
	v_add_u32_e32 v189, s61, v168
	ds_read_b128 v[134:137], v146
	ds_read_b128 v[138:141], v146 offset:1024
	ds_read_b128 v[142:145], v146 offset:2048
	ds_read_b128 v[146:149], v146 offset:3072
	ds_read_b128 v[150:153], v189
	ds_read_b128 v[162:165], v189 offset:1024
	ds_read_b128 v[190:193], v189 offset:2048
	ds_read_b128 v[194:197], v189 offset:3072
	s_add_u32 s30, s30, 0x80000
	s_addc_u32 s31, s31, 0
	s_mov_b32 m0, s53
	v_lshl_add_u64 v[248:249], s[30:31], 0, v[2:3]
	ds_read_b128 v[198:201], v187 offset:32768
	ds_read_b128 v[206:209], v187 offset:33792
	ds_read_b128 v[210:213], v187 offset:34816
	ds_read_b128 v[214:217], v187 offset:35840
	ds_read_b128 v[218:221], v187 offset:36864
	ds_read_b128 v[222:225], v187 offset:37888
	ds_read_b128 v[226:229], v187 offset:38912
	ds_read_b128 v[242:245], v187 offset:39936
	global_load_lds_dwordx4 v[248:249], off
	v_lshl_add_u64 v[248:249], s[30:31], 0, v[154:155]
	s_mov_b32 m0, s54
	s_nop 0
	global_load_lds_dwordx4 v[248:249], off
	s_waitcnt vmcnt(8)
	s_waitcnt lgkmcnt(0)
	s_barrier
	s_setprio 1
	s_waitcnt lgkmcnt(0)
	v_mfma_f32_16x16x32_bf16 v[130:133], v[134:137], v[198:201], v[130:133]
	v_mfma_f32_16x16x32_bf16 v[126:129], v[142:145], v[198:201], v[126:129]
	v_mfma_f32_16x16x32_bf16 v[114:117], v[134:137], v[210:213], v[114:117]
	v_mfma_f32_16x16x32_bf16 v[110:113], v[142:145], v[210:213], v[110:113]
	v_mfma_f32_16x16x32_bf16 v[98:101], v[134:137], v[218:221], v[98:101]
	v_mfma_f32_16x16x32_bf16 v[94:97], v[142:145], v[218:221], v[94:97]
	v_mfma_f32_16x16x32_bf16 v[82:85], v[134:137], v[226:229], v[82:85]
	v_mfma_f32_16x16x32_bf16 v[78:81], v[142:145], v[226:229], v[78:81]
	v_mfma_f32_16x16x32_bf16 v[130:133], v[138:141], v[206:209], v[130:133]
	v_mfma_f32_16x16x32_bf16 v[126:129], v[146:149], v[206:209], v[126:129]
	v_mfma_f32_16x16x32_bf16 v[114:117], v[138:141], v[214:217], v[114:117]
	v_mfma_f32_16x16x32_bf16 v[110:113], v[146:149], v[214:217], v[110:113]
	v_mfma_f32_16x16x32_bf16 v[98:101], v[138:141], v[222:225], v[98:101]
	v_mfma_f32_16x16x32_bf16 v[94:97], v[146:149], v[222:225], v[94:97]
	v_mfma_f32_16x16x32_bf16 v[82:85], v[138:141], v[242:245], v[82:85]
	v_mfma_f32_16x16x32_bf16 v[78:81], v[146:149], v[242:245], v[78:81]
	s_setprio 0
	s_setprio 1
	v_mfma_f32_16x16x32_bf16 v[122:125], v[150:153], v[198:201], v[122:125]
	v_mfma_f32_16x16x32_bf16 v[118:121], v[190:193], v[198:201], v[118:121]
	v_mfma_f32_16x16x32_bf16 v[106:109], v[150:153], v[210:213], v[106:109]
	v_mfma_f32_16x16x32_bf16 v[102:105], v[190:193], v[210:213], v[102:105]
	v_mfma_f32_16x16x32_bf16 v[90:93], v[150:153], v[218:221], v[90:93]
	v_mfma_f32_16x16x32_bf16 v[86:89], v[190:193], v[218:221], v[86:89]
	v_mfma_f32_16x16x32_bf16 v[74:77], v[150:153], v[226:229], v[74:77]
	v_mfma_f32_16x16x32_bf16 v[70:73], v[190:193], v[226:229], v[70:73]
	v_mfma_f32_16x16x32_bf16 v[122:125], v[162:165], v[206:209], v[122:125]
	v_mfma_f32_16x16x32_bf16 v[118:121], v[194:197], v[206:209], v[118:121]
	v_mfma_f32_16x16x32_bf16 v[106:109], v[162:165], v[214:217], v[106:109]
	v_mfma_f32_16x16x32_bf16 v[102:105], v[194:197], v[214:217], v[102:105]
	v_mfma_f32_16x16x32_bf16 v[90:93], v[162:165], v[222:225], v[90:93]
	v_mfma_f32_16x16x32_bf16 v[86:89], v[194:197], v[222:225], v[86:89]
	s_setprio 2
	s_barrier
	v_mfma_f32_16x16x32_bf16 v[74:77], v[162:165], v[242:245], v[74:77]
	v_mfma_f32_16x16x32_bf16 v[70:73], v[194:197], v[242:245], v[70:73]
	s_setprio 0
	s_mov_b32 m0, s57
	v_lshl_add_u64 v[166:167], v[166:167], 0, s[28:29]
	s_add_u32 s30, s34, 0x80080
	ds_read_b128 v[198:201], v187 offset:49152
	ds_read_b128 v[206:209], v187 offset:50176
	ds_read_b128 v[210:213], v187 offset:51200
	ds_read_b128 v[214:217], v187 offset:52224
	ds_read_b128 v[218:221], v187 offset:53248
	ds_read_b128 v[222:225], v187 offset:54272
	ds_read_b128 v[226:229], v187 offset:55296
	ds_read_b128 v[242:245], v187 offset:56320
	global_load_lds_dwordx4 v[166:167], off
	v_lshl_add_u64 v[166:167], v[232:233], 0, s[28:29]
	s_mov_b32 m0, s58
	s_addc_u32 s31, s35, 0
	global_load_lds_dwordx4 v[166:167], off
	v_lshl_add_u64 v[166:167], s[30:31], 0, v[0:1]
	s_mov_b32 m0, s62
	s_nop 0
	global_load_lds_dwordx4 v[166:167], off
	v_lshl_add_u64 v[166:167], s[30:31], 0, v[156:157]
	s_mov_b32 m0, s63
	s_nop 0
	global_load_lds_dwordx4 v[166:167], off
	v_lshl_add_u64 v[166:167], v[236:237], 0, s[28:29]
	s_mov_b32 m0, s59
	s_nop 0
	global_load_lds_dwordx4 v[166:167], off
	v_lshl_add_u64 v[166:167], v[246:247], 0, s[28:29]
	s_mov_b32 m0, s60
	s_nop 0
	global_load_lds_dwordx4 v[166:167], off
	s_waitcnt vmcnt(8)
	s_waitcnt lgkmcnt(0)
	s_barrier
	s_setprio 1
	s_waitcnt lgkmcnt(0)
	v_mfma_f32_16x16x32_bf16 v[66:69], v[134:137], v[198:201], v[66:69]
	v_mfma_f32_16x16x32_bf16 v[62:65], v[142:145], v[198:201], v[62:65]
	v_mfma_f32_16x16x32_bf16 v[50:53], v[134:137], v[210:213], v[50:53]
	v_mfma_f32_16x16x32_bf16 v[46:49], v[142:145], v[210:213], v[46:49]
	v_mfma_f32_16x16x32_bf16 v[34:37], v[134:137], v[218:221], v[34:37]
	v_mfma_f32_16x16x32_bf16 v[30:33], v[142:145], v[218:221], v[30:33]
	v_mfma_f32_16x16x32_bf16 v[18:21], v[134:137], v[226:229], v[18:21]
	v_mfma_f32_16x16x32_bf16 v[14:17], v[142:145], v[226:229], v[14:17]
	v_mfma_f32_16x16x32_bf16 v[66:69], v[138:141], v[206:209], v[66:69]
	v_mfma_f32_16x16x32_bf16 v[62:65], v[146:149], v[206:209], v[62:65]
	v_mfma_f32_16x16x32_bf16 v[50:53], v[138:141], v[214:217], v[50:53]
	v_mfma_f32_16x16x32_bf16 v[46:49], v[146:149], v[214:217], v[46:49]
	v_mfma_f32_16x16x32_bf16 v[34:37], v[138:141], v[222:225], v[34:37]
	v_mfma_f32_16x16x32_bf16 v[30:33], v[146:149], v[222:225], v[30:33]
	v_mfma_f32_16x16x32_bf16 v[18:21], v[138:141], v[242:245], v[18:21]
	v_mfma_f32_16x16x32_bf16 v[14:17], v[146:149], v[242:245], v[14:17]
	s_setprio 0
	s_setprio 1
	v_mfma_f32_16x16x32_bf16 v[58:61], v[150:153], v[198:201], v[58:61]
	v_mfma_f32_16x16x32_bf16 v[54:57], v[190:193], v[198:201], v[54:57]
	v_mfma_f32_16x16x32_bf16 v[42:45], v[150:153], v[210:213], v[42:45]
	v_mfma_f32_16x16x32_bf16 v[38:41], v[190:193], v[210:213], v[38:41]
	v_mfma_f32_16x16x32_bf16 v[26:29], v[150:153], v[218:221], v[26:29]
	v_mfma_f32_16x16x32_bf16 v[22:25], v[190:193], v[218:221], v[22:25]
	v_mfma_f32_16x16x32_bf16 v[10:13], v[150:153], v[226:229], v[10:13]
	v_mfma_f32_16x16x32_bf16 v[6:9], v[190:193], v[226:229], v[6:9]
	v_mfma_f32_16x16x32_bf16 v[58:61], v[162:165], v[206:209], v[58:61]
	v_mfma_f32_16x16x32_bf16 v[54:57], v[194:197], v[206:209], v[54:57]
	v_mfma_f32_16x16x32_bf16 v[42:45], v[162:165], v[214:217], v[42:45]
	v_mfma_f32_16x16x32_bf16 v[38:41], v[194:197], v[214:217], v[38:41]
	v_mfma_f32_16x16x32_bf16 v[26:29], v[162:165], v[222:225], v[26:29]
	v_mfma_f32_16x16x32_bf16 v[22:25], v[194:197], v[222:225], v[22:25]
	s_setprio 2
	s_barrier
	v_mfma_f32_16x16x32_bf16 v[10:13], v[162:165], v[242:245], v[10:13]
	v_mfma_f32_16x16x32_bf16 v[6:9], v[194:197], v[242:245], v[6:9]
	s_setprio 0
	s_add_i32 s42, s42, 2
	s_add_u32 s17, s17, 0x100
	s_addc_u32 s67, s67, 0
	s_add_u32 s40, s40, 0x100
	s_addc_u32 s41, s41, 0
	s_cmp_gt_u32 s42, 29
	s_cbranch_scc0 .LBB0_332
	s_and_b64 vcc, exec, s[8:9]
	s_cbranch_vccz .LBB0_335
	s_barrier

.LBB0_1806:
	s_andn2_saveexec_b64 s[4:5], s[4:5]
	s_cbranch_execz .LBB0_1823
	v_cmp_lt_u32_e32 vcc, 1, v0
	s_and_saveexec_b64 s[4:5], vcc
	s_cbranch_execz .LBB0_1822
	buffer_wbl2 sc1
	s_waitcnt vmcnt(0)
	v_mov_b32_e32 v2, s2
	v_add_co_u32_e32 v2, vcc, 0x3000, v2
	v_mov_b32_e32 v3, s3
	s_nop 0
	v_addc_co_u32_e32 v3, vcc, 0, v3, vcc
	v_mov_b32_e32 v5, 1
	flat_atomic_add v2, v[2:3], v5 offset:1024 sc0
	v_cvt_f32_u32_e32 v3, v0
	v_sub_u32_e32 v5, 0, v0
	s_mov_b64 s[10:11], -1
	v_rcp_iflag_f32_e32 v3, v3
	s_nop 0
	v_mul_f32_e32 v3, 0x4f7ffffe, v3
	v_cvt_u32_f32_e32 v3, v3
	v_mul_lo_u32 v5, v5, v3
	v_mul_hi_u32 v5, v3, v5
	v_add_u32_e32 v3, v3, v5
	s_waitcnt vmcnt(0) lgkmcnt(0)
	v_mul_hi_u32 v3, v2, v3
	v_mul_lo_u32 v5, v3, v0
	v_sub_u32_e32 v5, v2, v5
	v_cmp_ge_u32_e32 vcc, v5, v0
	v_add_u32_e32 v6, 1, v3
	s_nop 0
	v_cndmask_b32_e32 v3, v3, v6, vcc
	v_sub_u32_e32 v6, v5, v0
	v_cndmask_b32_e32 v5, v5, v6, vcc
	v_cmp_ge_u32_e32 vcc, v5, v0
	v_add_u32_e32 v5, 1, v3
	v_add_u32_e32 v6, 1, v2
	v_cndmask_b32_e32 v5, v3, v5, vcc
	v_mad_u64_u32 v[2:3], s[6:7], v0, v5, v[0:1]
	s_add_u32 s6, s2, 0x3500
	s_addc_u32 s7, s3, 0
	v_cmp_ne_u32_e32 vcc, v6, v2
	v_mov_b64_e32 v[2:3], s[6:7]
	s_and_saveexec_b64 s[8:9], vcc
	s_cbranch_execz .LBB0_1820
	v_mov_b64_e32 v[2:3], s[6:7]
	flat_load_dword v0, v[2:3] sc1
	s_mov_b64 s[14:15], 0
	s_waitcnt vmcnt(0) lgkmcnt(0)
	v_cmp_eq_u32_e32 vcc, v0, v5
	s_and_saveexec_b64 s[12:13], vcc
	s_cbranch_execz .LBB0_1819
	s_add_u32 s10, s2, 0x200
	s_addc_u32 s11, s3, 0
	s_mov_b32 s34, 1
	s_mov_b64 s[2:3], 0
	s_branch .LBB0_1812

.LBB0_1846:
	v_add_u32_e32 v146, s31, v172
	v_add_u32_e32 v170, s38, v172
	ds_read_b128 v[134:137], v146
	ds_read_b128 v[138:141], v146 offset:1024
	ds_read_b128 v[142:145], v146 offset:2048
	ds_read_b128 v[146:149], v146 offset:3072
	ds_read_b128 v[150:153], v170
	ds_read_b128 v[162:165], v170 offset:1024
	ds_read_b128 v[166:169], v170 offset:2048
	ds_read_b128 v[176:179], v170 offset:3072
	s_add_u32 s2, s18, 0x100
	s_addc_u32 s3, s19, 0
	s_cmp_eq_u32 s60, 28
	s_cselect_b32 s25, s13, s3
	s_cselect_b32 s24, s12, s2
	s_cselect_b32 s23, s11, s59
	s_cselect_b32 s22, s57, s58
	v_lshl_add_u64 v[170:171], s[18:19], 0, v[160:161]
	s_add_i32 m0, s41, 0xc000
	ds_read_b128 v[180:183], v174
	ds_read_b128 v[184:187], v174 offset:1024
	ds_read_b128 v[188:191], v174 offset:2048
	ds_read_b128 v[192:195], v174 offset:3072
	ds_read_b128 v[196:199], v174 offset:4096
	ds_read_b128 v[206:209], v174 offset:5120
	ds_read_b128 v[210:213], v174 offset:6144
	ds_read_b128 v[214:217], v174 offset:7168
	global_load_lds_dwordx4 v[170:171], off
	v_lshl_add_u64 v[170:171], s[18:19], 0, v[158:159]
	s_add_i32 m0, s41, 0xe000
	s_nop 0
	global_load_lds_dwordx4 v[170:171], off
	s_waitcnt vmcnt(8)
	s_waitcnt lgkmcnt(0)
	s_barrier
	s_setprio 1
	s_waitcnt lgkmcnt(0)
	v_mfma_f32_16x16x32_bf16 v[130:133], v[134:137], v[180:183], v[130:133]
	v_mfma_f32_16x16x32_bf16 v[126:129], v[142:145], v[180:183], v[126:129]
	v_mfma_f32_16x16x32_bf16 v[114:117], v[134:137], v[188:191], v[114:117]
	v_mfma_f32_16x16x32_bf16 v[110:113], v[142:145], v[188:191], v[110:113]
	v_mfma_f32_16x16x32_bf16 v[98:101], v[134:137], v[196:199], v[98:101]
	v_mfma_f32_16x16x32_bf16 v[94:97], v[142:145], v[196:199], v[94:97]
	v_mfma_f32_16x16x32_bf16 v[82:85], v[134:137], v[210:213], v[82:85]
	v_mfma_f32_16x16x32_bf16 v[78:81], v[142:145], v[210:213], v[78:81]
	v_mfma_f32_16x16x32_bf16 v[130:133], v[138:141], v[184:187], v[130:133]
	v_mfma_f32_16x16x32_bf16 v[126:129], v[146:149], v[184:187], v[126:129]
	v_mfma_f32_16x16x32_bf16 v[114:117], v[138:141], v[192:195], v[114:117]
	v_mfma_f32_16x16x32_bf16 v[110:113], v[146:149], v[192:195], v[110:113]
	v_mfma_f32_16x16x32_bf16 v[98:101], v[138:141], v[206:209], v[98:101]
	v_mfma_f32_16x16x32_bf16 v[94:97], v[146:149], v[206:209], v[94:97]
	v_mfma_f32_16x16x32_bf16 v[82:85], v[138:141], v[214:217], v[82:85]
	v_mfma_f32_16x16x32_bf16 v[78:81], v[146:149], v[214:217], v[78:81]
	s_setprio 0
	s_setprio 1
	v_mfma_f32_16x16x32_bf16 v[122:125], v[150:153], v[180:183], v[122:125]
	v_mfma_f32_16x16x32_bf16 v[118:121], v[166:169], v[180:183], v[118:121]
	v_mfma_f32_16x16x32_bf16 v[106:109], v[150:153], v[188:191], v[106:109]
	v_mfma_f32_16x16x32_bf16 v[102:105], v[166:169], v[188:191], v[102:105]
	v_mfma_f32_16x16x32_bf16 v[90:93], v[150:153], v[196:199], v[90:93]
	v_mfma_f32_16x16x32_bf16 v[86:89], v[166:169], v[196:199], v[86:89]
	v_mfma_f32_16x16x32_bf16 v[74:77], v[150:153], v[210:213], v[74:77]
	v_mfma_f32_16x16x32_bf16 v[70:73], v[166:169], v[210:213], v[70:73]
	v_mfma_f32_16x16x32_bf16 v[122:125], v[162:165], v[184:187], v[122:125]
	v_mfma_f32_16x16x32_bf16 v[118:121], v[176:179], v[184:187], v[118:121]
	v_mfma_f32_16x16x32_bf16 v[106:109], v[162:165], v[192:195], v[106:109]
	v_mfma_f32_16x16x32_bf16 v[102:105], v[176:179], v[192:195], v[102:105]
	v_mfma_f32_16x16x32_bf16 v[90:93], v[162:165], v[206:209], v[90:93]
	v_mfma_f32_16x16x32_bf16 v[86:89], v[176:179], v[206:209], v[86:89]
	s_setprio 2
	s_barrier
	v_mfma_f32_16x16x32_bf16 v[74:77], v[162:165], v[214:217], v[74:77]
	v_mfma_f32_16x16x32_bf16 v[70:73], v[176:179], v[214:217], v[70:73]
	s_setprio 0
	s_mov_b32 m0, s34
	v_lshl_add_u64 v[170:171], s[22:23], 0, v[0:1]
	s_add_u32 s18, s22, 0x80000
	ds_read_b128 v[180:183], v174 offset:16384
	ds_read_b128 v[184:187], v174 offset:17408
	ds_read_b128 v[188:191], v174 offset:18432
	ds_read_b128 v[192:195], v174 offset:19456
	ds_read_b128 v[196:199], v174 offset:20480
	ds_read_b128 v[206:209], v174 offset:21504
	ds_read_b128 v[210:213], v174 offset:22528
	ds_read_b128 v[214:217], v174 offset:23552
	global_load_lds_dwordx4 v[170:171], off
	v_lshl_add_u64 v[200:201], s[22:23], 0, v[156:157]
	s_mov_b32 m0, s35
	s_addc_u32 s19, s23, 0
	global_load_lds_dwordx4 v[200:201], off
	v_lshl_add_u64 v[218:219], s[18:19], 0, v[0:1]
	s_mov_b32 m0, s39
	v_lshl_add_u64 v[220:221], s[24:25], 0, v[154:155]
	global_load_lds_dwordx4 v[218:219], off
	v_lshl_add_u64 v[218:219], s[18:19], 0, v[156:157]
	s_mov_b32 m0, s40
	s_nop 0
	global_load_lds_dwordx4 v[218:219], off
	v_lshl_add_u64 v[218:219], s[24:25], 0, v[2:3]
	s_mov_b32 m0, s41
	s_nop 0
	global_load_lds_dwordx4 v[218:219], off
	s_mov_b32 m0, s42
	s_nop 0
	global_load_lds_dwordx4 v[220:221], off
	s_waitcnt vmcnt(8)
	s_waitcnt lgkmcnt(0)
	s_barrier
	s_setprio 1
	s_waitcnt lgkmcnt(0)
	v_mfma_f32_16x16x32_bf16 v[66:69], v[134:137], v[180:183], v[66:69]
	v_mfma_f32_16x16x32_bf16 v[62:65], v[142:145], v[180:183], v[62:65]
	v_mfma_f32_16x16x32_bf16 v[50:53], v[134:137], v[188:191], v[50:53]
	v_mfma_f32_16x16x32_bf16 v[46:49], v[142:145], v[188:191], v[46:49]
	v_mfma_f32_16x16x32_bf16 v[34:37], v[134:137], v[196:199], v[34:37]
	v_mfma_f32_16x16x32_bf16 v[30:33], v[142:145], v[196:199], v[30:33]
	v_mfma_f32_16x16x32_bf16 v[18:21], v[134:137], v[210:213], v[18:21]
	v_mfma_f32_16x16x32_bf16 v[14:17], v[142:145], v[210:213], v[14:17]
	v_mfma_f32_16x16x32_bf16 v[66:69], v[138:141], v[184:187], v[66:69]
	v_mfma_f32_16x16x32_bf16 v[62:65], v[146:149], v[184:187], v[62:65]
	v_mfma_f32_16x16x32_bf16 v[50:53], v[138:141], v[192:195], v[50:53]
	v_mfma_f32_16x16x32_bf16 v[46:49], v[146:149], v[192:195], v[46:49]
	v_mfma_f32_16x16x32_bf16 v[34:37], v[138:141], v[206:209], v[34:37]
	v_mfma_f32_16x16x32_bf16 v[30:33], v[146:149], v[206:209], v[30:33]
	v_mfma_f32_16x16x32_bf16 v[18:21], v[138:141], v[214:217], v[18:21]
	v_mfma_f32_16x16x32_bf16 v[14:17], v[146:149], v[214:217], v[14:17]
	s_setprio 0
	s_setprio 1
	v_mfma_f32_16x16x32_bf16 v[58:61], v[150:153], v[180:183], v[58:61]
	v_mfma_f32_16x16x32_bf16 v[54:57], v[166:169], v[180:183], v[54:57]
	v_mfma_f32_16x16x32_bf16 v[42:45], v[150:153], v[188:191], v[42:45]
	v_mfma_f32_16x16x32_bf16 v[38:41], v[166:169], v[188:191], v[38:41]
	v_mfma_f32_16x16x32_bf16 v[26:29], v[150:153], v[196:199], v[26:29]
	v_mfma_f32_16x16x32_bf16 v[22:25], v[166:169], v[196:199], v[22:25]
	v_mfma_f32_16x16x32_bf16 v[10:13], v[150:153], v[210:213], v[10:13]
	v_mfma_f32_16x16x32_bf16 v[6:9], v[166:169], v[210:213], v[6:9]
	v_mfma_f32_16x16x32_bf16 v[58:61], v[162:165], v[184:187], v[58:61]
	v_mfma_f32_16x16x32_bf16 v[54:57], v[176:179], v[184:187], v[54:57]
	v_mfma_f32_16x16x32_bf16 v[42:45], v[162:165], v[192:195], v[42:45]
	v_mfma_f32_16x16x32_bf16 v[38:41], v[176:179], v[192:195], v[38:41]
	v_mfma_f32_16x16x32_bf16 v[26:29], v[162:165], v[206:209], v[26:29]
	v_mfma_f32_16x16x32_bf16 v[22:25], v[176:179], v[206:209], v[22:25]
	s_setprio 2
	s_barrier
	v_mfma_f32_16x16x32_bf16 v[10:13], v[162:165], v[214:217], v[10:13]
	v_mfma_f32_16x16x32_bf16 v[6:9], v[176:179], v[214:217], v[6:9]
	s_setprio 0
	v_add_u32_e32 v146, s45, v172
	v_add_u32_e32 v175, s50, v172
	ds_read_b128 v[134:137], v146
	ds_read_b128 v[138:141], v146 offset:1024
	ds_read_b128 v[142:145], v146 offset:2048
	ds_read_b128 v[146:149], v146 offset:3072
	ds_read_b128 v[150:153], v175
	ds_read_b128 v[162:165], v175 offset:1024
	ds_read_b128 v[166:169], v175 offset:2048
	ds_read_b128 v[176:179], v175 offset:3072
	s_add_u32 s18, s24, 0x280000
	s_addc_u32 s19, s25, 0
	s_mov_b32 m0, s43
	v_lshl_add_u64 v[222:223], s[18:19], 0, v[2:3]
	ds_read_b128 v[180:183], v174 offset:32768
	ds_read_b128 v[184:187], v174 offset:33792
	ds_read_b128 v[188:191], v174 offset:34816
	ds_read_b128 v[192:195], v174 offset:35840
	ds_read_b128 v[196:199], v174 offset:36864
	ds_read_b128 v[206:209], v174 offset:37888
	ds_read_b128 v[210:213], v174 offset:38912
	ds_read_b128 v[214:217], v174 offset:39936
	global_load_lds_dwordx4 v[222:223], off
	v_lshl_add_u64 v[222:223], s[18:19], 0, v[154:155]
	s_mov_b32 m0, s44
	s_nop 0
	global_load_lds_dwordx4 v[222:223], off
	s_waitcnt vmcnt(8)
	s_waitcnt lgkmcnt(0)
	s_barrier
	s_setprio 1
	s_waitcnt lgkmcnt(0)
	v_mfma_f32_16x16x32_bf16 v[130:133], v[134:137], v[180:183], v[130:133]
	v_mfma_f32_16x16x32_bf16 v[126:129], v[142:145], v[180:183], v[126:129]
	v_mfma_f32_16x16x32_bf16 v[114:117], v[134:137], v[188:191], v[114:117]
	v_mfma_f32_16x16x32_bf16 v[110:113], v[142:145], v[188:191], v[110:113]
	v_mfma_f32_16x16x32_bf16 v[98:101], v[134:137], v[196:199], v[98:101]
	v_mfma_f32_16x16x32_bf16 v[94:97], v[142:145], v[196:199], v[94:97]
	v_mfma_f32_16x16x32_bf16 v[82:85], v[134:137], v[210:213], v[82:85]
	v_mfma_f32_16x16x32_bf16 v[78:81], v[142:145], v[210:213], v[78:81]
	v_mfma_f32_16x16x32_bf16 v[130:133], v[138:141], v[184:187], v[130:133]
	v_mfma_f32_16x16x32_bf16 v[126:129], v[146:149], v[184:187], v[126:129]
	v_mfma_f32_16x16x32_bf16 v[114:117], v[138:141], v[192:195], v[114:117]
	v_mfma_f32_16x16x32_bf16 v[110:113], v[146:149], v[192:195], v[110:113]
	v_mfma_f32_16x16x32_bf16 v[98:101], v[138:141], v[206:209], v[98:101]
	v_mfma_f32_16x16x32_bf16 v[94:97], v[146:149], v[206:209], v[94:97]
	v_mfma_f32_16x16x32_bf16 v[82:85], v[138:141], v[214:217], v[82:85]
	v_mfma_f32_16x16x32_bf16 v[78:81], v[146:149], v[214:217], v[78:81]
	s_setprio 0
	s_setprio 1
	v_mfma_f32_16x16x32_bf16 v[122:125], v[150:153], v[180:183], v[122:125]
	v_mfma_f32_16x16x32_bf16 v[118:121], v[166:169], v[180:183], v[118:121]
	v_mfma_f32_16x16x32_bf16 v[106:109], v[150:153], v[188:191], v[106:109]
	v_mfma_f32_16x16x32_bf16 v[102:105], v[166:169], v[188:191], v[102:105]
	v_mfma_f32_16x16x32_bf16 v[90:93], v[150:153], v[196:199], v[90:93]
	v_mfma_f32_16x16x32_bf16 v[86:89], v[166:169], v[196:199], v[86:89]
	v_mfma_f32_16x16x32_bf16 v[74:77], v[150:153], v[210:213], v[74:77]
	v_mfma_f32_16x16x32_bf16 v[70:73], v[166:169], v[210:213], v[70:73]
	v_mfma_f32_16x16x32_bf16 v[122:125], v[162:165], v[184:187], v[122:125]
	v_mfma_f32_16x16x32_bf16 v[118:121], v[176:179], v[184:187], v[118:121]
	v_mfma_f32_16x16x32_bf16 v[106:109], v[162:165], v[192:195], v[106:109]
	v_mfma_f32_16x16x32_bf16 v[102:105], v[176:179], v[192:195], v[102:105]
	v_mfma_f32_16x16x32_bf16 v[90:93], v[162:165], v[206:209], v[90:93]
	v_mfma_f32_16x16x32_bf16 v[86:89], v[176:179], v[206:209], v[86:89]
	s_setprio 2
	s_barrier
	v_mfma_f32_16x16x32_bf16 v[74:77], v[162:165], v[214:217], v[74:77]
	v_mfma_f32_16x16x32_bf16 v[70:73], v[176:179], v[214:217], v[70:73]
	s_setprio 0
	s_mov_b32 m0, s46
	v_lshl_add_u64 v[170:171], v[170:171], 0, s[28:29]
	s_add_u32 s18, s22, 0x80080
	ds_read_b128 v[180:183], v174 offset:49152
	ds_read_b128 v[184:187], v174 offset:50176
	ds_read_b128 v[188:191], v174 offset:51200
	ds_read_b128 v[192:195], v174 offset:52224
	ds_read_b128 v[196:199], v174 offset:53248
	ds_read_b128 v[206:209], v174 offset:54272
	ds_read_b128 v[210:213], v174 offset:55296
	ds_read_b128 v[214:217], v174 offset:56320
	global_load_lds_dwordx4 v[170:171], off
	v_lshl_add_u64 v[170:171], v[200:201], 0, s[28:29]
	s_mov_b32 m0, s47
	s_addc_u32 s19, s23, 0
	global_load_lds_dwordx4 v[170:171], off
	v_lshl_add_u64 v[170:171], s[18:19], 0, v[0:1]
	s_mov_b32 m0, s51
	s_nop 0
	global_load_lds_dwordx4 v[170:171], off
	v_lshl_add_u64 v[170:171], s[18:19], 0, v[156:157]
	s_mov_b32 m0, s52
	s_nop 0
	global_load_lds_dwordx4 v[170:171], off
	v_lshl_add_u64 v[170:171], v[218:219], 0, s[28:29]
	s_mov_b32 m0, s48
	s_nop 0
	global_load_lds_dwordx4 v[170:171], off
	v_lshl_add_u64 v[170:171], v[220:221], 0, s[28:29]
	s_mov_b32 m0, s49
	s_nop 0
	global_load_lds_dwordx4 v[170:171], off
	s_waitcnt vmcnt(8)
	s_waitcnt lgkmcnt(0)
	s_barrier
	s_setprio 1
	s_waitcnt lgkmcnt(0)
	v_mfma_f32_16x16x32_bf16 v[66:69], v[134:137], v[180:183], v[66:69]
	v_mfma_f32_16x16x32_bf16 v[62:65], v[142:145], v[180:183], v[62:65]
	v_mfma_f32_16x16x32_bf16 v[50:53], v[134:137], v[188:191], v[50:53]
	v_mfma_f32_16x16x32_bf16 v[46:49], v[142:145], v[188:191], v[46:49]
	v_mfma_f32_16x16x32_bf16 v[34:37], v[134:137], v[196:199], v[34:37]
	v_mfma_f32_16x16x32_bf16 v[30:33], v[142:145], v[196:199], v[30:33]
	v_mfma_f32_16x16x32_bf16 v[18:21], v[134:137], v[210:213], v[18:21]
	v_mfma_f32_16x16x32_bf16 v[14:17], v[142:145], v[210:213], v[14:17]
	v_mfma_f32_16x16x32_bf16 v[66:69], v[138:141], v[184:187], v[66:69]
	v_mfma_f32_16x16x32_bf16 v[62:65], v[146:149], v[184:187], v[62:65]
	v_mfma_f32_16x16x32_bf16 v[50:53], v[138:141], v[192:195], v[50:53]
	v_mfma_f32_16x16x32_bf16 v[46:49], v[146:149], v[192:195], v[46:49]
	v_mfma_f32_16x16x32_bf16 v[34:37], v[138:141], v[206:209], v[34:37]
	v_mfma_f32_16x16x32_bf16 v[30:33], v[146:149], v[206:209], v[30:33]
	v_mfma_f32_16x16x32_bf16 v[18:21], v[138:141], v[214:217], v[18:21]
	v_mfma_f32_16x16x32_bf16 v[14:17], v[146:149], v[214:217], v[14:17]
	s_setprio 0
	s_setprio 1
	v_mfma_f32_16x16x32_bf16 v[58:61], v[150:153], v[180:183], v[58:61]
	v_mfma_f32_16x16x32_bf16 v[54:57], v[166:169], v[180:183], v[54:57]
	v_mfma_f32_16x16x32_bf16 v[42:45], v[150:153], v[188:191], v[42:45]
	v_mfma_f32_16x16x32_bf16 v[38:41], v[166:169], v[188:191], v[38:41]
	v_mfma_f32_16x16x32_bf16 v[26:29], v[150:153], v[196:199], v[26:29]
	v_mfma_f32_16x16x32_bf16 v[22:25], v[166:169], v[196:199], v[22:25]
	v_mfma_f32_16x16x32_bf16 v[10:13], v[150:153], v[210:213], v[10:13]
	v_mfma_f32_16x16x32_bf16 v[6:9], v[166:169], v[210:213], v[6:9]
	v_mfma_f32_16x16x32_bf16 v[58:61], v[162:165], v[184:187], v[58:61]
	v_mfma_f32_16x16x32_bf16 v[54:57], v[176:179], v[184:187], v[54:57]
	v_mfma_f32_16x16x32_bf16 v[42:45], v[162:165], v[192:195], v[42:45]
	v_mfma_f32_16x16x32_bf16 v[38:41], v[176:179], v[192:195], v[38:41]
	v_mfma_f32_16x16x32_bf16 v[26:29], v[162:165], v[206:209], v[26:29]
	v_mfma_f32_16x16x32_bf16 v[22:25], v[176:179], v[206:209], v[22:25]
	s_setprio 2
	s_barrier
	v_mfma_f32_16x16x32_bf16 v[10:13], v[162:165], v[214:217], v[10:13]
	v_mfma_f32_16x16x32_bf16 v[6:9], v[176:179], v[214:217], v[6:9]
	s_setprio 0
	s_add_i32 s60, s60, 2
	s_add_u32 s58, s58, 0x100
	s_addc_u32 s59, s59, 0
	s_cmp_gt_u32 s60, 29
	s_mov_b64 s[18:19], s[2:3]
	s_cbranch_scc0 .LBB0_1846
	s_and_b64 vcc, exec, s[8:9]
	s_cbranch_vccz .LBB0_1849
	s_barrier

.LBB0_1875:
	v_add_u32_e32 v138, s35, v241
	v_add_u32_e32 v162, s40, v241
	ds_read_b128 v[118:121], v138
	ds_read_b128 v[122:125], v138 offset:1024
	ds_read_b128 v[130:133], v138 offset:2048
	ds_read_b128 v[138:141], v138 offset:3072
	ds_read_b128 v[142:145], v162
	ds_read_b128 v[150:153], v162 offset:1024
	ds_read_b128 v[154:157], v162 offset:2048
	ds_read_b128 v[162:165], v162 offset:3072
	s_add_u32 s22, s18, 0xfffc0080
	s_addc_u32 s23, s19, -1
	s_cmp_eq_u32 s60, 12
	s_cselect_b32 s25, s13, s23
	s_cselect_b32 s24, s56, s22
	s_cselect_b32 s23, s11, s59
	s_cselect_b32 s22, s57, s58
	v_lshl_add_u64 v[198:199], s[18:19], 0, v[212:213]
	s_add_i32 m0, s43, 0xc000
	ds_read_b128 v[166:169], v243
	ds_read_b128 v[170:173], v243 offset:1024
	ds_read_b128 v[174:177], v243 offset:2048
	ds_read_b128 v[178:181], v243 offset:3072
	ds_read_b128 v[182:185], v243 offset:4096
	ds_read_b128 v[186:189], v243 offset:5120
	ds_read_b128 v[190:193], v243 offset:6144
	ds_read_b128 v[194:197], v243 offset:7168
	global_load_lds_dwordx4 v[198:199], off
	v_lshl_add_u64 v[198:199], s[18:19], 0, v[210:211]
	s_add_i32 m0, s43, 0xe000
	s_nop 0
	global_load_lds_dwordx4 v[198:199], off
	s_waitcnt vmcnt(8)
	s_waitcnt lgkmcnt(0)
	s_barrier
	s_setprio 1
	s_waitcnt lgkmcnt(0)
	v_mfma_f32_16x16x32_bf16 v[158:161], v[118:121], v[166:169], v[158:161]
	v_mfma_f32_16x16x32_bf16 v[146:149], v[130:133], v[166:169], v[146:149]
	v_mfma_f32_16x16x32_bf16 v[114:117], v[118:121], v[174:177], v[114:117]
	v_mfma_f32_16x16x32_bf16 v[110:113], v[130:133], v[174:177], v[110:113]
	v_mfma_f32_16x16x32_bf16 v[98:101], v[118:121], v[182:185], v[98:101]
	v_mfma_f32_16x16x32_bf16 v[94:97], v[130:133], v[182:185], v[94:97]
	v_mfma_f32_16x16x32_bf16 v[82:85], v[118:121], v[190:193], v[82:85]
	v_mfma_f32_16x16x32_bf16 v[78:81], v[130:133], v[190:193], v[78:81]
	v_mfma_f32_16x16x32_bf16 v[158:161], v[122:125], v[170:173], v[158:161]
	v_mfma_f32_16x16x32_bf16 v[146:149], v[138:141], v[170:173], v[146:149]
	v_mfma_f32_16x16x32_bf16 v[114:117], v[122:125], v[178:181], v[114:117]
	v_mfma_f32_16x16x32_bf16 v[110:113], v[138:141], v[178:181], v[110:113]
	v_mfma_f32_16x16x32_bf16 v[98:101], v[122:125], v[186:189], v[98:101]
	v_mfma_f32_16x16x32_bf16 v[94:97], v[138:141], v[186:189], v[94:97]
	v_mfma_f32_16x16x32_bf16 v[82:85], v[122:125], v[194:197], v[82:85]
	v_mfma_f32_16x16x32_bf16 v[78:81], v[138:141], v[194:197], v[78:81]
	s_setprio 0
	s_setprio 1
	v_mfma_f32_16x16x32_bf16 v[134:137], v[142:145], v[166:169], v[134:137]
	v_mfma_f32_16x16x32_bf16 v[126:129], v[154:157], v[166:169], v[126:129]
	v_mfma_f32_16x16x32_bf16 v[106:109], v[142:145], v[174:177], v[106:109]
	v_mfma_f32_16x16x32_bf16 v[102:105], v[154:157], v[174:177], v[102:105]
	v_mfma_f32_16x16x32_bf16 v[90:93], v[142:145], v[182:185], v[90:93]
	v_mfma_f32_16x16x32_bf16 v[86:89], v[154:157], v[182:185], v[86:89]
	v_mfma_f32_16x16x32_bf16 v[74:77], v[142:145], v[190:193], v[74:77]
	v_mfma_f32_16x16x32_bf16 v[70:73], v[154:157], v[190:193], v[70:73]
	v_mfma_f32_16x16x32_bf16 v[134:137], v[150:153], v[170:173], v[134:137]
	v_mfma_f32_16x16x32_bf16 v[126:129], v[162:165], v[170:173], v[126:129]
	v_mfma_f32_16x16x32_bf16 v[106:109], v[150:153], v[178:181], v[106:109]
	v_mfma_f32_16x16x32_bf16 v[102:105], v[162:165], v[178:181], v[102:105]
	v_mfma_f32_16x16x32_bf16 v[90:93], v[150:153], v[186:189], v[90:93]
	v_mfma_f32_16x16x32_bf16 v[86:89], v[162:165], v[186:189], v[86:89]
	s_setprio 2
	s_barrier
	v_mfma_f32_16x16x32_bf16 v[74:77], v[150:153], v[194:197], v[74:77]
	v_mfma_f32_16x16x32_bf16 v[70:73], v[162:165], v[194:197], v[70:73]
	s_setprio 0
	s_mov_b32 m0, s38
	v_lshl_add_u64 v[198:199], s[22:23], 0, v[0:1]
	s_add_u32 s62, s22, 0x40000
	ds_read_b128 v[166:169], v243 offset:16384
	ds_read_b128 v[170:173], v243 offset:17408
	ds_read_b128 v[174:177], v243 offset:18432
	ds_read_b128 v[178:181], v243 offset:19456
	ds_read_b128 v[182:185], v243 offset:20480
	ds_read_b128 v[186:189], v243 offset:21504
	ds_read_b128 v[190:193], v243 offset:22528
	ds_read_b128 v[194:197], v243 offset:23552
	global_load_lds_dwordx4 v[198:199], off
	v_lshl_add_u64 v[200:201], s[22:23], 0, v[208:209]
	s_mov_b32 m0, s39
	s_addc_u32 s63, s23, 0
	global_load_lds_dwordx4 v[200:201], off
	v_lshl_add_u64 v[214:215], s[62:63], 0, v[0:1]
	s_mov_b32 m0, s41
	v_lshl_add_u64 v[216:217], s[24:25], 0, v[206:207]
	global_load_lds_dwordx4 v[214:215], off
	v_lshl_add_u64 v[214:215], s[62:63], 0, v[208:209]
	s_mov_b32 m0, s42
	s_nop 0
	global_load_lds_dwordx4 v[214:215], off
	v_lshl_add_u64 v[214:215], s[24:25], 0, v[2:3]
	s_mov_b32 m0, s43
	s_nop 0
	global_load_lds_dwordx4 v[214:215], off
	s_mov_b32 m0, s44
	s_nop 0
	global_load_lds_dwordx4 v[216:217], off
	s_waitcnt vmcnt(8)
	s_waitcnt lgkmcnt(0)
	s_barrier
	s_setprio 1
	s_waitcnt lgkmcnt(0)
	v_mfma_f32_16x16x32_bf16 v[66:69], v[118:121], v[166:169], v[66:69]
	v_mfma_f32_16x16x32_bf16 v[62:65], v[130:133], v[166:169], v[62:65]
	v_mfma_f32_16x16x32_bf16 v[50:53], v[118:121], v[174:177], v[50:53]
	v_mfma_f32_16x16x32_bf16 v[46:49], v[130:133], v[174:177], v[46:49]
	v_mfma_f32_16x16x32_bf16 v[34:37], v[118:121], v[182:185], v[34:37]
	v_mfma_f32_16x16x32_bf16 v[30:33], v[130:133], v[182:185], v[30:33]
	v_mfma_f32_16x16x32_bf16 v[18:21], v[118:121], v[190:193], v[18:21]
	v_mfma_f32_16x16x32_bf16 v[14:17], v[130:133], v[190:193], v[14:17]
	v_mfma_f32_16x16x32_bf16 v[66:69], v[122:125], v[170:173], v[66:69]
	v_mfma_f32_16x16x32_bf16 v[62:65], v[138:141], v[170:173], v[62:65]
	v_mfma_f32_16x16x32_bf16 v[50:53], v[122:125], v[178:181], v[50:53]
	v_mfma_f32_16x16x32_bf16 v[46:49], v[138:141], v[178:181], v[46:49]
	v_mfma_f32_16x16x32_bf16 v[34:37], v[122:125], v[186:189], v[34:37]
	v_mfma_f32_16x16x32_bf16 v[30:33], v[138:141], v[186:189], v[30:33]
	v_mfma_f32_16x16x32_bf16 v[18:21], v[122:125], v[194:197], v[18:21]
	v_mfma_f32_16x16x32_bf16 v[14:17], v[138:141], v[194:197], v[14:17]
	s_setprio 0
	s_setprio 1
	v_mfma_f32_16x16x32_bf16 v[58:61], v[142:145], v[166:169], v[58:61]
	v_mfma_f32_16x16x32_bf16 v[54:57], v[154:157], v[166:169], v[54:57]
	v_mfma_f32_16x16x32_bf16 v[42:45], v[142:145], v[174:177], v[42:45]
	v_mfma_f32_16x16x32_bf16 v[38:41], v[154:157], v[174:177], v[38:41]
	v_mfma_f32_16x16x32_bf16 v[26:29], v[142:145], v[182:185], v[26:29]
	v_mfma_f32_16x16x32_bf16 v[22:25], v[154:157], v[182:185], v[22:25]
	v_mfma_f32_16x16x32_bf16 v[10:13], v[142:145], v[190:193], v[10:13]
	v_mfma_f32_16x16x32_bf16 v[6:9], v[154:157], v[190:193], v[6:9]
	v_mfma_f32_16x16x32_bf16 v[58:61], v[150:153], v[170:173], v[58:61]
	v_mfma_f32_16x16x32_bf16 v[54:57], v[162:165], v[170:173], v[54:57]
	v_mfma_f32_16x16x32_bf16 v[42:45], v[150:153], v[178:181], v[42:45]
	v_mfma_f32_16x16x32_bf16 v[38:41], v[162:165], v[178:181], v[38:41]
	v_mfma_f32_16x16x32_bf16 v[26:29], v[150:153], v[186:189], v[26:29]
	v_mfma_f32_16x16x32_bf16 v[22:25], v[162:165], v[186:189], v[22:25]
	s_setprio 2
	s_barrier
	v_mfma_f32_16x16x32_bf16 v[10:13], v[150:153], v[194:197], v[10:13]
	v_mfma_f32_16x16x32_bf16 v[6:9], v[162:165], v[194:197], v[6:9]
	s_setprio 0
	v_add_u32_e32 v138, s47, v241
	v_add_u32_e32 v162, s52, v241
	ds_read_b128 v[118:121], v138
	ds_read_b128 v[122:125], v138 offset:1024
	ds_read_b128 v[130:133], v138 offset:2048
	ds_read_b128 v[138:141], v138 offset:3072
	ds_read_b128 v[142:145], v162
	ds_read_b128 v[150:153], v162 offset:1024
	ds_read_b128 v[154:157], v162 offset:2048
	ds_read_b128 v[162:165], v162 offset:3072
	s_add_u32 s24, s24, 0x40000
	s_addc_u32 s25, s25, 0
	s_mov_b32 m0, s45
	v_lshl_add_u64 v[218:219], s[24:25], 0, v[2:3]
	ds_read_b128 v[166:169], v243 offset:32768
	ds_read_b128 v[170:173], v243 offset:33792
	ds_read_b128 v[174:177], v243 offset:34816
	ds_read_b128 v[178:181], v243 offset:35840
	ds_read_b128 v[182:185], v243 offset:36864
	ds_read_b128 v[186:189], v243 offset:37888
	ds_read_b128 v[190:193], v243 offset:38912
	ds_read_b128 v[194:197], v243 offset:39936
	global_load_lds_dwordx4 v[218:219], off
	v_lshl_add_u64 v[218:219], s[24:25], 0, v[206:207]
	s_mov_b32 m0, s46
	s_nop 0
	global_load_lds_dwordx4 v[218:219], off
	s_waitcnt vmcnt(8)
	s_waitcnt lgkmcnt(0)
	s_barrier
	s_setprio 1
	s_waitcnt lgkmcnt(0)
	v_mfma_f32_16x16x32_bf16 v[158:161], v[118:121], v[166:169], v[158:161]
	v_mfma_f32_16x16x32_bf16 v[146:149], v[130:133], v[166:169], v[146:149]
	v_mfma_f32_16x16x32_bf16 v[114:117], v[118:121], v[174:177], v[114:117]
	v_mfma_f32_16x16x32_bf16 v[110:113], v[130:133], v[174:177], v[110:113]
	v_mfma_f32_16x16x32_bf16 v[98:101], v[118:121], v[182:185], v[98:101]
	v_mfma_f32_16x16x32_bf16 v[94:97], v[130:133], v[182:185], v[94:97]
	v_mfma_f32_16x16x32_bf16 v[82:85], v[118:121], v[190:193], v[82:85]
	v_mfma_f32_16x16x32_bf16 v[78:81], v[130:133], v[190:193], v[78:81]
	v_mfma_f32_16x16x32_bf16 v[158:161], v[122:125], v[170:173], v[158:161]
	v_mfma_f32_16x16x32_bf16 v[146:149], v[138:141], v[170:173], v[146:149]
	v_mfma_f32_16x16x32_bf16 v[114:117], v[122:125], v[178:181], v[114:117]
	v_mfma_f32_16x16x32_bf16 v[110:113], v[138:141], v[178:181], v[110:113]
	v_mfma_f32_16x16x32_bf16 v[98:101], v[122:125], v[186:189], v[98:101]
	v_mfma_f32_16x16x32_bf16 v[94:97], v[138:141], v[186:189], v[94:97]
	v_mfma_f32_16x16x32_bf16 v[82:85], v[122:125], v[194:197], v[82:85]
	v_mfma_f32_16x16x32_bf16 v[78:81], v[138:141], v[194:197], v[78:81]
	s_setprio 0
	s_setprio 1
	v_mfma_f32_16x16x32_bf16 v[134:137], v[142:145], v[166:169], v[134:137]
	v_mfma_f32_16x16x32_bf16 v[126:129], v[154:157], v[166:169], v[126:129]
	v_mfma_f32_16x16x32_bf16 v[106:109], v[142:145], v[174:177], v[106:109]
	v_mfma_f32_16x16x32_bf16 v[102:105], v[154:157], v[174:177], v[102:105]
	v_mfma_f32_16x16x32_bf16 v[90:93], v[142:145], v[182:185], v[90:93]
	v_mfma_f32_16x16x32_bf16 v[86:89], v[154:157], v[182:185], v[86:89]
	v_mfma_f32_16x16x32_bf16 v[74:77], v[142:145], v[190:193], v[74:77]
	v_mfma_f32_16x16x32_bf16 v[70:73], v[154:157], v[190:193], v[70:73]
	v_mfma_f32_16x16x32_bf16 v[134:137], v[150:153], v[170:173], v[134:137]
	v_mfma_f32_16x16x32_bf16 v[126:129], v[162:165], v[170:173], v[126:129]
	v_mfma_f32_16x16x32_bf16 v[106:109], v[150:153], v[178:181], v[106:109]
	v_mfma_f32_16x16x32_bf16 v[102:105], v[162:165], v[178:181], v[102:105]
	v_mfma_f32_16x16x32_bf16 v[90:93], v[150:153], v[186:189], v[90:93]
	v_mfma_f32_16x16x32_bf16 v[86:89], v[162:165], v[186:189], v[86:89]
	s_setprio 2
	s_barrier
	v_mfma_f32_16x16x32_bf16 v[74:77], v[150:153], v[194:197], v[74:77]
	v_mfma_f32_16x16x32_bf16 v[70:73], v[162:165], v[194:197], v[70:73]
	s_setprio 0
	s_mov_b32 m0, s48
	v_lshl_add_u64 v[198:199], v[198:199], 0, s[28:29]
	s_add_u32 s22, s22, 0x40080
	ds_read_b128 v[166:169], v243 offset:49152
	ds_read_b128 v[170:173], v243 offset:50176
	ds_read_b128 v[174:177], v243 offset:51200
	ds_read_b128 v[178:181], v243 offset:52224
	ds_read_b128 v[182:185], v243 offset:53248
	ds_read_b128 v[186:189], v243 offset:54272
	ds_read_b128 v[190:193], v243 offset:55296
	ds_read_b128 v[194:197], v243 offset:56320
	global_load_lds_dwordx4 v[198:199], off
	v_lshl_add_u64 v[198:199], v[200:201], 0, s[28:29]
	s_mov_b32 m0, s49
	s_addc_u32 s23, s23, 0
	global_load_lds_dwordx4 v[198:199], off
	v_lshl_add_u64 v[198:199], s[22:23], 0, v[0:1]
	s_mov_b32 m0, s53
	s_nop 0
	global_load_lds_dwordx4 v[198:199], off
	v_lshl_add_u64 v[198:199], s[22:23], 0, v[208:209]
	s_mov_b32 m0, s54
	s_nop 0
	global_load_lds_dwordx4 v[198:199], off
	v_lshl_add_u64 v[198:199], v[214:215], 0, s[28:29]
	s_mov_b32 m0, s50
	s_nop 0
	global_load_lds_dwordx4 v[198:199], off
	v_lshl_add_u64 v[198:199], v[216:217], 0, s[28:29]
	s_mov_b32 m0, s51
	s_nop 0
	global_load_lds_dwordx4 v[198:199], off
	s_waitcnt vmcnt(8)
	s_waitcnt lgkmcnt(0)
	s_barrier
	s_setprio 1
	s_waitcnt lgkmcnt(0)
	v_mfma_f32_16x16x32_bf16 v[66:69], v[118:121], v[166:169], v[66:69]
	v_mfma_f32_16x16x32_bf16 v[62:65], v[130:133], v[166:169], v[62:65]
	v_mfma_f32_16x16x32_bf16 v[50:53], v[118:121], v[174:177], v[50:53]
	v_mfma_f32_16x16x32_bf16 v[46:49], v[130:133], v[174:177], v[46:49]
	v_mfma_f32_16x16x32_bf16 v[34:37], v[118:121], v[182:185], v[34:37]
	v_mfma_f32_16x16x32_bf16 v[30:33], v[130:133], v[182:185], v[30:33]
	v_mfma_f32_16x16x32_bf16 v[18:21], v[118:121], v[190:193], v[18:21]
	v_mfma_f32_16x16x32_bf16 v[14:17], v[130:133], v[190:193], v[14:17]
	v_mfma_f32_16x16x32_bf16 v[66:69], v[122:125], v[170:173], v[66:69]
	v_mfma_f32_16x16x32_bf16 v[62:65], v[138:141], v[170:173], v[62:65]
	v_mfma_f32_16x16x32_bf16 v[50:53], v[122:125], v[178:181], v[50:53]
	v_mfma_f32_16x16x32_bf16 v[46:49], v[138:141], v[178:181], v[46:49]
	v_mfma_f32_16x16x32_bf16 v[34:37], v[122:125], v[186:189], v[34:37]
	v_mfma_f32_16x16x32_bf16 v[30:33], v[138:141], v[186:189], v[30:33]
	v_mfma_f32_16x16x32_bf16 v[18:21], v[122:125], v[194:197], v[18:21]
	v_mfma_f32_16x16x32_bf16 v[14:17], v[138:141], v[194:197], v[14:17]
	s_setprio 0
	s_setprio 1
	v_mfma_f32_16x16x32_bf16 v[58:61], v[142:145], v[166:169], v[58:61]
	v_mfma_f32_16x16x32_bf16 v[54:57], v[154:157], v[166:169], v[54:57]
	v_mfma_f32_16x16x32_bf16 v[42:45], v[142:145], v[174:177], v[42:45]
	v_mfma_f32_16x16x32_bf16 v[38:41], v[154:157], v[174:177], v[38:41]
	v_mfma_f32_16x16x32_bf16 v[26:29], v[142:145], v[182:185], v[26:29]
	v_mfma_f32_16x16x32_bf16 v[22:25], v[154:157], v[182:185], v[22:25]
	v_mfma_f32_16x16x32_bf16 v[10:13], v[142:145], v[190:193], v[10:13]
	v_mfma_f32_16x16x32_bf16 v[6:9], v[154:157], v[190:193], v[6:9]
	v_mfma_f32_16x16x32_bf16 v[58:61], v[150:153], v[170:173], v[58:61]
	v_mfma_f32_16x16x32_bf16 v[54:57], v[162:165], v[170:173], v[54:57]
	v_mfma_f32_16x16x32_bf16 v[42:45], v[150:153], v[178:181], v[42:45]
	v_mfma_f32_16x16x32_bf16 v[38:41], v[162:165], v[178:181], v[38:41]
	v_mfma_f32_16x16x32_bf16 v[26:29], v[150:153], v[186:189], v[26:29]
	v_mfma_f32_16x16x32_bf16 v[22:25], v[162:165], v[186:189], v[22:25]
	s_setprio 2
	s_barrier
	v_mfma_f32_16x16x32_bf16 v[10:13], v[150:153], v[194:197], v[10:13]
	v_mfma_f32_16x16x32_bf16 v[6:9], v[162:165], v[194:197], v[6:9]
	s_setprio 0
	s_add_i32 s60, s60, 2
	s_add_u32 s58, s58, 0x100
	s_addc_u32 s59, s59, 0
	s_add_u32 s18, s18, 0x100
	s_addc_u32 s19, s19, 0
	s_cmp_gt_u32 s60, 13
	s_cbranch_scc0 .LBB0_1875
	s_and_b64 vcc, exec, s[8:9]
	s_cbranch_vccz .LBB0_1878
	s_barrier

.LBB0_1911:
	s_andn2_saveexec_b64 s[6:7], s[6:7]
	s_cbranch_execz .LBB0_1928
	v_cmp_lt_u32_e32 vcc, 1, v0
	s_and_saveexec_b64 s[6:7], vcc
	s_cbranch_execz .LBB0_1927
	buffer_wbl2 sc1
	s_waitcnt vmcnt(0)
	v_mov_b32_e32 v2, s2
	v_add_co_u32_e32 v2, vcc, 0x3000, v2
	v_mov_b32_e32 v3, s3
	s_nop 0
	v_addc_co_u32_e32 v3, vcc, 0, v3, vcc
	v_mov_b32_e32 v5, 1
	flat_atomic_add v2, v[2:3], v5 offset:1024 sc0
	v_cvt_f32_u32_e32 v3, v0
	v_sub_u32_e32 v5, 0, v0
	s_mov_b64 s[12:13], -1
	v_rcp_iflag_f32_e32 v3, v3
	s_nop 0
	v_mul_f32_e32 v3, 0x4f7ffffe, v3
	v_cvt_u32_f32_e32 v3, v3
	v_mul_lo_u32 v5, v5, v3
	v_mul_hi_u32 v5, v3, v5
	v_add_u32_e32 v3, v3, v5
	s_waitcnt vmcnt(0) lgkmcnt(0)
	v_mul_hi_u32 v3, v2, v3
	v_mul_lo_u32 v5, v3, v0
	v_sub_u32_e32 v5, v2, v5
	v_cmp_ge_u32_e32 vcc, v5, v0
	v_add_u32_e32 v6, 1, v3
	s_nop 0
	v_cndmask_b32_e32 v3, v3, v6, vcc
	v_sub_u32_e32 v6, v5, v0
	v_cndmask_b32_e32 v5, v5, v6, vcc
	v_cmp_ge_u32_e32 vcc, v5, v0
	v_add_u32_e32 v5, 1, v3
	v_add_u32_e32 v6, 1, v2
	v_cndmask_b32_e32 v5, v3, v5, vcc
	v_mad_u64_u32 v[2:3], s[8:9], v0, v5, v[0:1]
	s_add_u32 s8, s2, 0x3500
	s_addc_u32 s9, s3, 0
	v_cmp_ne_u32_e32 vcc, v6, v2
	v_mov_b64_e32 v[2:3], s[8:9]
	s_and_saveexec_b64 s[10:11], vcc
	s_cbranch_execz .LBB0_1925
	v_mov_b64_e32 v[2:3], s[8:9]
	flat_load_dword v0, v[2:3] sc1
	s_mov_b64 s[16:17], 0
	s_waitcnt vmcnt(0) lgkmcnt(0)
	v_cmp_eq_u32_e32 vcc, v0, v5
	s_and_saveexec_b64 s[14:15], vcc
	s_cbranch_execz .LBB0_1924
	s_add_u32 s12, s2, 0x200
	s_addc_u32 s13, s3, 0
	s_mov_b32 s34, 1
	s_mov_b64 s[2:3], 0
	s_branch .LBB0_1917

.LBB0_1951:
	v_add_u32_e32 v146, s31, v182
	v_add_u32_e32 v170, s40, v182
	ds_read_b128 v[134:137], v146
	ds_read_b128 v[138:141], v146 offset:1024
	ds_read_b128 v[142:145], v146 offset:2048
	ds_read_b128 v[146:149], v146 offset:3072
	ds_read_b128 v[150:153], v170
	ds_read_b128 v[154:157], v170 offset:1024
	ds_read_b128 v[158:161], v170 offset:2048
	ds_read_b128 v[170:173], v170 offset:3072
	s_add_u32 s22, s18, 0xfff80080
	s_addc_u32 s23, s19, -1
	s_cmp_eq_u32 s59, 28
	s_cselect_b32 s25, s9, s23
	s_cselect_b32 s24, s15, s22
	s_cselect_b32 s23, s7, s58
	s_cselect_b32 s22, s17, s26
	v_lshl_add_u64 v[214:215], s[18:19], 0, v[168:169]
	s_add_i32 m0, s43, 0xc000
	ds_read_b128 v[174:177], v184
	ds_read_b128 v[178:181], v184 offset:1024
	ds_read_b128 v[186:189], v184 offset:2048
	ds_read_b128 v[190:193], v184 offset:3072
	ds_read_b128 v[194:197], v184 offset:4096
	ds_read_b128 v[198:201], v184 offset:5120
	ds_read_b128 v[206:209], v184 offset:6144
	ds_read_b128 v[210:213], v184 offset:7168
	global_load_lds_dwordx4 v[214:215], off
	v_lshl_add_u64 v[214:215], s[18:19], 0, v[166:167]
	s_add_i32 m0, s43, 0xe000
	s_nop 0
	global_load_lds_dwordx4 v[214:215], off
	s_waitcnt vmcnt(8)
	s_waitcnt lgkmcnt(0)
	s_barrier
	s_setprio 1
	s_waitcnt lgkmcnt(0)
	v_mfma_f32_16x16x32_bf16 v[130:133], v[134:137], v[174:177], v[130:133]
	v_mfma_f32_16x16x32_bf16 v[126:129], v[142:145], v[174:177], v[126:129]
	v_mfma_f32_16x16x32_bf16 v[114:117], v[134:137], v[186:189], v[114:117]
	v_mfma_f32_16x16x32_bf16 v[110:113], v[142:145], v[186:189], v[110:113]
	v_mfma_f32_16x16x32_bf16 v[98:101], v[134:137], v[194:197], v[98:101]
	v_mfma_f32_16x16x32_bf16 v[94:97], v[142:145], v[194:197], v[94:97]
	v_mfma_f32_16x16x32_bf16 v[82:85], v[134:137], v[206:209], v[82:85]
	v_mfma_f32_16x16x32_bf16 v[78:81], v[142:145], v[206:209], v[78:81]
	v_mfma_f32_16x16x32_bf16 v[130:133], v[138:141], v[178:181], v[130:133]
	v_mfma_f32_16x16x32_bf16 v[126:129], v[146:149], v[178:181], v[126:129]
	v_mfma_f32_16x16x32_bf16 v[114:117], v[138:141], v[190:193], v[114:117]
	v_mfma_f32_16x16x32_bf16 v[110:113], v[146:149], v[190:193], v[110:113]
	v_mfma_f32_16x16x32_bf16 v[98:101], v[138:141], v[198:201], v[98:101]
	v_mfma_f32_16x16x32_bf16 v[94:97], v[146:149], v[198:201], v[94:97]
	v_mfma_f32_16x16x32_bf16 v[82:85], v[138:141], v[210:213], v[82:85]
	v_mfma_f32_16x16x32_bf16 v[78:81], v[146:149], v[210:213], v[78:81]
	s_setprio 0
	s_setprio 1
	v_mfma_f32_16x16x32_bf16 v[122:125], v[150:153], v[174:177], v[122:125]
	v_mfma_f32_16x16x32_bf16 v[118:121], v[158:161], v[174:177], v[118:121]
	v_mfma_f32_16x16x32_bf16 v[106:109], v[150:153], v[186:189], v[106:109]
	v_mfma_f32_16x16x32_bf16 v[102:105], v[158:161], v[186:189], v[102:105]
	v_mfma_f32_16x16x32_bf16 v[90:93], v[150:153], v[194:197], v[90:93]
	v_mfma_f32_16x16x32_bf16 v[86:89], v[158:161], v[194:197], v[86:89]
	v_mfma_f32_16x16x32_bf16 v[74:77], v[150:153], v[206:209], v[74:77]
	v_mfma_f32_16x16x32_bf16 v[70:73], v[158:161], v[206:209], v[70:73]
	v_mfma_f32_16x16x32_bf16 v[122:125], v[154:157], v[178:181], v[122:125]
	v_mfma_f32_16x16x32_bf16 v[118:121], v[170:173], v[178:181], v[118:121]
	v_mfma_f32_16x16x32_bf16 v[106:109], v[154:157], v[190:193], v[106:109]
	v_mfma_f32_16x16x32_bf16 v[102:105], v[170:173], v[190:193], v[102:105]
	v_mfma_f32_16x16x32_bf16 v[90:93], v[154:157], v[198:201], v[90:93]
	v_mfma_f32_16x16x32_bf16 v[86:89], v[170:173], v[198:201], v[86:89]
	s_setprio 2
	s_barrier
	v_mfma_f32_16x16x32_bf16 v[74:77], v[154:157], v[210:213], v[74:77]
	v_mfma_f32_16x16x32_bf16 v[70:73], v[170:173], v[210:213], v[70:73]
	s_setprio 0
	s_mov_b32 m0, s34
	v_lshl_add_u64 v[214:215], s[22:23], 0, v[0:1]
	s_add_u32 s60, s22, 0x80000
	ds_read_b128 v[174:177], v184 offset:16384
	ds_read_b128 v[178:181], v184 offset:17408
	ds_read_b128 v[186:189], v184 offset:18432
	ds_read_b128 v[190:193], v184 offset:19456
	ds_read_b128 v[194:197], v184 offset:20480
	ds_read_b128 v[198:201], v184 offset:21504
	ds_read_b128 v[206:209], v184 offset:22528
	ds_read_b128 v[210:213], v184 offset:23552
	global_load_lds_dwordx4 v[214:215], off
	v_lshl_add_u64 v[216:217], s[22:23], 0, v[164:165]
	s_mov_b32 m0, s35
	s_addc_u32 s61, s23, 0
	global_load_lds_dwordx4 v[216:217], off
	v_lshl_add_u64 v[218:219], s[60:61], 0, v[0:1]
	s_mov_b32 m0, s41
	v_lshl_add_u64 v[220:221], s[24:25], 0, v[162:163]
	global_load_lds_dwordx4 v[218:219], off
	v_lshl_add_u64 v[218:219], s[60:61], 0, v[164:165]
	s_mov_b32 m0, s42
	s_nop 0
	global_load_lds_dwordx4 v[218:219], off
	v_lshl_add_u64 v[218:219], s[24:25], 0, v[2:3]
	s_mov_b32 m0, s43
	s_nop 0
	global_load_lds_dwordx4 v[218:219], off
	s_mov_b32 m0, s44
	s_nop 0
	global_load_lds_dwordx4 v[220:221], off
	s_waitcnt vmcnt(8)
	s_waitcnt lgkmcnt(0)
	s_barrier
	s_setprio 1
	s_waitcnt lgkmcnt(0)
	v_mfma_f32_16x16x32_bf16 v[66:69], v[134:137], v[174:177], v[66:69]
	v_mfma_f32_16x16x32_bf16 v[62:65], v[142:145], v[174:177], v[62:65]
	v_mfma_f32_16x16x32_bf16 v[50:53], v[134:137], v[186:189], v[50:53]
	v_mfma_f32_16x16x32_bf16 v[46:49], v[142:145], v[186:189], v[46:49]
	v_mfma_f32_16x16x32_bf16 v[34:37], v[134:137], v[194:197], v[34:37]
	v_mfma_f32_16x16x32_bf16 v[30:33], v[142:145], v[194:197], v[30:33]
	v_mfma_f32_16x16x32_bf16 v[18:21], v[134:137], v[206:209], v[18:21]
	v_mfma_f32_16x16x32_bf16 v[14:17], v[142:145], v[206:209], v[14:17]
	v_mfma_f32_16x16x32_bf16 v[66:69], v[138:141], v[178:181], v[66:69]
	v_mfma_f32_16x16x32_bf16 v[62:65], v[146:149], v[178:181], v[62:65]
	v_mfma_f32_16x16x32_bf16 v[50:53], v[138:141], v[190:193], v[50:53]
	v_mfma_f32_16x16x32_bf16 v[46:49], v[146:149], v[190:193], v[46:49]
	v_mfma_f32_16x16x32_bf16 v[34:37], v[138:141], v[198:201], v[34:37]
	v_mfma_f32_16x16x32_bf16 v[30:33], v[146:149], v[198:201], v[30:33]
	v_mfma_f32_16x16x32_bf16 v[18:21], v[138:141], v[210:213], v[18:21]
	v_mfma_f32_16x16x32_bf16 v[14:17], v[146:149], v[210:213], v[14:17]
	s_setprio 0
	s_setprio 1
	v_mfma_f32_16x16x32_bf16 v[58:61], v[150:153], v[174:177], v[58:61]
	v_mfma_f32_16x16x32_bf16 v[54:57], v[158:161], v[174:177], v[54:57]
	v_mfma_f32_16x16x32_bf16 v[42:45], v[150:153], v[186:189], v[42:45]
	v_mfma_f32_16x16x32_bf16 v[38:41], v[158:161], v[186:189], v[38:41]
	v_mfma_f32_16x16x32_bf16 v[26:29], v[150:153], v[194:197], v[26:29]
	v_mfma_f32_16x16x32_bf16 v[22:25], v[158:161], v[194:197], v[22:25]
	v_mfma_f32_16x16x32_bf16 v[10:13], v[150:153], v[206:209], v[10:13]
	v_mfma_f32_16x16x32_bf16 v[6:9], v[158:161], v[206:209], v[6:9]
	v_mfma_f32_16x16x32_bf16 v[58:61], v[154:157], v[178:181], v[58:61]
	v_mfma_f32_16x16x32_bf16 v[54:57], v[170:173], v[178:181], v[54:57]
	v_mfma_f32_16x16x32_bf16 v[42:45], v[154:157], v[190:193], v[42:45]
	v_mfma_f32_16x16x32_bf16 v[38:41], v[170:173], v[190:193], v[38:41]
	v_mfma_f32_16x16x32_bf16 v[26:29], v[154:157], v[198:201], v[26:29]
	v_mfma_f32_16x16x32_bf16 v[22:25], v[170:173], v[198:201], v[22:25]
	s_setprio 2
	s_barrier
	v_mfma_f32_16x16x32_bf16 v[10:13], v[154:157], v[210:213], v[10:13]
	v_mfma_f32_16x16x32_bf16 v[6:9], v[170:173], v[210:213], v[6:9]
	s_setprio 0
	v_add_u32_e32 v146, s48, v182
	v_add_u32_e32 v170, s53, v182
	ds_read_b128 v[134:137], v146
	ds_read_b128 v[138:141], v146 offset:1024
	ds_read_b128 v[142:145], v146 offset:2048
	ds_read_b128 v[146:149], v146 offset:3072
	ds_read_b128 v[150:153], v170
	ds_read_b128 v[154:157], v170 offset:1024
	ds_read_b128 v[158:161], v170 offset:2048
	ds_read_b128 v[170:173], v170 offset:3072
	s_add_u32 s24, s24, 0x80000
	s_addc_u32 s25, s25, 0
	s_mov_b32 m0, s45
	v_lshl_add_u64 v[222:223], s[24:25], 0, v[2:3]
	ds_read_b128 v[174:177], v184 offset:32768
	ds_read_b128 v[178:181], v184 offset:33792
	ds_read_b128 v[186:189], v184 offset:34816
	ds_read_b128 v[190:193], v184 offset:35840
	ds_read_b128 v[194:197], v184 offset:36864
	ds_read_b128 v[198:201], v184 offset:37888
	ds_read_b128 v[206:209], v184 offset:38912
	ds_read_b128 v[210:213], v184 offset:39936
	global_load_lds_dwordx4 v[222:223], off
	v_lshl_add_u64 v[222:223], s[24:25], 0, v[162:163]
	s_mov_b32 m0, s46
	s_nop 0
	global_load_lds_dwordx4 v[222:223], off
	s_waitcnt vmcnt(8)
	s_waitcnt lgkmcnt(0)
	s_barrier
	s_setprio 1
	s_waitcnt lgkmcnt(0)
	v_mfma_f32_16x16x32_bf16 v[130:133], v[134:137], v[174:177], v[130:133]
	v_mfma_f32_16x16x32_bf16 v[126:129], v[142:145], v[174:177], v[126:129]
	v_mfma_f32_16x16x32_bf16 v[114:117], v[134:137], v[186:189], v[114:117]
	v_mfma_f32_16x16x32_bf16 v[110:113], v[142:145], v[186:189], v[110:113]
	v_mfma_f32_16x16x32_bf16 v[98:101], v[134:137], v[194:197], v[98:101]
	v_mfma_f32_16x16x32_bf16 v[94:97], v[142:145], v[194:197], v[94:97]
	v_mfma_f32_16x16x32_bf16 v[82:85], v[134:137], v[206:209], v[82:85]
	v_mfma_f32_16x16x32_bf16 v[78:81], v[142:145], v[206:209], v[78:81]
	v_mfma_f32_16x16x32_bf16 v[130:133], v[138:141], v[178:181], v[130:133]
	v_mfma_f32_16x16x32_bf16 v[126:129], v[146:149], v[178:181], v[126:129]
	v_mfma_f32_16x16x32_bf16 v[114:117], v[138:141], v[190:193], v[114:117]
	v_mfma_f32_16x16x32_bf16 v[110:113], v[146:149], v[190:193], v[110:113]
	v_mfma_f32_16x16x32_bf16 v[98:101], v[138:141], v[198:201], v[98:101]
	v_mfma_f32_16x16x32_bf16 v[94:97], v[146:149], v[198:201], v[94:97]
	v_mfma_f32_16x16x32_bf16 v[82:85], v[138:141], v[210:213], v[82:85]
	v_mfma_f32_16x16x32_bf16 v[78:81], v[146:149], v[210:213], v[78:81]
	s_setprio 0
	s_setprio 1
	v_mfma_f32_16x16x32_bf16 v[122:125], v[150:153], v[174:177], v[122:125]
	v_mfma_f32_16x16x32_bf16 v[118:121], v[158:161], v[174:177], v[118:121]
	v_mfma_f32_16x16x32_bf16 v[106:109], v[150:153], v[186:189], v[106:109]
	v_mfma_f32_16x16x32_bf16 v[102:105], v[158:161], v[186:189], v[102:105]
	v_mfma_f32_16x16x32_bf16 v[90:93], v[150:153], v[194:197], v[90:93]
	v_mfma_f32_16x16x32_bf16 v[86:89], v[158:161], v[194:197], v[86:89]
	v_mfma_f32_16x16x32_bf16 v[74:77], v[150:153], v[206:209], v[74:77]
	v_mfma_f32_16x16x32_bf16 v[70:73], v[158:161], v[206:209], v[70:73]
	v_mfma_f32_16x16x32_bf16 v[122:125], v[154:157], v[178:181], v[122:125]
	v_mfma_f32_16x16x32_bf16 v[118:121], v[170:173], v[178:181], v[118:121]
	v_mfma_f32_16x16x32_bf16 v[106:109], v[154:157], v[190:193], v[106:109]
	v_mfma_f32_16x16x32_bf16 v[102:105], v[170:173], v[190:193], v[102:105]
	v_mfma_f32_16x16x32_bf16 v[90:93], v[154:157], v[198:201], v[90:93]
	v_mfma_f32_16x16x32_bf16 v[86:89], v[170:173], v[198:201], v[86:89]
	s_setprio 2
	s_barrier
	v_mfma_f32_16x16x32_bf16 v[74:77], v[154:157], v[210:213], v[74:77]
	v_mfma_f32_16x16x32_bf16 v[70:73], v[170:173], v[210:213], v[70:73]
	s_setprio 0
	s_mov_b32 m0, s49
	v_lshl_add_u64 v[214:215], v[214:215], 0, s[28:29]
	s_add_u32 s22, s22, 0x80080
	ds_read_b128 v[174:177], v184 offset:49152
	ds_read_b128 v[178:181], v184 offset:50176
	ds_read_b128 v[186:189], v184 offset:51200
	ds_read_b128 v[190:193], v184 offset:52224
	ds_read_b128 v[194:197], v184 offset:53248
	ds_read_b128 v[198:201], v184 offset:54272
	ds_read_b128 v[206:209], v184 offset:55296
	ds_read_b128 v[210:213], v184 offset:56320
	global_load_lds_dwordx4 v[214:215], off
	v_lshl_add_u64 v[214:215], v[216:217], 0, s[28:29]
	s_mov_b32 m0, s50
	s_addc_u32 s23, s23, 0
	global_load_lds_dwordx4 v[214:215], off
	v_lshl_add_u64 v[214:215], s[22:23], 0, v[0:1]
	s_mov_b32 m0, s54
	s_nop 0
	global_load_lds_dwordx4 v[214:215], off
	v_lshl_add_u64 v[214:215], s[22:23], 0, v[164:165]
	s_mov_b32 m0, s55
	s_nop 0
	global_load_lds_dwordx4 v[214:215], off
	v_lshl_add_u64 v[214:215], v[218:219], 0, s[28:29]
	s_mov_b32 m0, s51
	s_nop 0
	global_load_lds_dwordx4 v[214:215], off
	v_lshl_add_u64 v[214:215], v[220:221], 0, s[28:29]
	s_mov_b32 m0, s52
	s_nop 0
	global_load_lds_dwordx4 v[214:215], off
	s_waitcnt vmcnt(8)
	s_waitcnt lgkmcnt(0)
	s_barrier
	s_setprio 1
	s_waitcnt lgkmcnt(0)
	v_mfma_f32_16x16x32_bf16 v[66:69], v[134:137], v[174:177], v[66:69]
	v_mfma_f32_16x16x32_bf16 v[62:65], v[142:145], v[174:177], v[62:65]
	v_mfma_f32_16x16x32_bf16 v[50:53], v[134:137], v[186:189], v[50:53]
	v_mfma_f32_16x16x32_bf16 v[46:49], v[142:145], v[186:189], v[46:49]
	v_mfma_f32_16x16x32_bf16 v[34:37], v[134:137], v[194:197], v[34:37]
	v_mfma_f32_16x16x32_bf16 v[30:33], v[142:145], v[194:197], v[30:33]
	v_mfma_f32_16x16x32_bf16 v[18:21], v[134:137], v[206:209], v[18:21]
	v_mfma_f32_16x16x32_bf16 v[14:17], v[142:145], v[206:209], v[14:17]
	v_mfma_f32_16x16x32_bf16 v[66:69], v[138:141], v[178:181], v[66:69]
	v_mfma_f32_16x16x32_bf16 v[62:65], v[146:149], v[178:181], v[62:65]
	v_mfma_f32_16x16x32_bf16 v[50:53], v[138:141], v[190:193], v[50:53]
	v_mfma_f32_16x16x32_bf16 v[46:49], v[146:149], v[190:193], v[46:49]
	v_mfma_f32_16x16x32_bf16 v[34:37], v[138:141], v[198:201], v[34:37]
	v_mfma_f32_16x16x32_bf16 v[30:33], v[146:149], v[198:201], v[30:33]
	v_mfma_f32_16x16x32_bf16 v[18:21], v[138:141], v[210:213], v[18:21]
	v_mfma_f32_16x16x32_bf16 v[14:17], v[146:149], v[210:213], v[14:17]
	s_setprio 0
	s_setprio 1
	v_mfma_f32_16x16x32_bf16 v[58:61], v[150:153], v[174:177], v[58:61]
	v_mfma_f32_16x16x32_bf16 v[54:57], v[158:161], v[174:177], v[54:57]
	v_mfma_f32_16x16x32_bf16 v[42:45], v[150:153], v[186:189], v[42:45]
	v_mfma_f32_16x16x32_bf16 v[38:41], v[158:161], v[186:189], v[38:41]
	v_mfma_f32_16x16x32_bf16 v[26:29], v[150:153], v[194:197], v[26:29]
	v_mfma_f32_16x16x32_bf16 v[22:25], v[158:161], v[194:197], v[22:25]
	v_mfma_f32_16x16x32_bf16 v[10:13], v[150:153], v[206:209], v[10:13]
	v_mfma_f32_16x16x32_bf16 v[6:9], v[158:161], v[206:209], v[6:9]
	v_mfma_f32_16x16x32_bf16 v[58:61], v[154:157], v[178:181], v[58:61]
	v_mfma_f32_16x16x32_bf16 v[54:57], v[170:173], v[178:181], v[54:57]
	v_mfma_f32_16x16x32_bf16 v[42:45], v[154:157], v[190:193], v[42:45]
	v_mfma_f32_16x16x32_bf16 v[38:41], v[170:173], v[190:193], v[38:41]
	v_mfma_f32_16x16x32_bf16 v[26:29], v[154:157], v[198:201], v[26:29]
	v_mfma_f32_16x16x32_bf16 v[22:25], v[170:173], v[198:201], v[22:25]
	s_setprio 2
	s_barrier
	v_mfma_f32_16x16x32_bf16 v[10:13], v[154:157], v[210:213], v[10:13]
	v_mfma_f32_16x16x32_bf16 v[6:9], v[170:173], v[210:213], v[6:9]
	s_setprio 0
	s_add_i32 s59, s59, 2
	s_add_u32 s26, s26, 0x100
	s_addc_u32 s58, s58, 0
	s_add_u32 s18, s18, 0x100
	s_addc_u32 s19, s19, 0
	s_cmp_gt_u32 s59, 29
	s_cbranch_scc0 .LBB0_1951
	s_and_b64 vcc, exec, s[2:3]
	s_cbranch_vccz .LBB0_1954
	s_barrier

.LBB0_2003:
	s_andn2_saveexec_b64 s[4:5], s[4:5]
	s_cbranch_execz .LBB0_2020
	v_cmp_lt_u32_e32 vcc, 1, v0
	s_and_saveexec_b64 s[4:5], vcc
	s_cbranch_execz .LBB0_2019
	buffer_wbl2 sc1
	s_waitcnt vmcnt(0)
	v_mov_b32_e32 v2, s2
	v_add_co_u32_e32 v2, vcc, 0x3000, v2
	v_mov_b32_e32 v3, s3
	s_nop 0
	v_addc_co_u32_e32 v3, vcc, 0, v3, vcc
	v_mov_b32_e32 v5, 1
	flat_atomic_add v2, v[2:3], v5 offset:1024 sc0
	v_cvt_f32_u32_e32 v3, v0
	v_sub_u32_e32 v5, 0, v0
	s_mov_b64 s[10:11], -1
	v_rcp_iflag_f32_e32 v3, v3
	s_nop 0
	v_mul_f32_e32 v3, 0x4f7ffffe, v3
	v_cvt_u32_f32_e32 v3, v3
	v_mul_lo_u32 v5, v5, v3
	v_mul_hi_u32 v5, v3, v5
	v_add_u32_e32 v3, v3, v5
	s_waitcnt vmcnt(0) lgkmcnt(0)
	v_mul_hi_u32 v3, v2, v3
	v_mul_lo_u32 v5, v3, v0
	v_sub_u32_e32 v5, v2, v5
	v_cmp_ge_u32_e32 vcc, v5, v0
	v_add_u32_e32 v6, 1, v3
	s_nop 0
	v_cndmask_b32_e32 v3, v3, v6, vcc
	v_sub_u32_e32 v6, v5, v0
	v_cndmask_b32_e32 v5, v5, v6, vcc
	v_cmp_ge_u32_e32 vcc, v5, v0
	v_add_u32_e32 v5, 1, v3
	v_add_u32_e32 v6, 1, v2
	v_cndmask_b32_e32 v5, v3, v5, vcc
	v_mad_u64_u32 v[2:3], s[6:7], v0, v5, v[0:1]
	s_add_u32 s6, s2, 0x3500
	s_addc_u32 s7, s3, 0
	v_cmp_ne_u32_e32 vcc, v6, v2
	v_mov_b64_e32 v[2:3], s[6:7]
	s_and_saveexec_b64 s[8:9], vcc
	s_cbranch_execz .LBB0_2017
	v_mov_b64_e32 v[2:3], s[6:7]
	flat_load_dword v0, v[2:3] sc1
	s_mov_b64 s[14:15], 0
	s_waitcnt vmcnt(0) lgkmcnt(0)
	v_cmp_eq_u32_e32 vcc, v0, v5
	s_and_saveexec_b64 s[12:13], vcc
	s_cbranch_execz .LBB0_2016
	s_add_u32 s10, s2, 0x200
	s_addc_u32 s11, s3, 0
	s_mov_b32 s30, 1
	s_mov_b64 s[2:3], 0
	s_branch .LBB0_2009

.LBB0_2035:
	v_add_u32_e32 v142, s15, v144
	ds_read_b128 v[148:151], v142
	ds_read_b128 v[152:155], v142 offset:1024
	ds_read_b128 v[156:159], v142 offset:2048
	ds_read_b128 v[160:163], v142 offset:3072
	v_add_u32_e32 v142, s31, v144
	ds_read_b128 v[164:167], v142
	ds_read_b128 v[168:171], v142 offset:1024
	ds_read_b128 v[172:175], v142 offset:2048
	ds_read_b128 v[176:179], v142 offset:3072
	s_add_u32 s18, s16, 0xfff80080
	s_addc_u32 s19, s17, -1
	s_cmp_eq_u32 s54, 28
	s_cselect_b32 s23, s9, s19
	s_cselect_b32 s22, s50, s18
	s_cselect_b32 s19, s7, s53
	s_cselect_b32 s18, s51, s52
	v_lshl_add_u64 v[142:143], s[16:17], 0, v[140:141]
	s_add_i32 m0, s36, 0xc000
	ds_read_b128 v[180:183], v147
	ds_read_b128 v[184:187], v147 offset:1024
	ds_read_b128 v[188:191], v147 offset:2048
	ds_read_b128 v[192:195], v147 offset:3072
	ds_read_b128 v[196:199], v147 offset:4096
	ds_read_b128 v[206:209], v147 offset:5120
	ds_read_b128 v[210:213], v147 offset:6144
	ds_read_b128 v[214:217], v147 offset:7168
	global_load_lds_dwordx4 v[142:143], off
	v_lshl_add_u64 v[142:143], s[16:17], 0, v[138:139]
	s_add_i32 m0, s36, 0xe000
	s_nop 0
	global_load_lds_dwordx4 v[142:143], off
	s_waitcnt vmcnt(8)
	s_waitcnt lgkmcnt(0)
	s_barrier
	s_setprio 1
	s_waitcnt lgkmcnt(0)
	v_mfma_f32_16x16x32_bf16 v[130:133], v[148:151], v[180:183], v[130:133]
	v_mfma_f32_16x16x32_bf16 v[122:125], v[156:159], v[180:183], v[122:125]
	v_mfma_f32_16x16x32_bf16 v[114:117], v[148:151], v[188:191], v[114:117]
	v_mfma_f32_16x16x32_bf16 v[106:109], v[156:159], v[188:191], v[106:109]
	v_mfma_f32_16x16x32_bf16 v[98:101], v[148:151], v[196:199], v[98:101]
	v_mfma_f32_16x16x32_bf16 v[90:93], v[156:159], v[196:199], v[90:93]
	v_mfma_f32_16x16x32_bf16 v[82:85], v[148:151], v[210:213], v[82:85]
	v_mfma_f32_16x16x32_bf16 v[74:77], v[156:159], v[210:213], v[74:77]
	v_mfma_f32_16x16x32_bf16 v[130:133], v[152:155], v[184:187], v[130:133]
	v_mfma_f32_16x16x32_bf16 v[122:125], v[160:163], v[184:187], v[122:125]
	v_mfma_f32_16x16x32_bf16 v[114:117], v[152:155], v[192:195], v[114:117]
	v_mfma_f32_16x16x32_bf16 v[106:109], v[160:163], v[192:195], v[106:109]
	v_mfma_f32_16x16x32_bf16 v[98:101], v[152:155], v[206:209], v[98:101]
	v_mfma_f32_16x16x32_bf16 v[90:93], v[160:163], v[206:209], v[90:93]
	v_mfma_f32_16x16x32_bf16 v[82:85], v[152:155], v[214:217], v[82:85]
	v_mfma_f32_16x16x32_bf16 v[74:77], v[160:163], v[214:217], v[74:77]
	s_setprio 0
	s_setprio 1
	v_mfma_f32_16x16x32_bf16 v[126:129], v[164:167], v[180:183], v[126:129]
	v_mfma_f32_16x16x32_bf16 v[118:121], v[172:175], v[180:183], v[118:121]
	v_mfma_f32_16x16x32_bf16 v[110:113], v[164:167], v[188:191], v[110:113]
	v_mfma_f32_16x16x32_bf16 v[102:105], v[172:175], v[188:191], v[102:105]
	v_mfma_f32_16x16x32_bf16 v[94:97], v[164:167], v[196:199], v[94:97]
	v_mfma_f32_16x16x32_bf16 v[86:89], v[172:175], v[196:199], v[86:89]
	v_mfma_f32_16x16x32_bf16 v[78:81], v[164:167], v[210:213], v[78:81]
	v_mfma_f32_16x16x32_bf16 v[70:73], v[172:175], v[210:213], v[70:73]
	v_mfma_f32_16x16x32_bf16 v[126:129], v[168:171], v[184:187], v[126:129]
	v_mfma_f32_16x16x32_bf16 v[118:121], v[176:179], v[184:187], v[118:121]
	v_mfma_f32_16x16x32_bf16 v[110:113], v[168:171], v[192:195], v[110:113]
	v_mfma_f32_16x16x32_bf16 v[102:105], v[176:179], v[192:195], v[102:105]
	v_mfma_f32_16x16x32_bf16 v[94:97], v[168:171], v[206:209], v[94:97]
	v_mfma_f32_16x16x32_bf16 v[86:89], v[176:179], v[206:209], v[86:89]
	s_setprio 2
	s_barrier
	v_mfma_f32_16x16x32_bf16 v[78:81], v[168:171], v[214:217], v[78:81]
	v_mfma_f32_16x16x32_bf16 v[70:73], v[176:179], v[214:217], v[70:73]
	s_setprio 0
	s_mov_b32 m0, s26
	v_lshl_add_u64 v[142:143], s[18:19], 0, v[0:1]
	s_add_u32 s56, s18, 0x80000
	ds_read_b128 v[180:183], v147 offset:16384
	ds_read_b128 v[184:187], v147 offset:17408
	ds_read_b128 v[188:191], v147 offset:18432
	ds_read_b128 v[192:195], v147 offset:19456
	ds_read_b128 v[196:199], v147 offset:20480
	ds_read_b128 v[206:209], v147 offset:21504
	ds_read_b128 v[210:213], v147 offset:22528
	ds_read_b128 v[214:217], v147 offset:23552
	global_load_lds_dwordx4 v[142:143], off
	v_lshl_add_u64 v[200:201], s[18:19], 0, v[2:3]
	s_mov_b32 m0, s30
	s_addc_u32 s57, s19, 0
	global_load_lds_dwordx4 v[200:201], off
	v_lshl_add_u64 v[218:219], s[56:57], 0, v[0:1]
	s_mov_b32 m0, s34
	v_lshl_add_u64 v[220:221], s[22:23], 0, v[134:135]
	global_load_lds_dwordx4 v[218:219], off
	v_lshl_add_u64 v[218:219], s[56:57], 0, v[2:3]
	s_mov_b32 m0, s35
	s_nop 0
	global_load_lds_dwordx4 v[218:219], off
	v_lshl_add_u64 v[218:219], s[22:23], 0, v[136:137]
	s_mov_b32 m0, s36
	s_nop 0
	global_load_lds_dwordx4 v[218:219], off
	s_mov_b32 m0, s37
	s_nop 0
	global_load_lds_dwordx4 v[220:221], off
	s_waitcnt vmcnt(8)
	s_waitcnt lgkmcnt(0)
	s_barrier
	s_setprio 1
	s_waitcnt lgkmcnt(0)
	v_mfma_f32_16x16x32_bf16 v[66:69], v[148:151], v[180:183], v[66:69]
	v_mfma_f32_16x16x32_bf16 v[58:61], v[156:159], v[180:183], v[58:61]
	v_mfma_f32_16x16x32_bf16 v[50:53], v[148:151], v[188:191], v[50:53]
	v_mfma_f32_16x16x32_bf16 v[42:45], v[156:159], v[188:191], v[42:45]
	v_mfma_f32_16x16x32_bf16 v[34:37], v[148:151], v[196:199], v[34:37]
	v_mfma_f32_16x16x32_bf16 v[26:29], v[156:159], v[196:199], v[26:29]
	v_mfma_f32_16x16x32_bf16 v[18:21], v[148:151], v[210:213], v[18:21]
	v_mfma_f32_16x16x32_bf16 v[10:13], v[156:159], v[210:213], v[10:13]
	v_mfma_f32_16x16x32_bf16 v[66:69], v[152:155], v[184:187], v[66:69]
	v_mfma_f32_16x16x32_bf16 v[58:61], v[160:163], v[184:187], v[58:61]
	v_mfma_f32_16x16x32_bf16 v[50:53], v[152:155], v[192:195], v[50:53]
	v_mfma_f32_16x16x32_bf16 v[42:45], v[160:163], v[192:195], v[42:45]
	v_mfma_f32_16x16x32_bf16 v[34:37], v[152:155], v[206:209], v[34:37]
	v_mfma_f32_16x16x32_bf16 v[26:29], v[160:163], v[206:209], v[26:29]
	v_mfma_f32_16x16x32_bf16 v[18:21], v[152:155], v[214:217], v[18:21]
	v_mfma_f32_16x16x32_bf16 v[10:13], v[160:163], v[214:217], v[10:13]
	s_setprio 0
	s_setprio 1
	v_mfma_f32_16x16x32_bf16 v[62:65], v[164:167], v[180:183], v[62:65]
	v_mfma_f32_16x16x32_bf16 v[54:57], v[172:175], v[180:183], v[54:57]
	v_mfma_f32_16x16x32_bf16 v[46:49], v[164:167], v[188:191], v[46:49]
	v_mfma_f32_16x16x32_bf16 v[38:41], v[172:175], v[188:191], v[38:41]
	v_mfma_f32_16x16x32_bf16 v[30:33], v[164:167], v[196:199], v[30:33]
	v_mfma_f32_16x16x32_bf16 v[22:25], v[172:175], v[196:199], v[22:25]
	v_mfma_f32_16x16x32_bf16 v[14:17], v[164:167], v[210:213], v[14:17]
	v_mfma_f32_16x16x32_bf16 v[6:9], v[172:175], v[210:213], v[6:9]
	v_mfma_f32_16x16x32_bf16 v[62:65], v[168:171], v[184:187], v[62:65]
	v_mfma_f32_16x16x32_bf16 v[54:57], v[176:179], v[184:187], v[54:57]
	v_mfma_f32_16x16x32_bf16 v[46:49], v[168:171], v[192:195], v[46:49]
	v_mfma_f32_16x16x32_bf16 v[38:41], v[176:179], v[192:195], v[38:41]
	v_mfma_f32_16x16x32_bf16 v[30:33], v[168:171], v[206:209], v[30:33]
	v_mfma_f32_16x16x32_bf16 v[22:25], v[176:179], v[206:209], v[22:25]
	s_setprio 2
	s_barrier
	v_mfma_f32_16x16x32_bf16 v[14:17], v[168:171], v[214:217], v[14:17]
	v_mfma_f32_16x16x32_bf16 v[6:9], v[176:179], v[214:217], v[6:9]
	s_setprio 0
	v_add_u32_e32 v160, s40, v144
	v_add_u32_e32 v176, s45, v144
	ds_read_b128 v[148:151], v160
	ds_read_b128 v[152:155], v160 offset:1024
	ds_read_b128 v[156:159], v160 offset:2048
	ds_read_b128 v[160:163], v160 offset:3072
	ds_read_b128 v[164:167], v176
	ds_read_b128 v[168:171], v176 offset:1024
	ds_read_b128 v[172:175], v176 offset:2048
	ds_read_b128 v[176:179], v176 offset:3072
	s_add_u32 s22, s22, 0x80000
	s_addc_u32 s23, s23, 0
	s_mov_b32 m0, s38
	v_lshl_add_u64 v[222:223], s[22:23], 0, v[136:137]
	ds_read_b128 v[180:183], v147 offset:32768
	ds_read_b128 v[184:187], v147 offset:33792
	ds_read_b128 v[188:191], v147 offset:34816
	ds_read_b128 v[192:195], v147 offset:35840
	ds_read_b128 v[196:199], v147 offset:36864
	ds_read_b128 v[206:209], v147 offset:37888
	ds_read_b128 v[210:213], v147 offset:38912
	ds_read_b128 v[214:217], v147 offset:39936
	global_load_lds_dwordx4 v[222:223], off
	v_lshl_add_u64 v[222:223], s[22:23], 0, v[134:135]
	s_mov_b32 m0, s39
	s_nop 0
	global_load_lds_dwordx4 v[222:223], off
	s_waitcnt vmcnt(8)
	s_waitcnt lgkmcnt(0)
	s_barrier
	s_setprio 1
	s_waitcnt lgkmcnt(0)
	v_mfma_f32_16x16x32_bf16 v[130:133], v[148:151], v[180:183], v[130:133]
	v_mfma_f32_16x16x32_bf16 v[122:125], v[156:159], v[180:183], v[122:125]
	v_mfma_f32_16x16x32_bf16 v[114:117], v[148:151], v[188:191], v[114:117]
	v_mfma_f32_16x16x32_bf16 v[106:109], v[156:159], v[188:191], v[106:109]
	v_mfma_f32_16x16x32_bf16 v[98:101], v[148:151], v[196:199], v[98:101]
	v_mfma_f32_16x16x32_bf16 v[90:93], v[156:159], v[196:199], v[90:93]
	v_mfma_f32_16x16x32_bf16 v[82:85], v[148:151], v[210:213], v[82:85]
	v_mfma_f32_16x16x32_bf16 v[74:77], v[156:159], v[210:213], v[74:77]
	v_mfma_f32_16x16x32_bf16 v[130:133], v[152:155], v[184:187], v[130:133]
	v_mfma_f32_16x16x32_bf16 v[122:125], v[160:163], v[184:187], v[122:125]
	v_mfma_f32_16x16x32_bf16 v[114:117], v[152:155], v[192:195], v[114:117]
	v_mfma_f32_16x16x32_bf16 v[106:109], v[160:163], v[192:195], v[106:109]
	v_mfma_f32_16x16x32_bf16 v[98:101], v[152:155], v[206:209], v[98:101]
	v_mfma_f32_16x16x32_bf16 v[90:93], v[160:163], v[206:209], v[90:93]
	v_mfma_f32_16x16x32_bf16 v[82:85], v[152:155], v[214:217], v[82:85]
	v_mfma_f32_16x16x32_bf16 v[74:77], v[160:163], v[214:217], v[74:77]
	s_setprio 0
	s_setprio 1
	v_mfma_f32_16x16x32_bf16 v[126:129], v[164:167], v[180:183], v[126:129]
	v_mfma_f32_16x16x32_bf16 v[118:121], v[172:175], v[180:183], v[118:121]
	v_mfma_f32_16x16x32_bf16 v[110:113], v[164:167], v[188:191], v[110:113]
	v_mfma_f32_16x16x32_bf16 v[102:105], v[172:175], v[188:191], v[102:105]
	v_mfma_f32_16x16x32_bf16 v[94:97], v[164:167], v[196:199], v[94:97]
	v_mfma_f32_16x16x32_bf16 v[86:89], v[172:175], v[196:199], v[86:89]
	v_mfma_f32_16x16x32_bf16 v[78:81], v[164:167], v[210:213], v[78:81]
	v_mfma_f32_16x16x32_bf16 v[70:73], v[172:175], v[210:213], v[70:73]
	v_mfma_f32_16x16x32_bf16 v[126:129], v[168:171], v[184:187], v[126:129]
	v_mfma_f32_16x16x32_bf16 v[118:121], v[176:179], v[184:187], v[118:121]
	v_mfma_f32_16x16x32_bf16 v[110:113], v[168:171], v[192:195], v[110:113]
	v_mfma_f32_16x16x32_bf16 v[102:105], v[176:179], v[192:195], v[102:105]
	v_mfma_f32_16x16x32_bf16 v[94:97], v[168:171], v[206:209], v[94:97]
	v_mfma_f32_16x16x32_bf16 v[86:89], v[176:179], v[206:209], v[86:89]
	s_setprio 2
	s_barrier
	v_mfma_f32_16x16x32_bf16 v[78:81], v[168:171], v[214:217], v[78:81]
	v_mfma_f32_16x16x32_bf16 v[70:73], v[176:179], v[214:217], v[70:73]
	s_setprio 0
	s_mov_b32 m0, s41
	v_lshl_add_u64 v[142:143], v[142:143], 0, s[28:29]
	s_add_u32 s18, s18, 0x80080
	ds_read_b128 v[180:183], v147 offset:49152
	ds_read_b128 v[184:187], v147 offset:50176
	ds_read_b128 v[188:191], v147 offset:51200
	ds_read_b128 v[192:195], v147 offset:52224
	ds_read_b128 v[196:199], v147 offset:53248
	ds_read_b128 v[206:209], v147 offset:54272
	ds_read_b128 v[210:213], v147 offset:55296
	ds_read_b128 v[214:217], v147 offset:56320
	global_load_lds_dwordx4 v[142:143], off
	v_lshl_add_u64 v[142:143], v[200:201], 0, s[28:29]
	s_mov_b32 m0, s42
	s_addc_u32 s19, s19, 0
	global_load_lds_dwordx4 v[142:143], off
	v_lshl_add_u64 v[142:143], s[18:19], 0, v[0:1]
	s_mov_b32 m0, s46
	s_nop 0
	global_load_lds_dwordx4 v[142:143], off
	v_lshl_add_u64 v[142:143], s[18:19], 0, v[2:3]
	s_mov_b32 m0, s47
	s_nop 0
	global_load_lds_dwordx4 v[142:143], off
	v_lshl_add_u64 v[142:143], v[218:219], 0, s[28:29]
	s_mov_b32 m0, s43
	s_nop 0
	global_load_lds_dwordx4 v[142:143], off
	v_lshl_add_u64 v[142:143], v[220:221], 0, s[28:29]
	s_mov_b32 m0, s44
	s_nop 0
	global_load_lds_dwordx4 v[142:143], off
	s_waitcnt vmcnt(8)
	s_waitcnt lgkmcnt(0)
	s_barrier
	s_setprio 1
	s_waitcnt lgkmcnt(0)
	v_mfma_f32_16x16x32_bf16 v[66:69], v[148:151], v[180:183], v[66:69]
	v_mfma_f32_16x16x32_bf16 v[58:61], v[156:159], v[180:183], v[58:61]
	v_mfma_f32_16x16x32_bf16 v[50:53], v[148:151], v[188:191], v[50:53]
	v_mfma_f32_16x16x32_bf16 v[42:45], v[156:159], v[188:191], v[42:45]
	v_mfma_f32_16x16x32_bf16 v[34:37], v[148:151], v[196:199], v[34:37]
	v_mfma_f32_16x16x32_bf16 v[26:29], v[156:159], v[196:199], v[26:29]
	v_mfma_f32_16x16x32_bf16 v[18:21], v[148:151], v[210:213], v[18:21]
	v_mfma_f32_16x16x32_bf16 v[10:13], v[156:159], v[210:213], v[10:13]
	v_mfma_f32_16x16x32_bf16 v[66:69], v[152:155], v[184:187], v[66:69]
	v_mfma_f32_16x16x32_bf16 v[58:61], v[160:163], v[184:187], v[58:61]
	v_mfma_f32_16x16x32_bf16 v[50:53], v[152:155], v[192:195], v[50:53]
	v_mfma_f32_16x16x32_bf16 v[42:45], v[160:163], v[192:195], v[42:45]
	v_mfma_f32_16x16x32_bf16 v[34:37], v[152:155], v[206:209], v[34:37]
	v_mfma_f32_16x16x32_bf16 v[26:29], v[160:163], v[206:209], v[26:29]
	v_mfma_f32_16x16x32_bf16 v[18:21], v[152:155], v[214:217], v[18:21]
	v_mfma_f32_16x16x32_bf16 v[10:13], v[160:163], v[214:217], v[10:13]
	s_setprio 0
	s_setprio 1
	v_mfma_f32_16x16x32_bf16 v[62:65], v[164:167], v[180:183], v[62:65]
	v_mfma_f32_16x16x32_bf16 v[54:57], v[172:175], v[180:183], v[54:57]
	v_mfma_f32_16x16x32_bf16 v[46:49], v[164:167], v[188:191], v[46:49]
	v_mfma_f32_16x16x32_bf16 v[38:41], v[172:175], v[188:191], v[38:41]
	v_mfma_f32_16x16x32_bf16 v[30:33], v[164:167], v[196:199], v[30:33]
	v_mfma_f32_16x16x32_bf16 v[22:25], v[172:175], v[196:199], v[22:25]
	v_mfma_f32_16x16x32_bf16 v[14:17], v[164:167], v[210:213], v[14:17]
	v_mfma_f32_16x16x32_bf16 v[6:9], v[172:175], v[210:213], v[6:9]
	v_mfma_f32_16x16x32_bf16 v[62:65], v[168:171], v[184:187], v[62:65]
	v_mfma_f32_16x16x32_bf16 v[54:57], v[176:179], v[184:187], v[54:57]
	v_mfma_f32_16x16x32_bf16 v[46:49], v[168:171], v[192:195], v[46:49]
	v_mfma_f32_16x16x32_bf16 v[38:41], v[176:179], v[192:195], v[38:41]
	v_mfma_f32_16x16x32_bf16 v[30:33], v[168:171], v[206:209], v[30:33]
	v_mfma_f32_16x16x32_bf16 v[22:25], v[176:179], v[206:209], v[22:25]
	s_setprio 2
	s_barrier
	v_mfma_f32_16x16x32_bf16 v[14:17], v[168:171], v[214:217], v[14:17]
	v_mfma_f32_16x16x32_bf16 v[6:9], v[176:179], v[214:217], v[6:9]
	s_setprio 0
	s_add_i32 s54, s54, 2
	s_add_u32 s52, s52, 0x100
	s_addc_u32 s53, s53, 0
	s_add_u32 s16, s16, 0x100
	s_addc_u32 s17, s17, 0
	s_cmp_gt_u32 s54, 29
	s_cbranch_scc0 .LBB0_2035
	s_and_b64 vcc, exec, s[4:5]
	s_cbranch_vccz .LBB0_2038
	s_barrier

.LBB0_2114:
	v_add_u32_e32 v146, s19, v182
	v_add_u32_e32 v170, s22, v182
	ds_read_b128 v[134:137], v146
	ds_read_b128 v[138:141], v146 offset:1024
	ds_read_b128 v[142:145], v146 offset:2048
	ds_read_b128 v[146:149], v146 offset:3072
	ds_read_b128 v[150:153], v170
	ds_read_b128 v[154:157], v170 offset:1024
	ds_read_b128 v[158:161], v170 offset:2048
	ds_read_b128 v[170:173], v170 offset:3072
	s_add_u32 s10, s8, 0x100
	s_addc_u32 s11, s9, 0
	s_cmpk_eq_i32 s55, 0x52
	s_cselect_b32 s15, s3, s11
	s_cselect_b32 s14, s2, s10
	s_cselect_b32 s13, s7, s54
	s_cselect_b32 s12, s6, s53
	v_lshl_add_u64 v[214:215], s[8:9], 0, v[168:169]
	s_add_i32 m0, s25, 0xc000
	ds_read_b128 v[174:177], v184
	ds_read_b128 v[178:181], v184 offset:1024
	ds_read_b128 v[186:189], v184 offset:2048
	ds_read_b128 v[190:193], v184 offset:3072
	ds_read_b128 v[194:197], v184 offset:4096
	ds_read_b128 v[198:201], v184 offset:5120
	ds_read_b128 v[206:209], v184 offset:6144
	ds_read_b128 v[210:213], v184 offset:7168
	global_load_lds_dwordx4 v[214:215], off
	v_lshl_add_u64 v[214:215], s[8:9], 0, v[166:167]
	s_add_i32 m0, s25, 0xe000
	s_nop 0
	global_load_lds_dwordx4 v[214:215], off
	s_waitcnt vmcnt(8)
	s_waitcnt lgkmcnt(0)
	s_barrier
	s_setprio 1
	s_waitcnt lgkmcnt(0)
	v_mfma_f32_16x16x32_bf16 v[130:133], v[134:137], v[174:177], v[130:133]
	v_mfma_f32_16x16x32_bf16 v[126:129], v[142:145], v[174:177], v[126:129]
	v_mfma_f32_16x16x32_bf16 v[114:117], v[134:137], v[186:189], v[114:117]
	v_mfma_f32_16x16x32_bf16 v[110:113], v[142:145], v[186:189], v[110:113]
	v_mfma_f32_16x16x32_bf16 v[98:101], v[134:137], v[194:197], v[98:101]
	v_mfma_f32_16x16x32_bf16 v[94:97], v[142:145], v[194:197], v[94:97]
	v_mfma_f32_16x16x32_bf16 v[82:85], v[134:137], v[206:209], v[82:85]
	v_mfma_f32_16x16x32_bf16 v[78:81], v[142:145], v[206:209], v[78:81]
	v_mfma_f32_16x16x32_bf16 v[130:133], v[138:141], v[178:181], v[130:133]
	v_mfma_f32_16x16x32_bf16 v[126:129], v[146:149], v[178:181], v[126:129]
	v_mfma_f32_16x16x32_bf16 v[114:117], v[138:141], v[190:193], v[114:117]
	v_mfma_f32_16x16x32_bf16 v[110:113], v[146:149], v[190:193], v[110:113]
	v_mfma_f32_16x16x32_bf16 v[98:101], v[138:141], v[198:201], v[98:101]
	v_mfma_f32_16x16x32_bf16 v[94:97], v[146:149], v[198:201], v[94:97]
	v_mfma_f32_16x16x32_bf16 v[82:85], v[138:141], v[210:213], v[82:85]
	v_mfma_f32_16x16x32_bf16 v[78:81], v[146:149], v[210:213], v[78:81]
	s_setprio 0
	s_setprio 1
	v_mfma_f32_16x16x32_bf16 v[122:125], v[150:153], v[174:177], v[122:125]
	v_mfma_f32_16x16x32_bf16 v[118:121], v[158:161], v[174:177], v[118:121]
	v_mfma_f32_16x16x32_bf16 v[106:109], v[150:153], v[186:189], v[106:109]
	v_mfma_f32_16x16x32_bf16 v[102:105], v[158:161], v[186:189], v[102:105]
	v_mfma_f32_16x16x32_bf16 v[90:93], v[150:153], v[194:197], v[90:93]
	v_mfma_f32_16x16x32_bf16 v[86:89], v[158:161], v[194:197], v[86:89]
	v_mfma_f32_16x16x32_bf16 v[74:77], v[150:153], v[206:209], v[74:77]
	v_mfma_f32_16x16x32_bf16 v[70:73], v[158:161], v[206:209], v[70:73]
	v_mfma_f32_16x16x32_bf16 v[122:125], v[154:157], v[178:181], v[122:125]
	v_mfma_f32_16x16x32_bf16 v[118:121], v[170:173], v[178:181], v[118:121]
	v_mfma_f32_16x16x32_bf16 v[106:109], v[154:157], v[190:193], v[106:109]
	v_mfma_f32_16x16x32_bf16 v[102:105], v[170:173], v[190:193], v[102:105]
	v_mfma_f32_16x16x32_bf16 v[90:93], v[154:157], v[198:201], v[90:93]
	v_mfma_f32_16x16x32_bf16 v[86:89], v[170:173], v[198:201], v[86:89]
	s_setprio 2
	s_barrier
	v_mfma_f32_16x16x32_bf16 v[74:77], v[154:157], v[210:213], v[74:77]
	v_mfma_f32_16x16x32_bf16 v[70:73], v[170:173], v[210:213], v[70:73]
	s_setprio 0
	s_mov_b32 m0, s20
	v_lshl_add_u64 v[214:215], s[12:13], 0, v[0:1]
	s_add_u32 s8, s12, 0x158000
	ds_read_b128 v[174:177], v184 offset:16384
	ds_read_b128 v[178:181], v184 offset:17408
	ds_read_b128 v[186:189], v184 offset:18432
	ds_read_b128 v[190:193], v184 offset:19456
	ds_read_b128 v[194:197], v184 offset:20480
	ds_read_b128 v[198:201], v184 offset:21504
	ds_read_b128 v[206:209], v184 offset:22528
	ds_read_b128 v[210:213], v184 offset:23552
	global_load_lds_dwordx4 v[214:215], off
	v_lshl_add_u64 v[216:217], s[12:13], 0, v[164:165]
	s_mov_b32 m0, s21
	s_addc_u32 s9, s13, 0
	global_load_lds_dwordx4 v[216:217], off
	v_lshl_add_u64 v[218:219], s[8:9], 0, v[0:1]
	s_mov_b32 m0, s23
	v_lshl_add_u64 v[220:221], s[14:15], 0, v[162:163]
	global_load_lds_dwordx4 v[218:219], off
	v_lshl_add_u64 v[218:219], s[8:9], 0, v[164:165]
	s_mov_b32 m0, s24
	s_nop 0
	global_load_lds_dwordx4 v[218:219], off
	v_lshl_add_u64 v[218:219], s[14:15], 0, v[2:3]
	s_mov_b32 m0, s25
	s_nop 0
	global_load_lds_dwordx4 v[218:219], off
	s_mov_b32 m0, s30
	s_nop 0
	global_load_lds_dwordx4 v[220:221], off
	s_waitcnt vmcnt(8)
	s_waitcnt lgkmcnt(0)
	s_barrier
	s_setprio 1
	s_waitcnt lgkmcnt(0)
	v_mfma_f32_16x16x32_bf16 v[66:69], v[134:137], v[174:177], v[66:69]
	v_mfma_f32_16x16x32_bf16 v[62:65], v[142:145], v[174:177], v[62:65]
	v_mfma_f32_16x16x32_bf16 v[50:53], v[134:137], v[186:189], v[50:53]
	v_mfma_f32_16x16x32_bf16 v[46:49], v[142:145], v[186:189], v[46:49]
	v_mfma_f32_16x16x32_bf16 v[34:37], v[134:137], v[194:197], v[34:37]
	v_mfma_f32_16x16x32_bf16 v[30:33], v[142:145], v[194:197], v[30:33]
	v_mfma_f32_16x16x32_bf16 v[18:21], v[134:137], v[206:209], v[18:21]
	v_mfma_f32_16x16x32_bf16 v[14:17], v[142:145], v[206:209], v[14:17]
	v_mfma_f32_16x16x32_bf16 v[66:69], v[138:141], v[178:181], v[66:69]
	v_mfma_f32_16x16x32_bf16 v[62:65], v[146:149], v[178:181], v[62:65]
	v_mfma_f32_16x16x32_bf16 v[50:53], v[138:141], v[190:193], v[50:53]
	v_mfma_f32_16x16x32_bf16 v[46:49], v[146:149], v[190:193], v[46:49]
	v_mfma_f32_16x16x32_bf16 v[34:37], v[138:141], v[198:201], v[34:37]
	v_mfma_f32_16x16x32_bf16 v[30:33], v[146:149], v[198:201], v[30:33]
	v_mfma_f32_16x16x32_bf16 v[18:21], v[138:141], v[210:213], v[18:21]
	v_mfma_f32_16x16x32_bf16 v[14:17], v[146:149], v[210:213], v[14:17]
	s_setprio 0
	s_setprio 1
	v_mfma_f32_16x16x32_bf16 v[58:61], v[150:153], v[174:177], v[58:61]
	v_mfma_f32_16x16x32_bf16 v[54:57], v[158:161], v[174:177], v[54:57]
	v_mfma_f32_16x16x32_bf16 v[42:45], v[150:153], v[186:189], v[42:45]
	v_mfma_f32_16x16x32_bf16 v[38:41], v[158:161], v[186:189], v[38:41]
	v_mfma_f32_16x16x32_bf16 v[26:29], v[150:153], v[194:197], v[26:29]
	v_mfma_f32_16x16x32_bf16 v[22:25], v[158:161], v[194:197], v[22:25]
	v_mfma_f32_16x16x32_bf16 v[10:13], v[150:153], v[206:209], v[10:13]
	v_mfma_f32_16x16x32_bf16 v[6:9], v[158:161], v[206:209], v[6:9]
	v_mfma_f32_16x16x32_bf16 v[58:61], v[154:157], v[178:181], v[58:61]
	v_mfma_f32_16x16x32_bf16 v[54:57], v[170:173], v[178:181], v[54:57]
	v_mfma_f32_16x16x32_bf16 v[42:45], v[154:157], v[190:193], v[42:45]
	v_mfma_f32_16x16x32_bf16 v[38:41], v[170:173], v[190:193], v[38:41]
	v_mfma_f32_16x16x32_bf16 v[26:29], v[154:157], v[198:201], v[26:29]
	v_mfma_f32_16x16x32_bf16 v[22:25], v[170:173], v[198:201], v[22:25]
	s_setprio 2
	s_barrier
	v_mfma_f32_16x16x32_bf16 v[10:13], v[154:157], v[210:213], v[10:13]
	v_mfma_f32_16x16x32_bf16 v[6:9], v[170:173], v[210:213], v[6:9]
	s_setprio 0
	v_add_u32_e32 v146, s40, v182
	v_add_u32_e32 v170, s45, v182
	ds_read_b128 v[134:137], v146
	ds_read_b128 v[138:141], v146 offset:1024
	ds_read_b128 v[142:145], v146 offset:2048
	ds_read_b128 v[146:149], v146 offset:3072
	ds_read_b128 v[150:153], v170
	ds_read_b128 v[154:157], v170 offset:1024
	ds_read_b128 v[158:161], v170 offset:2048
	ds_read_b128 v[170:173], v170 offset:3072
	s_add_u32 s8, s14, 0x280000
	s_addc_u32 s9, s15, 0
	s_mov_b32 m0, s31
	v_lshl_add_u64 v[222:223], s[8:9], 0, v[2:3]
	ds_read_b128 v[174:177], v184 offset:32768
	ds_read_b128 v[178:181], v184 offset:33792
	ds_read_b128 v[186:189], v184 offset:34816
	ds_read_b128 v[190:193], v184 offset:35840
	ds_read_b128 v[194:197], v184 offset:36864
	ds_read_b128 v[198:201], v184 offset:37888
	ds_read_b128 v[206:209], v184 offset:38912
	ds_read_b128 v[210:213], v184 offset:39936
	global_load_lds_dwordx4 v[222:223], off
	v_lshl_add_u64 v[222:223], s[8:9], 0, v[162:163]
	s_mov_b32 m0, s34
	s_nop 0
	global_load_lds_dwordx4 v[222:223], off
	s_waitcnt vmcnt(8)
	s_waitcnt lgkmcnt(0)
	s_barrier
	s_setprio 1
	s_waitcnt lgkmcnt(0)
	v_mfma_f32_16x16x32_bf16 v[130:133], v[134:137], v[174:177], v[130:133]
	v_mfma_f32_16x16x32_bf16 v[126:129], v[142:145], v[174:177], v[126:129]
	v_mfma_f32_16x16x32_bf16 v[114:117], v[134:137], v[186:189], v[114:117]
	v_mfma_f32_16x16x32_bf16 v[110:113], v[142:145], v[186:189], v[110:113]
	v_mfma_f32_16x16x32_bf16 v[98:101], v[134:137], v[194:197], v[98:101]
	v_mfma_f32_16x16x32_bf16 v[94:97], v[142:145], v[194:197], v[94:97]
	v_mfma_f32_16x16x32_bf16 v[82:85], v[134:137], v[206:209], v[82:85]
	v_mfma_f32_16x16x32_bf16 v[78:81], v[142:145], v[206:209], v[78:81]
	v_mfma_f32_16x16x32_bf16 v[130:133], v[138:141], v[178:181], v[130:133]
	v_mfma_f32_16x16x32_bf16 v[126:129], v[146:149], v[178:181], v[126:129]
	v_mfma_f32_16x16x32_bf16 v[114:117], v[138:141], v[190:193], v[114:117]
	v_mfma_f32_16x16x32_bf16 v[110:113], v[146:149], v[190:193], v[110:113]
	v_mfma_f32_16x16x32_bf16 v[98:101], v[138:141], v[198:201], v[98:101]
	v_mfma_f32_16x16x32_bf16 v[94:97], v[146:149], v[198:201], v[94:97]
	v_mfma_f32_16x16x32_bf16 v[82:85], v[138:141], v[210:213], v[82:85]
	v_mfma_f32_16x16x32_bf16 v[78:81], v[146:149], v[210:213], v[78:81]
	s_setprio 0
	s_setprio 1
	v_mfma_f32_16x16x32_bf16 v[122:125], v[150:153], v[174:177], v[122:125]
	v_mfma_f32_16x16x32_bf16 v[118:121], v[158:161], v[174:177], v[118:121]
	v_mfma_f32_16x16x32_bf16 v[106:109], v[150:153], v[186:189], v[106:109]
	v_mfma_f32_16x16x32_bf16 v[102:105], v[158:161], v[186:189], v[102:105]
	v_mfma_f32_16x16x32_bf16 v[90:93], v[150:153], v[194:197], v[90:93]
	v_mfma_f32_16x16x32_bf16 v[86:89], v[158:161], v[194:197], v[86:89]
	v_mfma_f32_16x16x32_bf16 v[74:77], v[150:153], v[206:209], v[74:77]
	v_mfma_f32_16x16x32_bf16 v[70:73], v[158:161], v[206:209], v[70:73]
	v_mfma_f32_16x16x32_bf16 v[122:125], v[154:157], v[178:181], v[122:125]
	v_mfma_f32_16x16x32_bf16 v[118:121], v[170:173], v[178:181], v[118:121]
	v_mfma_f32_16x16x32_bf16 v[106:109], v[154:157], v[190:193], v[106:109]
	v_mfma_f32_16x16x32_bf16 v[102:105], v[170:173], v[190:193], v[102:105]
	v_mfma_f32_16x16x32_bf16 v[90:93], v[154:157], v[198:201], v[90:93]
	v_mfma_f32_16x16x32_bf16 v[86:89], v[170:173], v[198:201], v[86:89]
	s_setprio 2
	s_barrier
	v_mfma_f32_16x16x32_bf16 v[74:77], v[154:157], v[210:213], v[74:77]
	v_mfma_f32_16x16x32_bf16 v[70:73], v[170:173], v[210:213], v[70:73]
	s_setprio 0
	s_mov_b32 m0, s41
	v_lshl_add_u64 v[214:215], v[214:215], 0, s[28:29]
	s_add_u32 s8, s12, 0x158080
	ds_read_b128 v[174:177], v184 offset:49152
	ds_read_b128 v[178:181], v184 offset:50176
	ds_read_b128 v[186:189], v184 offset:51200
	ds_read_b128 v[190:193], v184 offset:52224
	ds_read_b128 v[194:197], v184 offset:53248
	ds_read_b128 v[198:201], v184 offset:54272
	ds_read_b128 v[206:209], v184 offset:55296
	ds_read_b128 v[210:213], v184 offset:56320
	global_load_lds_dwordx4 v[214:215], off
	v_lshl_add_u64 v[214:215], v[216:217], 0, s[28:29]
	s_mov_b32 m0, s42
	s_addc_u32 s9, s13, 0
	global_load_lds_dwordx4 v[214:215], off
	v_lshl_add_u64 v[214:215], s[8:9], 0, v[0:1]
	s_mov_b32 m0, s46
	s_nop 0
	global_load_lds_dwordx4 v[214:215], off
	v_lshl_add_u64 v[214:215], s[8:9], 0, v[164:165]
	s_mov_b32 m0, s47
	s_nop 0
	global_load_lds_dwordx4 v[214:215], off
	v_lshl_add_u64 v[214:215], v[218:219], 0, s[28:29]
	s_mov_b32 m0, s43
	s_nop 0
	global_load_lds_dwordx4 v[214:215], off
	v_lshl_add_u64 v[214:215], v[220:221], 0, s[28:29]
	s_mov_b32 m0, s44
	s_nop 0
	global_load_lds_dwordx4 v[214:215], off
	s_waitcnt vmcnt(8)
	s_waitcnt lgkmcnt(0)
	s_barrier
	s_setprio 1
	s_waitcnt lgkmcnt(0)
	v_mfma_f32_16x16x32_bf16 v[66:69], v[134:137], v[174:177], v[66:69]
	v_mfma_f32_16x16x32_bf16 v[62:65], v[142:145], v[174:177], v[62:65]
	v_mfma_f32_16x16x32_bf16 v[50:53], v[134:137], v[186:189], v[50:53]
	v_mfma_f32_16x16x32_bf16 v[46:49], v[142:145], v[186:189], v[46:49]
	v_mfma_f32_16x16x32_bf16 v[34:37], v[134:137], v[194:197], v[34:37]
	v_mfma_f32_16x16x32_bf16 v[30:33], v[142:145], v[194:197], v[30:33]
	v_mfma_f32_16x16x32_bf16 v[18:21], v[134:137], v[206:209], v[18:21]
	v_mfma_f32_16x16x32_bf16 v[14:17], v[142:145], v[206:209], v[14:17]
	v_mfma_f32_16x16x32_bf16 v[66:69], v[138:141], v[178:181], v[66:69]
	v_mfma_f32_16x16x32_bf16 v[62:65], v[146:149], v[178:181], v[62:65]
	v_mfma_f32_16x16x32_bf16 v[50:53], v[138:141], v[190:193], v[50:53]
	v_mfma_f32_16x16x32_bf16 v[46:49], v[146:149], v[190:193], v[46:49]
	v_mfma_f32_16x16x32_bf16 v[34:37], v[138:141], v[198:201], v[34:37]
	v_mfma_f32_16x16x32_bf16 v[30:33], v[146:149], v[198:201], v[30:33]
	v_mfma_f32_16x16x32_bf16 v[18:21], v[138:141], v[210:213], v[18:21]
	v_mfma_f32_16x16x32_bf16 v[14:17], v[146:149], v[210:213], v[14:17]
	s_setprio 0
	s_setprio 1
	v_mfma_f32_16x16x32_bf16 v[58:61], v[150:153], v[174:177], v[58:61]
	v_mfma_f32_16x16x32_bf16 v[54:57], v[158:161], v[174:177], v[54:57]
	v_mfma_f32_16x16x32_bf16 v[42:45], v[150:153], v[186:189], v[42:45]
	v_mfma_f32_16x16x32_bf16 v[38:41], v[158:161], v[186:189], v[38:41]
	v_mfma_f32_16x16x32_bf16 v[26:29], v[150:153], v[194:197], v[26:29]
	v_mfma_f32_16x16x32_bf16 v[22:25], v[158:161], v[194:197], v[22:25]
	v_mfma_f32_16x16x32_bf16 v[10:13], v[150:153], v[206:209], v[10:13]
	v_mfma_f32_16x16x32_bf16 v[6:9], v[158:161], v[206:209], v[6:9]
	v_mfma_f32_16x16x32_bf16 v[58:61], v[154:157], v[178:181], v[58:61]
	v_mfma_f32_16x16x32_bf16 v[54:57], v[170:173], v[178:181], v[54:57]
	v_mfma_f32_16x16x32_bf16 v[42:45], v[154:157], v[190:193], v[42:45]
	v_mfma_f32_16x16x32_bf16 v[38:41], v[170:173], v[190:193], v[38:41]
	v_mfma_f32_16x16x32_bf16 v[26:29], v[154:157], v[198:201], v[26:29]
	v_mfma_f32_16x16x32_bf16 v[22:25], v[170:173], v[198:201], v[22:25]
	s_setprio 2
	s_barrier
	v_mfma_f32_16x16x32_bf16 v[10:13], v[154:157], v[210:213], v[10:13]
	v_mfma_f32_16x16x32_bf16 v[6:9], v[170:173], v[210:213], v[6:9]
	s_setprio 0
	s_add_i32 s55, s55, 2
	s_add_u32 s53, s53, 0x100
	s_addc_u32 s54, s54, 0
	s_cmpk_gt_u32 s55, 0x53
	s_mov_b64 s[8:9], s[10:11]
	s_cbranch_scc0 .LBB0_2114
	s_and_b64 vcc, exec, s[4:5]
	s_cbranch_vccz .LBB0_2117
	s_barrier

.LBB0_2160:
	v_add_u32_e32 v146, s20, v172
	v_add_u32_e32 v170, s23, v172
	ds_read_b128 v[134:137], v146
	ds_read_b128 v[138:141], v146 offset:1024
	ds_read_b128 v[142:145], v146 offset:2048
	ds_read_b128 v[146:149], v146 offset:3072
	ds_read_b128 v[150:153], v170
	ds_read_b128 v[162:165], v170 offset:1024
	ds_read_b128 v[166:169], v170 offset:2048
	ds_read_b128 v[176:179], v170 offset:3072
	s_add_u32 s10, s8, 0x100
	s_addc_u32 s11, s9, 0
	s_cmpk_eq_i32 s52, 0x52
	s_cselect_b32 s15, s3, s11
	s_cselect_b32 s14, s2, s10
	s_cselect_b32 s13, s7, s51
	s_cselect_b32 s12, s6, s50
	v_lshl_add_u64 v[170:171], s[8:9], 0, v[160:161]
	s_add_i32 m0, s26, 0xc000
	ds_read_b128 v[180:183], v174
	ds_read_b128 v[184:187], v174 offset:1024
	ds_read_b128 v[188:191], v174 offset:2048
	ds_read_b128 v[192:195], v174 offset:3072
	ds_read_b128 v[196:199], v174 offset:4096
	ds_read_b128 v[206:209], v174 offset:5120
	ds_read_b128 v[210:213], v174 offset:6144
	ds_read_b128 v[214:217], v174 offset:7168
	global_load_lds_dwordx4 v[170:171], off
	v_lshl_add_u64 v[170:171], s[8:9], 0, v[158:159]
	s_add_i32 m0, s26, 0xe000
	s_nop 0
	global_load_lds_dwordx4 v[170:171], off
	s_waitcnt vmcnt(8)
	s_waitcnt lgkmcnt(0)
	s_barrier
	s_setprio 1
	s_waitcnt lgkmcnt(0)
	v_mfma_f32_16x16x32_bf16 v[130:133], v[134:137], v[180:183], v[130:133]
	v_mfma_f32_16x16x32_bf16 v[126:129], v[142:145], v[180:183], v[126:129]
	v_mfma_f32_16x16x32_bf16 v[122:125], v[134:137], v[188:191], v[122:125]
	v_mfma_f32_16x16x32_bf16 v[118:121], v[142:145], v[188:191], v[118:121]
	v_mfma_f32_16x16x32_bf16 v[98:101], v[134:137], v[196:199], v[98:101]
	v_mfma_f32_16x16x32_bf16 v[94:97], v[142:145], v[196:199], v[94:97]
	v_mfma_f32_16x16x32_bf16 v[86:89], v[134:137], v[210:213], v[86:89]
	v_mfma_f32_16x16x32_bf16 v[78:81], v[142:145], v[210:213], v[78:81]
	v_mfma_f32_16x16x32_bf16 v[130:133], v[138:141], v[184:187], v[130:133]
	v_mfma_f32_16x16x32_bf16 v[126:129], v[146:149], v[184:187], v[126:129]
	v_mfma_f32_16x16x32_bf16 v[122:125], v[138:141], v[192:195], v[122:125]
	v_mfma_f32_16x16x32_bf16 v[118:121], v[146:149], v[192:195], v[118:121]
	v_mfma_f32_16x16x32_bf16 v[98:101], v[138:141], v[206:209], v[98:101]
	v_mfma_f32_16x16x32_bf16 v[94:97], v[146:149], v[206:209], v[94:97]
	v_mfma_f32_16x16x32_bf16 v[86:89], v[138:141], v[214:217], v[86:89]
	v_mfma_f32_16x16x32_bf16 v[78:81], v[146:149], v[214:217], v[78:81]
	s_setprio 0
	s_setprio 1
	v_mfma_f32_16x16x32_bf16 v[114:117], v[150:153], v[180:183], v[114:117]
	v_mfma_f32_16x16x32_bf16 v[110:113], v[166:169], v[180:183], v[110:113]
	v_mfma_f32_16x16x32_bf16 v[106:109], v[150:153], v[188:191], v[106:109]
	v_mfma_f32_16x16x32_bf16 v[102:105], v[166:169], v[188:191], v[102:105]
	v_mfma_f32_16x16x32_bf16 v[90:93], v[150:153], v[196:199], v[90:93]
	v_mfma_f32_16x16x32_bf16 v[82:85], v[166:169], v[196:199], v[82:85]
	v_mfma_f32_16x16x32_bf16 v[74:77], v[150:153], v[210:213], v[74:77]
	v_mfma_f32_16x16x32_bf16 v[70:73], v[166:169], v[210:213], v[70:73]
	v_mfma_f32_16x16x32_bf16 v[114:117], v[162:165], v[184:187], v[114:117]
	v_mfma_f32_16x16x32_bf16 v[110:113], v[176:179], v[184:187], v[110:113]
	v_mfma_f32_16x16x32_bf16 v[106:109], v[162:165], v[192:195], v[106:109]
	v_mfma_f32_16x16x32_bf16 v[102:105], v[176:179], v[192:195], v[102:105]
	v_mfma_f32_16x16x32_bf16 v[90:93], v[162:165], v[206:209], v[90:93]
	v_mfma_f32_16x16x32_bf16 v[82:85], v[176:179], v[206:209], v[82:85]
	s_setprio 2
	s_barrier
	v_mfma_f32_16x16x32_bf16 v[74:77], v[162:165], v[214:217], v[74:77]
	v_mfma_f32_16x16x32_bf16 v[70:73], v[176:179], v[214:217], v[70:73]
	s_setprio 0
	s_mov_b32 m0, s21
	v_lshl_add_u64 v[170:171], s[12:13], 0, v[0:1]
	s_add_u32 s8, s12, 0x158000
	ds_read_b128 v[180:183], v174 offset:16384
	ds_read_b128 v[184:187], v174 offset:17408
	ds_read_b128 v[188:191], v174 offset:18432
	ds_read_b128 v[192:195], v174 offset:19456
	ds_read_b128 v[196:199], v174 offset:20480
	ds_read_b128 v[206:209], v174 offset:21504
	ds_read_b128 v[210:213], v174 offset:22528
	ds_read_b128 v[214:217], v174 offset:23552
	global_load_lds_dwordx4 v[170:171], off
	v_lshl_add_u64 v[200:201], s[12:13], 0, v[156:157]
	s_mov_b32 m0, s22
	s_addc_u32 s9, s13, 0
	global_load_lds_dwordx4 v[200:201], off
	v_lshl_add_u64 v[218:219], s[8:9], 0, v[0:1]
	s_mov_b32 m0, s24
	v_lshl_add_u64 v[220:221], s[14:15], 0, v[154:155]
	global_load_lds_dwordx4 v[218:219], off
	v_lshl_add_u64 v[218:219], s[8:9], 0, v[156:157]
	s_mov_b32 m0, s25
	s_nop 0
	global_load_lds_dwordx4 v[218:219], off
	v_lshl_add_u64 v[218:219], s[14:15], 0, v[2:3]
	s_mov_b32 m0, s26
	s_nop 0
	global_load_lds_dwordx4 v[218:219], off
	s_mov_b32 m0, s30
	s_nop 0
	global_load_lds_dwordx4 v[220:221], off
	s_waitcnt vmcnt(8)
	s_waitcnt lgkmcnt(0)
	s_barrier
	s_setprio 1
	s_waitcnt lgkmcnt(0)
	v_mfma_f32_16x16x32_bf16 v[66:69], v[134:137], v[180:183], v[66:69]
	v_mfma_f32_16x16x32_bf16 v[62:65], v[142:145], v[180:183], v[62:65]
	v_mfma_f32_16x16x32_bf16 v[54:57], v[134:137], v[188:191], v[54:57]
	v_mfma_f32_16x16x32_bf16 v[46:49], v[142:145], v[188:191], v[46:49]
	v_mfma_f32_16x16x32_bf16 v[38:41], v[134:137], v[196:199], v[38:41]
	v_mfma_f32_16x16x32_bf16 v[30:33], v[142:145], v[196:199], v[30:33]
	v_mfma_f32_16x16x32_bf16 v[22:25], v[134:137], v[210:213], v[22:25]
	v_mfma_f32_16x16x32_bf16 v[14:17], v[142:145], v[210:213], v[14:17]
	v_mfma_f32_16x16x32_bf16 v[66:69], v[138:141], v[184:187], v[66:69]
	v_mfma_f32_16x16x32_bf16 v[62:65], v[146:149], v[184:187], v[62:65]
	v_mfma_f32_16x16x32_bf16 v[54:57], v[138:141], v[192:195], v[54:57]
	v_mfma_f32_16x16x32_bf16 v[46:49], v[146:149], v[192:195], v[46:49]
	v_mfma_f32_16x16x32_bf16 v[38:41], v[138:141], v[206:209], v[38:41]
	v_mfma_f32_16x16x32_bf16 v[30:33], v[146:149], v[206:209], v[30:33]
	v_mfma_f32_16x16x32_bf16 v[22:25], v[138:141], v[214:217], v[22:25]
	v_mfma_f32_16x16x32_bf16 v[14:17], v[146:149], v[214:217], v[14:17]
	s_setprio 0
	s_setprio 1
	v_mfma_f32_16x16x32_bf16 v[58:61], v[150:153], v[180:183], v[58:61]
	v_mfma_f32_16x16x32_bf16 v[50:53], v[166:169], v[180:183], v[50:53]
	v_mfma_f32_16x16x32_bf16 v[42:45], v[150:153], v[188:191], v[42:45]
	v_mfma_f32_16x16x32_bf16 v[34:37], v[166:169], v[188:191], v[34:37]
	v_mfma_f32_16x16x32_bf16 v[26:29], v[150:153], v[196:199], v[26:29]
	v_mfma_f32_16x16x32_bf16 v[18:21], v[166:169], v[196:199], v[18:21]
	v_mfma_f32_16x16x32_bf16 v[10:13], v[150:153], v[210:213], v[10:13]
	v_mfma_f32_16x16x32_bf16 v[6:9], v[166:169], v[210:213], v[6:9]
	v_mfma_f32_16x16x32_bf16 v[58:61], v[162:165], v[184:187], v[58:61]
	v_mfma_f32_16x16x32_bf16 v[50:53], v[176:179], v[184:187], v[50:53]
	v_mfma_f32_16x16x32_bf16 v[42:45], v[162:165], v[192:195], v[42:45]
	v_mfma_f32_16x16x32_bf16 v[34:37], v[176:179], v[192:195], v[34:37]
	v_mfma_f32_16x16x32_bf16 v[26:29], v[162:165], v[206:209], v[26:29]
	v_mfma_f32_16x16x32_bf16 v[18:21], v[176:179], v[206:209], v[18:21]
	s_setprio 2
	s_barrier
	v_mfma_f32_16x16x32_bf16 v[10:13], v[162:165], v[214:217], v[10:13]
	v_mfma_f32_16x16x32_bf16 v[6:9], v[176:179], v[214:217], v[6:9]
	s_setprio 0
	v_add_u32_e32 v146, s35, v172
	v_add_u32_e32 v175, s42, v172
	ds_read_b128 v[134:137], v146
	ds_read_b128 v[138:141], v146 offset:1024
	ds_read_b128 v[142:145], v146 offset:2048
	ds_read_b128 v[146:149], v146 offset:3072
	ds_read_b128 v[150:153], v175
	ds_read_b128 v[162:165], v175 offset:1024
	ds_read_b128 v[166:169], v175 offset:2048
	ds_read_b128 v[176:179], v175 offset:3072
	s_add_u32 s8, s14, 0x280000
	s_addc_u32 s9, s15, 0
	s_mov_b32 m0, s31
	v_lshl_add_u64 v[222:223], s[8:9], 0, v[2:3]
	ds_read_b128 v[180:183], v174 offset:32768
	ds_read_b128 v[184:187], v174 offset:33792
	ds_read_b128 v[188:191], v174 offset:34816
	ds_read_b128 v[192:195], v174 offset:35840
	ds_read_b128 v[196:199], v174 offset:36864
	ds_read_b128 v[206:209], v174 offset:37888
	ds_read_b128 v[210:213], v174 offset:38912
	ds_read_b128 v[214:217], v174 offset:39936
	global_load_lds_dwordx4 v[222:223], off
	v_lshl_add_u64 v[222:223], s[8:9], 0, v[154:155]
	s_mov_b32 m0, s34
	s_nop 0
	global_load_lds_dwordx4 v[222:223], off
	s_waitcnt vmcnt(8)
	s_waitcnt lgkmcnt(0)
	s_barrier
	s_setprio 1
	s_waitcnt lgkmcnt(0)
	v_mfma_f32_16x16x32_bf16 v[130:133], v[134:137], v[180:183], v[130:133]
	v_mfma_f32_16x16x32_bf16 v[126:129], v[142:145], v[180:183], v[126:129]
	v_mfma_f32_16x16x32_bf16 v[122:125], v[134:137], v[188:191], v[122:125]
	v_mfma_f32_16x16x32_bf16 v[118:121], v[142:145], v[188:191], v[118:121]
	v_mfma_f32_16x16x32_bf16 v[98:101], v[134:137], v[196:199], v[98:101]
	v_mfma_f32_16x16x32_bf16 v[94:97], v[142:145], v[196:199], v[94:97]
	v_mfma_f32_16x16x32_bf16 v[86:89], v[134:137], v[210:213], v[86:89]
	v_mfma_f32_16x16x32_bf16 v[78:81], v[142:145], v[210:213], v[78:81]
	v_mfma_f32_16x16x32_bf16 v[130:133], v[138:141], v[184:187], v[130:133]
	v_mfma_f32_16x16x32_bf16 v[126:129], v[146:149], v[184:187], v[126:129]
	v_mfma_f32_16x16x32_bf16 v[122:125], v[138:141], v[192:195], v[122:125]
	v_mfma_f32_16x16x32_bf16 v[118:121], v[146:149], v[192:195], v[118:121]
	v_mfma_f32_16x16x32_bf16 v[98:101], v[138:141], v[206:209], v[98:101]
	v_mfma_f32_16x16x32_bf16 v[94:97], v[146:149], v[206:209], v[94:97]
	v_mfma_f32_16x16x32_bf16 v[86:89], v[138:141], v[214:217], v[86:89]
	v_mfma_f32_16x16x32_bf16 v[78:81], v[146:149], v[214:217], v[78:81]
	s_setprio 0
	s_setprio 1
	v_mfma_f32_16x16x32_bf16 v[114:117], v[150:153], v[180:183], v[114:117]
	v_mfma_f32_16x16x32_bf16 v[110:113], v[166:169], v[180:183], v[110:113]
	v_mfma_f32_16x16x32_bf16 v[106:109], v[150:153], v[188:191], v[106:109]
	v_mfma_f32_16x16x32_bf16 v[102:105], v[166:169], v[188:191], v[102:105]
	v_mfma_f32_16x16x32_bf16 v[90:93], v[150:153], v[196:199], v[90:93]
	v_mfma_f32_16x16x32_bf16 v[82:85], v[166:169], v[196:199], v[82:85]
	v_mfma_f32_16x16x32_bf16 v[74:77], v[150:153], v[210:213], v[74:77]
	v_mfma_f32_16x16x32_bf16 v[70:73], v[166:169], v[210:213], v[70:73]
	v_mfma_f32_16x16x32_bf16 v[114:117], v[162:165], v[184:187], v[114:117]
	v_mfma_f32_16x16x32_bf16 v[110:113], v[176:179], v[184:187], v[110:113]
	v_mfma_f32_16x16x32_bf16 v[106:109], v[162:165], v[192:195], v[106:109]
	v_mfma_f32_16x16x32_bf16 v[102:105], v[176:179], v[192:195], v[102:105]
	v_mfma_f32_16x16x32_bf16 v[90:93], v[162:165], v[206:209], v[90:93]
	v_mfma_f32_16x16x32_bf16 v[82:85], v[176:179], v[206:209], v[82:85]
	s_setprio 2
	s_barrier
	v_mfma_f32_16x16x32_bf16 v[74:77], v[162:165], v[214:217], v[74:77]
	v_mfma_f32_16x16x32_bf16 v[70:73], v[176:179], v[214:217], v[70:73]
	s_setprio 0
	s_mov_b32 m0, s38
	v_lshl_add_u64 v[170:171], v[170:171], 0, s[28:29]
	s_add_u32 s8, s12, 0x158080
	ds_read_b128 v[180:183], v174 offset:49152
	ds_read_b128 v[184:187], v174 offset:50176
	ds_read_b128 v[188:191], v174 offset:51200
	ds_read_b128 v[192:195], v174 offset:52224
	ds_read_b128 v[196:199], v174 offset:53248
	ds_read_b128 v[206:209], v174 offset:54272
	ds_read_b128 v[210:213], v174 offset:55296
	ds_read_b128 v[214:217], v174 offset:56320
	global_load_lds_dwordx4 v[170:171], off
	v_lshl_add_u64 v[170:171], v[200:201], 0, s[28:29]
	s_mov_b32 m0, s39
	s_addc_u32 s9, s13, 0
	global_load_lds_dwordx4 v[170:171], off
	v_lshl_add_u64 v[170:171], s[8:9], 0, v[0:1]
	s_mov_b32 m0, s43
	s_nop 0
	global_load_lds_dwordx4 v[170:171], off
	v_lshl_add_u64 v[170:171], s[8:9], 0, v[156:157]
	s_mov_b32 m0, s44
	s_nop 0
	global_load_lds_dwordx4 v[170:171], off
	v_lshl_add_u64 v[170:171], v[218:219], 0, s[28:29]
	s_mov_b32 m0, s40
	s_nop 0
	global_load_lds_dwordx4 v[170:171], off
	v_lshl_add_u64 v[170:171], v[220:221], 0, s[28:29]
	s_mov_b32 m0, s41
	s_nop 0
	global_load_lds_dwordx4 v[170:171], off
	s_waitcnt vmcnt(8)
	s_waitcnt lgkmcnt(0)
	s_barrier
	s_setprio 1
	s_waitcnt lgkmcnt(0)
	v_mfma_f32_16x16x32_bf16 v[66:69], v[134:137], v[180:183], v[66:69]
	v_mfma_f32_16x16x32_bf16 v[62:65], v[142:145], v[180:183], v[62:65]
	v_mfma_f32_16x16x32_bf16 v[54:57], v[134:137], v[188:191], v[54:57]
	v_mfma_f32_16x16x32_bf16 v[46:49], v[142:145], v[188:191], v[46:49]
	v_mfma_f32_16x16x32_bf16 v[38:41], v[134:137], v[196:199], v[38:41]
	v_mfma_f32_16x16x32_bf16 v[30:33], v[142:145], v[196:199], v[30:33]
	v_mfma_f32_16x16x32_bf16 v[22:25], v[134:137], v[210:213], v[22:25]
	v_mfma_f32_16x16x32_bf16 v[14:17], v[142:145], v[210:213], v[14:17]
	v_mfma_f32_16x16x32_bf16 v[66:69], v[138:141], v[184:187], v[66:69]
	v_mfma_f32_16x16x32_bf16 v[62:65], v[146:149], v[184:187], v[62:65]
	v_mfma_f32_16x16x32_bf16 v[54:57], v[138:141], v[192:195], v[54:57]
	v_mfma_f32_16x16x32_bf16 v[46:49], v[146:149], v[192:195], v[46:49]
	v_mfma_f32_16x16x32_bf16 v[38:41], v[138:141], v[206:209], v[38:41]
	v_mfma_f32_16x16x32_bf16 v[30:33], v[146:149], v[206:209], v[30:33]
	v_mfma_f32_16x16x32_bf16 v[22:25], v[138:141], v[214:217], v[22:25]
	v_mfma_f32_16x16x32_bf16 v[14:17], v[146:149], v[214:217], v[14:17]
	s_setprio 0
	s_setprio 1
	v_mfma_f32_16x16x32_bf16 v[58:61], v[150:153], v[180:183], v[58:61]
	v_mfma_f32_16x16x32_bf16 v[50:53], v[166:169], v[180:183], v[50:53]
	v_mfma_f32_16x16x32_bf16 v[42:45], v[150:153], v[188:191], v[42:45]
	v_mfma_f32_16x16x32_bf16 v[34:37], v[166:169], v[188:191], v[34:37]
	v_mfma_f32_16x16x32_bf16 v[26:29], v[150:153], v[196:199], v[26:29]
	v_mfma_f32_16x16x32_bf16 v[18:21], v[166:169], v[196:199], v[18:21]
	v_mfma_f32_16x16x32_bf16 v[10:13], v[150:153], v[210:213], v[10:13]
	v_mfma_f32_16x16x32_bf16 v[6:9], v[166:169], v[210:213], v[6:9]
	v_mfma_f32_16x16x32_bf16 v[58:61], v[162:165], v[184:187], v[58:61]
	v_mfma_f32_16x16x32_bf16 v[50:53], v[176:179], v[184:187], v[50:53]
	v_mfma_f32_16x16x32_bf16 v[42:45], v[162:165], v[192:195], v[42:45]
	v_mfma_f32_16x16x32_bf16 v[34:37], v[176:179], v[192:195], v[34:37]
	v_mfma_f32_16x16x32_bf16 v[26:29], v[162:165], v[206:209], v[26:29]
	v_mfma_f32_16x16x32_bf16 v[18:21], v[176:179], v[206:209], v[18:21]
	s_setprio 2
	s_barrier
	v_mfma_f32_16x16x32_bf16 v[10:13], v[162:165], v[214:217], v[10:13]
	v_mfma_f32_16x16x32_bf16 v[6:9], v[176:179], v[214:217], v[6:9]
	s_setprio 0
	s_add_i32 s52, s52, 2
	s_add_u32 s50, s50, 0x100
	s_addc_u32 s51, s51, 0
	s_cmpk_gt_u32 s52, 0x53
	s_mov_b64 s[8:9], s[10:11]
	s_cbranch_scc0 .LBB0_2160
	s_and_b64 vcc, exec, s[4:5]
	s_cbranch_vccz .LBB0_2163
	s_barrier

.LBB0_2197:
	v_cmp_lt_u32_e32 vcc, 1, v0
	s_and_saveexec_b64 s[4:5], vcc
	s_cbranch_execnz .LBB0_2198
	s_getpc_b64 s[98:99]

.LBB0_2198:
	buffer_wbl2 sc1
	s_waitcnt vmcnt(0)
	v_mov_b32_e32 v2, s2
	v_add_co_u32_e32 v2, vcc, 0x3000, v2
	v_mov_b32_e32 v3, s3
	s_nop 0
	v_addc_co_u32_e32 v3, vcc, 0, v3, vcc
	v_mov_b32_e32 v5, 1
	flat_atomic_add v2, v[2:3], v5 offset:1024 sc0
	v_cvt_f32_u32_e32 v3, v0
	v_sub_u32_e32 v5, 0, v0
	s_mov_b64 s[10:11], -1
	v_rcp_iflag_f32_e32 v3, v3
	s_nop 0
	v_mul_f32_e32 v3, 0x4f7ffffe, v3
	v_cvt_u32_f32_e32 v3, v3
	v_mul_lo_u32 v5, v5, v3
	v_mul_hi_u32 v5, v3, v5
	v_add_u32_e32 v3, v3, v5
	s_waitcnt vmcnt(0) lgkmcnt(0)
	v_mul_hi_u32 v3, v2, v3
	v_mul_lo_u32 v5, v3, v0
	v_sub_u32_e32 v5, v2, v5
	v_cmp_ge_u32_e32 vcc, v5, v0
	v_add_u32_e32 v6, 1, v3
	s_nop 0
	v_cndmask_b32_e32 v3, v3, v6, vcc
	v_sub_u32_e32 v6, v5, v0
	v_cndmask_b32_e32 v5, v5, v6, vcc
	v_cmp_ge_u32_e32 vcc, v5, v0
	v_add_u32_e32 v5, 1, v3
	v_add_u32_e32 v6, 1, v2
	v_cndmask_b32_e32 v5, v3, v5, vcc
	v_mad_u64_u32 v[2:3], s[6:7], v0, v5, v[0:1]
	s_add_u32 s6, s2, 0x3500
	s_addc_u32 s7, s3, 0
	v_cmp_ne_u32_e32 vcc, v6, v2
	v_mov_b64_e32 v[2:3], s[6:7]
	s_and_saveexec_b64 s[8:9], vcc
	s_cbranch_execz .LBB0_2210
	v_mov_b64_e32 v[2:3], s[6:7]
	flat_load_dword v0, v[2:3] sc1
	s_mov_b64 s[14:15], 0
	s_waitcnt vmcnt(0) lgkmcnt(0)
	v_cmp_eq_u32_e32 vcc, v0, v5
	s_and_saveexec_b64 s[12:13], vcc
	s_cbranch_execz .LBB0_2209
	s_add_u32 s10, s2, 0x200
	s_addc_u32 s11, s3, 0
	s_mov_b32 s26, 1
	s_mov_b64 s[2:3], 0
	s_branch .LBB0_2202
